# baseline (speedup 1.0000x reference)
.Lmy_noperm_in:
	v_mfma_f32_16x16x32_f16 v[210:213], v[70:73], v[150:153], v[98:101]
	v_mfma_f32_16x16x32_f16 v[214:217], v[74:77], v[150:153], v[102:105]
	v_mfma_f32_16x16x32_f16 v[210:213], v[66:69], v[154:157], v[210:213]
	v_mfma_f32_16x16x32_f16 v[214:217], v[78:81], v[154:157], v[214:217]
	s_add_u32 s48, s20, 0x600000
	s_addc_u32 s49, s21, 0
	s_sub_u32 s50, s22, 0x600000
	s_mov_b32 s51, s23
	s_add_u32 s68, s16, 0xc000
	s_addc_u32 s69, s17, 0
	s_sub_u32 s70, s18, 0xc000
	s_mov_b32 s71, s19
	s_add_u32 s52, s20, 0x700000
	s_addc_u32 s53, s21, 0
	s_sub_u32 s54, s22, 0x700000
	s_mov_b32 s55, s23
	s_add_u32 s72, s16, 0x10000
	s_addc_u32 s73, s17, 0
	s_sub_u32 s74, s18, 0x10000
	s_mov_b32 s75, s19
	s_add_u32 s56, s20, 0x800000
	s_addc_u32 s57, s21, 0
	s_sub_u32 s58, s22, 0x800000
	s_mov_b32 s59, s23
	s_add_u32 s76, s16, 0x14000
	s_addc_u32 s77, s17, 0
	s_sub_u32 s78, s18, 0x14000
	s_mov_b32 s79, s19
	s_add_u32 s60, s20, 0x900000
	s_addc_u32 s61, s21, 0
	s_sub_u32 s62, s22, 0x900000
	s_mov_b32 s63, s23
	s_add_u32 s80, s16, 0x18000
	s_addc_u32 s81, s17, 0
	s_sub_u32 s82, s18, 0x18000
	s_mov_b32 s83, s19
	v_mfma_f32_16x16x32_f16 v[218:221], v[82:85], v[150:153], v[106:109]
	v_mfma_f32_16x16x32_f16 v[222:225], v[90:93], v[150:153], v[110:113]
	v_mfma_f32_16x16x32_f16 v[218:221], v[86:89], v[154:157], v[218:221]
	v_mfma_f32_16x16x32_f16 v[222:225], v[94:97], v[154:157], v[222:225]
	s_waitcnt lgkmcnt(2)
	s_waitcnt lgkmcnt(0)
	s_waitcnt vmcnt(9)
	v_cvt_pk_f16_f32 v251, v196, v197
	ds_write_b32 v1, v251 offset:4096
	ds_read_b128 v[150:153], v186 offset:2048
	ds_read_b128 v[154:157], v186 offset:3072
	s_add_i32 s45, s45, 0x100000
	s_add_i32 s46, s46, 0x4000
	s_movk_i32 s47, 0x0
	s_add_i32 s43, s40, -12
	s_lshl_b32 s43, s43, 12
	s_cmp_lt_u32 s40, 14
	s_cselect_b32 s43, s47, s43
	v_exp_f32_e32 v226, v210
	v_exp_f32_e32 v227, v211
	v_min_f32_e32 v228, s42, v212
	v_exp_f32_e32 v229, v213
	v_exp_f32_e32 v228, v228
	v_add_f32_e32 v227, 1.0, v227
	v_fma_f32 v230, v228, s41, s41
	v_rcp_f32_e32 v227, v227
	v_fma_f32 v230, v226, v230, v230
	v_rcp_f32_e32 v230, v230
	s_nop 0
	v_fma_f32 v226, -v228, v230, v230
	v_fma_f32 v200, v200, v227, v226
	v_exp_f32_e32 v226, v200
	s_nop 0
	v_add_f32_e32 v227, 1.0, v226
	v_fma_f32 v227, v229, v227, v227
	v_rcp_f32_e32 v227, v227
	s_nop 0
	v_fma_mixlo_f16 v246, -v226, v227, v227
	v_exp_f32_e32 v231, v214
	v_exp_f32_e32 v232, v215
	v_min_f32_e32 v233, s42, v216
	v_exp_f32_e32 v234, v217
	v_exp_f32_e32 v233, v233
	v_exp_f32_e32 v236, v218
	v_add_f32_e32 v232, 1.0, v232
	v_fma_f32 v235, v233, s41, s41
	v_exp_f32_e32 v227, v219
	v_rcp_f32_e32 v232, v232
	v_fma_f32 v235, v231, v235, v235
	v_min_f32_e32 v228, s42, v220
	v_rcp_f32_e32 v235, v235
	s_nop 0
	v_fma_f32 v231, -v233, v235, v235
	v_exp_f32_e32 v229, v221
	v_fma_f32 v201, v201, v232, v231
	v_exp_f32_e32 v231, v201
	v_exp_f32_e32 v228, v228
	v_add_f32_e32 v232, 1.0, v231
	v_fma_f32 v232, v234, v232, v232
	v_add_f32_e32 v227, 1.0, v227
	v_rcp_f32_e32 v232, v232
	s_nop 0
	v_fma_mixhi_f16 v246, -v231, v232, v232
	v_fma_f32 v230, v228, s41, s41
	v_exp_f32_e32 v231, v222
	v_exp_f32_e32 v232, v223
	v_rcp_f32_e32 v227, v227
	v_min_f32_e32 v233, s42, v224
	buffer_load_dwordx4 v[138:141], v189, s[16:19], s46 offen
	buffer_load_dwordx4 v[142:145], v208, s[16:19], s46 offen
	v_exp_f32_e32 v234, v225
	v_fma_f32 v230, v236, v230, v230
	v_exp_f32_e32 v233, v233
	s_waitcnt lgkmcnt(0)
	v_mfma_f32_16x16x32_f16 v[210:213], v[70:73], v[150:153], v[98:101]
	v_add_f32_e32 v232, 1.0, v232
	v_rcp_f32_e32 v230, v230
	v_fma_f32 v235, v233, s41, s41
	v_mfma_f32_16x16x32_f16 v[214:217], v[74:77], v[150:153], v[102:105]
	v_rcp_f32_e32 v232, v232
	v_fma_f32 v236, -v228, v230, v230
	v_fma_f32 v235, v231, v235, v235
	v_rcp_f32_e32 v235, v235
	v_fma_f32 v198, v198, v227, v236
	v_fma_f32 v231, -v233, v235, v235
	v_fma_f32 v199, v199, v232, v231
	v_exp_f32_e32 v236, v198
	v_exp_f32_e32 v231, v199
	s_nop 0
	v_add_f32_e32 v232, 1.0, v231
	v_add_f32_e32 v227, 1.0, v236
	v_fma_f32 v232, v234, v232, v232
	v_rcp_f32_e32 v232, v232
	v_fma_f32 v227, v229, v227, v227
	v_fma_mixhi_f16 v247, -v231, v232, v232
	v_rcp_f32_e32 v227, v227
	s_nop 0
	v_fma_mixlo_f16 v247, -v236, v227, v227
	ds_write_b64 v206, v[246:247] offset:8192
	v_mfma_f32_16x16x32_f16 v[210:213], v[66:69], v[154:157], v[210:213]
	v_mfma_f32_16x16x32_f16 v[214:217], v[78:81], v[154:157], v[214:217]
	v_mov_b32_e32 v174, v246
	v_mov_b32_e32 v175, v247
	buffer_load_dwordx2 v[196:197], v209, s[20:23], s45 offen
	s_add_i32 s40, s40, 1
	s_add_i32 s44, s44, 0x1000
	s_waitcnt lgkmcnt(0)
	s_barrier
	ds_read_b128 v[158:161], v252 offset:0
	ds_read_b128 v[162:165], v252 offset:1024
	ds_read_b128 v[166:169], v253 offset:2048
	ds_read_b128 v[170:173], v253 offset:3072
	v_mfma_f32_16x16x32_f16 v[218:221], v[82:85], v[150:153], v[106:109]
	v_mfma_f32_16x16x32_f16 v[222:225], v[90:93], v[150:153], v[110:113]
	v_mfma_f32_16x16x32_f16 v[218:221], v[86:89], v[154:157], v[218:221]
	v_mfma_f32_16x16x32_f16 v[222:225], v[94:97], v[154:157], v[222:225]
	s_waitcnt lgkmcnt(2)
	v_mfma_f32_16x16x32_f16 v[210:213], v[54:57], v[158:161], v[210:213]
	v_mfma_f32_16x16x32_f16 v[210:213], v[58:61], v[162:165], v[210:213]
	s_waitcnt lgkmcnt(0)
	v_mfma_f32_16x16x32_f16 v[210:213], v[62:65], v[166:169], v[210:213]
	v_mfma_f32_16x16x32_f16 v[210:213], v[50:53], v[170:173], v[210:213]
	s_waitcnt vmcnt(9)
	v_cvt_pk_f16_f32 v251, v194, v195
	ds_write_b32 v1, v251 offset:6144
	ds_read_b128 v[150:153], v186 offset:4096
	ds_read_b128 v[154:157], v186 offset:5120
	s_add_i32 s45, s45, 0x100000
	s_add_i32 s46, s46, 0x4000
	s_movk_i32 s47, 0x1000
	s_add_i32 s43, s40, -12
	s_lshl_b32 s43, s43, 12
	s_cmp_lt_u32 s40, 14
	s_cselect_b32 s43, s47, s43
	v_exp_f32_e32 v226, v210
	v_exp_f32_e32 v227, v211
	v_mfma_f32_16x16x32_f16 v[214:217], v[34:37], v[158:161], v[214:217]
	v_min_f32_e32 v228, s42, v212
	v_exp_f32_e32 v229, v213
	v_mfma_f32_16x16x32_f16 v[214:217], v[38:41], v[162:165], v[214:217]
	v_exp_f32_e32 v228, v228
	v_add_f32_e32 v227, 1.0, v227
	v_mfma_f32_16x16x32_f16 v[214:217], v[42:45], v[166:169], v[214:217]
	v_fma_f32 v230, v228, s41, s41
	v_rcp_f32_e32 v227, v227
	v_mfma_f32_16x16x32_f16 v[214:217], v[46:49], v[170:173], v[214:217]
	v_fma_f32 v230, v226, v230, v230
	v_rcp_f32_e32 v230, v230
	v_mfma_f32_16x16x32_f16 v[218:221], v[18:21], v[158:161], v[218:221]
	v_fma_f32 v226, -v228, v230, v230
	v_fma_f32 v200, v200, v227, v226
	v_mfma_f32_16x16x32_f16 v[218:221], v[14:17], v[162:165], v[218:221]
	v_exp_f32_e32 v226, v200
	s_nop 0
	v_add_f32_e32 v227, 1.0, v226
	v_mfma_f32_16x16x32_f16 v[218:221], v[10:13], v[166:169], v[218:221]
	v_fma_f32 v227, v229, v227, v227
	v_rcp_f32_e32 v227, v227
	v_mfma_f32_16x16x32_f16 v[218:221], v[26:29], v[170:173], v[218:221]
	v_fma_mixlo_f16 v246, -v226, v227, v227
	v_exp_f32_e32 v231, v214
	v_mfma_f32_16x16x32_f16 v[222:225], v[2:5], v[158:161], v[222:225]
	v_exp_f32_e32 v232, v215
	v_min_f32_e32 v233, s42, v216
	v_mfma_f32_16x16x32_f16 v[222:225], v[6:9], v[162:165], v[222:225]
	v_exp_f32_e32 v234, v217
	v_exp_f32_e32 v233, v233
	v_mfma_f32_16x16x32_f16 v[222:225], v[22:25], v[166:169], v[222:225]
	v_exp_f32_e32 v236, v218
	v_add_f32_e32 v232, 1.0, v232
	v_mfma_f32_16x16x32_f16 v[222:225], v[30:33], v[170:173], v[222:225]
	v_fma_f32 v235, v233, s41, s41
	v_exp_f32_e32 v227, v219
	v_rcp_f32_e32 v232, v232
	v_fma_f32 v235, v231, v235, v235
	v_min_f32_e32 v228, s42, v220
	v_rcp_f32_e32 v235, v235
	s_nop 0
	v_fma_f32 v231, -v233, v235, v235
	v_exp_f32_e32 v229, v221
	v_fma_f32 v201, v201, v232, v231
	v_exp_f32_e32 v231, v201
	v_exp_f32_e32 v228, v228
	v_add_f32_e32 v232, 1.0, v231
	v_fma_f32 v232, v234, v232, v232
	v_add_f32_e32 v227, 1.0, v227
	v_rcp_f32_e32 v232, v232
	v_mfma_f32_16x16x32_f16 v[146:149], v[130:133], v[158:161], v[146:149]
	v_fma_mixhi_f16 v246, -v231, v232, v232
	v_fma_f32 v230, v228, s41, s41
	v_exp_f32_e32 v231, v222
	v_mfma_f32_16x16x32_f16 v[146:149], v[134:137], v[162:165], v[146:149]
	v_exp_f32_e32 v232, v223
	v_rcp_f32_e32 v227, v227
	v_min_f32_e32 v233, s42, v224
	buffer_load_dwordx4 v[130:133], v189, s[16:19], s46 offen
	buffer_load_dwordx4 v[134:137], v208, s[16:19], s46 offen
	v_exp_f32_e32 v234, v225
	v_fma_f32 v230, v236, v230, v230
	v_exp_f32_e32 v233, v233
	s_waitcnt lgkmcnt(0)
	v_mfma_f32_16x16x32_f16 v[210:213], v[70:73], v[150:153], v[98:101]
	v_add_f32_e32 v232, 1.0, v232
	v_rcp_f32_e32 v230, v230
	v_fma_f32 v235, v233, s41, s41
	v_mfma_f32_16x16x32_f16 v[214:217], v[74:77], v[150:153], v[102:105]
	v_rcp_f32_e32 v232, v232
	v_fma_f32 v236, -v228, v230, v230
	v_fma_f32 v235, v231, v235, v235
	v_rcp_f32_e32 v235, v235
	v_fma_f32 v198, v198, v227, v236
	v_fma_f32 v231, -v233, v235, v235
	v_fma_f32 v199, v199, v232, v231
	v_exp_f32_e32 v236, v198
	v_exp_f32_e32 v231, v199
	s_nop 0
	v_add_f32_e32 v232, 1.0, v231
	v_add_f32_e32 v227, 1.0, v236
	v_fma_f32 v232, v234, v232, v232
	v_rcp_f32_e32 v232, v232
	v_fma_f32 v227, v229, v227, v227
	v_fma_mixhi_f16 v247, -v231, v232, v232
	v_rcp_f32_e32 v227, v227
	s_nop 0
	v_fma_mixlo_f16 v247, -v236, v227, v227
	ds_write_b64 v206, v[246:247] offset:12288
	v_mfma_f32_16x16x32_f16 v[210:213], v[66:69], v[154:157], v[210:213]
	v_mfma_f32_16x16x32_f16 v[214:217], v[78:81], v[154:157], v[214:217]
	v_mov_b32_e32 v176, v246
	v_mov_b32_e32 v177, v247
	buffer_load_dwordx2 v[194:195], v209, s[20:23], s45 offen
	s_add_i32 s40, s40, 1
	s_add_i32 s44, s44, 0x1000
	s_waitcnt lgkmcnt(0)
	s_barrier
	ds_read_b128 v[158:161], v252 offset:4096
	ds_read_b128 v[162:165], v252 offset:5120
	ds_read_b128 v[166:169], v253 offset:6144
	ds_read_b128 v[170:173], v253 offset:7168
	v_mfma_f32_16x16x32_f16 v[218:221], v[82:85], v[150:153], v[106:109]
	v_mfma_f32_16x16x32_f16 v[222:225], v[90:93], v[150:153], v[110:113]
	v_mfma_f32_16x16x32_f16 v[218:221], v[86:89], v[154:157], v[218:221]
	v_mfma_f32_16x16x32_f16 v[222:225], v[94:97], v[154:157], v[222:225]
	s_waitcnt lgkmcnt(2)
	v_mfma_f32_16x16x32_f16 v[210:213], v[54:57], v[158:161], v[210:213]
	v_mfma_f32_16x16x32_f16 v[210:213], v[58:61], v[162:165], v[210:213]
	s_waitcnt lgkmcnt(0)
	v_mfma_f32_16x16x32_f16 v[210:213], v[62:65], v[166:169], v[210:213]
	v_mfma_f32_16x16x32_f16 v[210:213], v[50:53], v[170:173], v[210:213]
	s_waitcnt vmcnt(9)
	v_cvt_pk_f16_f32 v251, v192, v193
	ds_write_b32 v1, v251 offset:0
	ds_read_b128 v[150:153], v186 offset:6144
	ds_read_b128 v[154:157], v186 offset:7168
	s_add_i32 s45, s45, 0x100000
	s_add_i32 s46, s46, 0x4000
	s_movk_i32 s47, 0x0
	s_add_i32 s43, s40, -12
	s_lshl_b32 s43, s43, 12
	s_cmp_lt_u32 s40, 14
	s_cselect_b32 s43, s47, s43
	v_exp_f32_e32 v226, v210
	v_exp_f32_e32 v227, v211
	v_mfma_f32_16x16x32_f16 v[214:217], v[34:37], v[158:161], v[214:217]
	v_min_f32_e32 v228, s42, v212
	v_exp_f32_e32 v229, v213
	v_mfma_f32_16x16x32_f16 v[214:217], v[38:41], v[162:165], v[214:217]
	v_exp_f32_e32 v228, v228
	v_add_f32_e32 v227, 1.0, v227
	v_mfma_f32_16x16x32_f16 v[214:217], v[42:45], v[166:169], v[214:217]
	v_fma_f32 v230, v228, s41, s41
	v_rcp_f32_e32 v227, v227
	v_mfma_f32_16x16x32_f16 v[214:217], v[46:49], v[170:173], v[214:217]
	v_fma_f32 v230, v226, v230, v230
	v_rcp_f32_e32 v230, v230
	v_mfma_f32_16x16x32_f16 v[218:221], v[18:21], v[158:161], v[218:221]
	v_fma_f32 v226, -v228, v230, v230
	v_fma_f32 v200, v200, v227, v226
	v_mfma_f32_16x16x32_f16 v[218:221], v[14:17], v[162:165], v[218:221]
	v_exp_f32_e32 v226, v200
	s_nop 0
	v_add_f32_e32 v227, 1.0, v226
	v_mfma_f32_16x16x32_f16 v[218:221], v[10:13], v[166:169], v[218:221]
	v_fma_f32 v227, v229, v227, v227
	v_rcp_f32_e32 v227, v227
	v_mfma_f32_16x16x32_f16 v[218:221], v[26:29], v[170:173], v[218:221]
	v_fma_mixlo_f16 v246, -v226, v227, v227
	v_exp_f32_e32 v231, v214
	v_mfma_f32_16x16x32_f16 v[222:225], v[2:5], v[158:161], v[222:225]
	v_exp_f32_e32 v232, v215
	v_min_f32_e32 v233, s42, v216
	v_mfma_f32_16x16x32_f16 v[222:225], v[6:9], v[162:165], v[222:225]
	v_exp_f32_e32 v234, v217
	v_exp_f32_e32 v233, v233
	v_mfma_f32_16x16x32_f16 v[222:225], v[22:25], v[166:169], v[222:225]
	v_exp_f32_e32 v236, v218
	v_add_f32_e32 v232, 1.0, v232
	v_mfma_f32_16x16x32_f16 v[222:225], v[30:33], v[170:173], v[222:225]
	v_fma_f32 v235, v233, s41, s41
	v_exp_f32_e32 v227, v219
	v_rcp_f32_e32 v232, v232
	v_fma_f32 v235, v231, v235, v235
	v_min_f32_e32 v228, s42, v220
	v_rcp_f32_e32 v235, v235
	s_nop 0
	v_fma_f32 v231, -v233, v235, v235
	v_exp_f32_e32 v229, v221
	v_fma_f32 v201, v201, v232, v231
	v_exp_f32_e32 v231, v201
	v_exp_f32_e32 v228, v228
	v_add_f32_e32 v232, 1.0, v231
	v_fma_f32 v232, v234, v232, v232
	v_add_f32_e32 v227, 1.0, v227
	v_rcp_f32_e32 v232, v232
	v_mfma_f32_16x16x32_f16 v[146:149], v[122:125], v[158:161], v[146:149]
	v_fma_mixhi_f16 v246, -v231, v232, v232
	v_fma_f32 v230, v228, s41, s41
	v_exp_f32_e32 v231, v222
	v_mfma_f32_16x16x32_f16 v[146:149], v[126:129], v[162:165], v[146:149]
	v_exp_f32_e32 v232, v223
	v_rcp_f32_e32 v227, v227
	v_min_f32_e32 v233, s42, v224
	buffer_load_dwordx4 v[122:125], v189, s[16:19], s46 offen
	buffer_load_dwordx4 v[126:129], v208, s[16:19], s46 offen
	v_exp_f32_e32 v234, v225
	v_fma_f32 v230, v236, v230, v230
	v_exp_f32_e32 v233, v233
	s_waitcnt lgkmcnt(0)
	v_mfma_f32_16x16x32_f16 v[210:213], v[70:73], v[150:153], v[98:101]
	v_add_f32_e32 v232, 1.0, v232
	v_rcp_f32_e32 v230, v230
	v_fma_f32 v235, v233, s41, s41
	v_mfma_f32_16x16x32_f16 v[214:217], v[74:77], v[150:153], v[102:105]
	v_rcp_f32_e32 v232, v232
	v_fma_f32 v236, -v228, v230, v230
	v_fma_f32 v235, v231, v235, v235
	v_rcp_f32_e32 v235, v235
	v_fma_f32 v198, v198, v227, v236
	v_fma_f32 v231, -v233, v235, v235
	v_fma_f32 v199, v199, v232, v231
	v_exp_f32_e32 v236, v198
	v_exp_f32_e32 v231, v199
	s_nop 0
	v_add_f32_e32 v232, 1.0, v231
	v_add_f32_e32 v227, 1.0, v236
	v_fma_f32 v232, v234, v232, v232
	v_rcp_f32_e32 v232, v232
	v_fma_f32 v227, v229, v227, v227
	v_fma_mixhi_f16 v247, -v231, v232, v232
	v_rcp_f32_e32 v227, v227
	s_nop 0
	v_fma_mixlo_f16 v247, -v236, v227, v227
	ds_write_b64 v206, v[246:247] offset:8192
	v_mfma_f32_16x16x32_f16 v[210:213], v[66:69], v[154:157], v[210:213]
	v_mfma_f32_16x16x32_f16 v[214:217], v[78:81], v[154:157], v[214:217]
	v_mov_b32_e32 v178, v246
	v_mov_b32_e32 v179, v247
	buffer_load_dwordx2 v[192:193], v209, s[20:23], s45 offen
	s_add_i32 s40, s40, 1
	s_add_i32 s44, s44, 0x1000
	s_waitcnt lgkmcnt(0)
	s_barrier
	ds_read_b128 v[158:161], v252 offset:0
	ds_read_b128 v[162:165], v252 offset:1024
	ds_read_b128 v[166:169], v253 offset:2048
	ds_read_b128 v[170:173], v253 offset:3072
	v_mfma_f32_16x16x32_f16 v[218:221], v[82:85], v[150:153], v[106:109]
	v_mfma_f32_16x16x32_f16 v[222:225], v[90:93], v[150:153], v[110:113]
	v_mfma_f32_16x16x32_f16 v[218:221], v[86:89], v[154:157], v[218:221]
	v_mfma_f32_16x16x32_f16 v[222:225], v[94:97], v[154:157], v[222:225]
	s_waitcnt lgkmcnt(2)
	v_mfma_f32_16x16x32_f16 v[210:213], v[54:57], v[158:161], v[210:213]
	v_mfma_f32_16x16x32_f16 v[210:213], v[58:61], v[162:165], v[210:213]
	s_waitcnt lgkmcnt(0)
	v_mfma_f32_16x16x32_f16 v[210:213], v[62:65], v[166:169], v[210:213]
	v_mfma_f32_16x16x32_f16 v[210:213], v[50:53], v[170:173], v[210:213]
	s_waitcnt vmcnt(9)
	v_cvt_pk_f16_f32 v251, v190, v191
	ds_write_b32 v1, v251 offset:2048
	ds_read_b128 v[150:153], v186 offset:0
	ds_read_b128 v[154:157], v186 offset:1024
	s_add_i32 s45, s45, 0x100000
	s_add_i32 s46, s46, 0x4000
	s_movk_i32 s47, 0x1000
	s_add_i32 s43, s40, -12
	s_lshl_b32 s43, s43, 12
	s_cmp_lt_u32 s40, 14
	s_cselect_b32 s43, s47, s43
	v_exp_f32_e32 v226, v210
	v_exp_f32_e32 v227, v211
	v_mfma_f32_16x16x32_f16 v[214:217], v[34:37], v[158:161], v[214:217]
	v_min_f32_e32 v228, s42, v212
	v_exp_f32_e32 v229, v213
	v_mfma_f32_16x16x32_f16 v[214:217], v[38:41], v[162:165], v[214:217]
	v_exp_f32_e32 v228, v228
	v_add_f32_e32 v227, 1.0, v227
	v_mfma_f32_16x16x32_f16 v[214:217], v[42:45], v[166:169], v[214:217]
	v_fma_f32 v230, v228, s41, s41
	v_rcp_f32_e32 v227, v227
	v_mfma_f32_16x16x32_f16 v[214:217], v[46:49], v[170:173], v[214:217]
	v_fma_f32 v230, v226, v230, v230
	v_rcp_f32_e32 v230, v230
	v_mfma_f32_16x16x32_f16 v[218:221], v[18:21], v[158:161], v[218:221]
	v_fma_f32 v226, -v228, v230, v230
	v_fma_f32 v200, v200, v227, v226
	v_mfma_f32_16x16x32_f16 v[218:221], v[14:17], v[162:165], v[218:221]
	v_exp_f32_e32 v226, v200
	s_nop 0
	v_add_f32_e32 v227, 1.0, v226
	v_mfma_f32_16x16x32_f16 v[218:221], v[10:13], v[166:169], v[218:221]
	v_fma_f32 v227, v229, v227, v227
	v_rcp_f32_e32 v227, v227
	v_mfma_f32_16x16x32_f16 v[218:221], v[26:29], v[170:173], v[218:221]
	v_fma_mixlo_f16 v246, -v226, v227, v227
	v_exp_f32_e32 v231, v214
	v_mfma_f32_16x16x32_f16 v[222:225], v[2:5], v[158:161], v[222:225]
	v_exp_f32_e32 v232, v215
	v_min_f32_e32 v233, s42, v216
	v_mfma_f32_16x16x32_f16 v[222:225], v[6:9], v[162:165], v[222:225]
	v_exp_f32_e32 v234, v217
	v_exp_f32_e32 v233, v233
	v_mfma_f32_16x16x32_f16 v[222:225], v[22:25], v[166:169], v[222:225]
	v_exp_f32_e32 v236, v218
	v_add_f32_e32 v232, 1.0, v232
	v_mfma_f32_16x16x32_f16 v[222:225], v[30:33], v[170:173], v[222:225]
	v_fma_f32 v235, v233, s41, s41
	v_exp_f32_e32 v227, v219
	v_rcp_f32_e32 v232, v232
	v_fma_f32 v235, v231, v235, v235
	v_min_f32_e32 v228, s42, v220
	v_rcp_f32_e32 v235, v235
	s_nop 0
	v_fma_f32 v231, -v233, v235, v235
	v_exp_f32_e32 v229, v221
	v_fma_f32 v201, v201, v232, v231
	v_exp_f32_e32 v231, v201
	v_exp_f32_e32 v228, v228
	v_add_f32_e32 v232, 1.0, v231
	v_fma_f32 v232, v234, v232, v232
	v_add_f32_e32 v227, 1.0, v227
	v_rcp_f32_e32 v232, v232
	v_mfma_f32_16x16x32_f16 v[146:149], v[114:117], v[158:161], v[146:149]
	v_fma_mixhi_f16 v246, -v231, v232, v232
	v_fma_f32 v230, v228, s41, s41
	v_exp_f32_e32 v231, v222
	v_mfma_f32_16x16x32_f16 v[146:149], v[118:121], v[162:165], v[146:149]
	v_exp_f32_e32 v232, v223
	v_rcp_f32_e32 v227, v227
	v_min_f32_e32 v233, s42, v224
	buffer_load_dwordx4 v[114:117], v189, s[16:19], s46 offen
	buffer_load_dwordx4 v[118:121], v208, s[16:19], s46 offen
	v_exp_f32_e32 v234, v225
	v_fma_f32 v230, v236, v230, v230
	v_exp_f32_e32 v233, v233
	s_waitcnt lgkmcnt(0)
	v_mfma_f32_16x16x32_f16 v[210:213], v[70:73], v[150:153], v[98:101]
	v_add_f32_e32 v232, 1.0, v232
	v_rcp_f32_e32 v230, v230
	v_fma_f32 v235, v233, s41, s41
	v_mfma_f32_16x16x32_f16 v[214:217], v[74:77], v[150:153], v[102:105]
	v_rcp_f32_e32 v232, v232
	v_fma_f32 v236, -v228, v230, v230
	v_fma_f32 v235, v231, v235, v235
	v_rcp_f32_e32 v235, v235
	v_fma_f32 v198, v198, v227, v236
	v_fma_f32 v231, -v233, v235, v235
	v_fma_f32 v199, v199, v232, v231
	v_exp_f32_e32 v236, v198
	v_exp_f32_e32 v231, v199
	s_nop 0
	v_add_f32_e32 v232, 1.0, v231
	v_add_f32_e32 v227, 1.0, v236
	v_fma_f32 v232, v234, v232, v232
	v_rcp_f32_e32 v232, v232
	v_fma_f32 v227, v229, v227, v227
	v_fma_mixhi_f16 v247, -v231, v232, v232
	v_rcp_f32_e32 v227, v227
	s_nop 0
	v_fma_mixlo_f16 v247, -v236, v227, v227
	ds_write_b64 v206, v[246:247] offset:12288
	v_mfma_f32_16x16x32_f16 v[210:213], v[66:69], v[154:157], v[210:213]
	v_mfma_f32_16x16x32_f16 v[214:217], v[78:81], v[154:157], v[214:217]
	v_mov_b32_e32 v180, v246
	v_mov_b32_e32 v181, v247
	buffer_load_dwordx2 v[190:191], v209, s[20:23], s45 offen
	s_add_i32 s40, s40, 1
	s_add_i32 s44, s44, 0x1000
	s_waitcnt lgkmcnt(0)
	s_barrier
	ds_read_b128 v[158:161], v252 offset:4096
	ds_read_b128 v[162:165], v252 offset:5120
	ds_read_b128 v[166:169], v253 offset:6144
	ds_read_b128 v[170:173], v253 offset:7168
	v_mfma_f32_16x16x32_f16 v[218:221], v[82:85], v[150:153], v[106:109]
	v_mfma_f32_16x16x32_f16 v[222:225], v[90:93], v[150:153], v[110:113]
	v_mfma_f32_16x16x32_f16 v[218:221], v[86:89], v[154:157], v[218:221]
	v_mfma_f32_16x16x32_f16 v[222:225], v[94:97], v[154:157], v[222:225]
	s_waitcnt lgkmcnt(2)
	v_mfma_f32_16x16x32_f16 v[210:213], v[54:57], v[158:161], v[210:213]
	v_mfma_f32_16x16x32_f16 v[210:213], v[58:61], v[162:165], v[210:213]
	s_waitcnt lgkmcnt(0)
	v_mfma_f32_16x16x32_f16 v[210:213], v[62:65], v[166:169], v[210:213]
	v_mfma_f32_16x16x32_f16 v[210:213], v[50:53], v[170:173], v[210:213]
	s_waitcnt vmcnt(9)
	v_cvt_pk_f16_f32 v251, v196, v197
	ds_write_b32 v1, v251 offset:4096
	ds_read_b128 v[150:153], v186 offset:2048
	ds_read_b128 v[154:157], v186 offset:3072
	s_add_i32 s45, s45, 0x100000
	s_add_i32 s46, s46, 0x4000
	s_movk_i32 s47, 0x0
	s_add_i32 s43, s40, -12
	s_lshl_b32 s43, s43, 12
	s_cmp_lt_u32 s40, 14
	s_cselect_b32 s43, s47, s43
	v_exp_f32_e32 v226, v210
	v_exp_f32_e32 v227, v211
	v_mfma_f32_16x16x32_f16 v[214:217], v[34:37], v[158:161], v[214:217]
	v_min_f32_e32 v228, s42, v212
	v_exp_f32_e32 v229, v213
	v_mfma_f32_16x16x32_f16 v[214:217], v[38:41], v[162:165], v[214:217]
	v_exp_f32_e32 v228, v228
	v_add_f32_e32 v227, 1.0, v227
	v_mfma_f32_16x16x32_f16 v[214:217], v[42:45], v[166:169], v[214:217]
	v_fma_f32 v230, v228, s41, s41
	v_rcp_f32_e32 v227, v227
	v_mfma_f32_16x16x32_f16 v[214:217], v[46:49], v[170:173], v[214:217]
	v_fma_f32 v230, v226, v230, v230
	v_rcp_f32_e32 v230, v230
	v_mfma_f32_16x16x32_f16 v[218:221], v[18:21], v[158:161], v[218:221]
	v_fma_f32 v226, -v228, v230, v230
	v_fma_f32 v200, v200, v227, v226
	v_mfma_f32_16x16x32_f16 v[218:221], v[14:17], v[162:165], v[218:221]
	v_exp_f32_e32 v226, v200
	s_nop 0
	v_add_f32_e32 v227, 1.0, v226
	v_mfma_f32_16x16x32_f16 v[218:221], v[10:13], v[166:169], v[218:221]
	v_fma_f32 v227, v229, v227, v227
	v_rcp_f32_e32 v227, v227
	v_mfma_f32_16x16x32_f16 v[218:221], v[26:29], v[170:173], v[218:221]
	v_fma_mixlo_f16 v246, -v226, v227, v227
	v_exp_f32_e32 v231, v214
	v_mfma_f32_16x16x32_f16 v[222:225], v[2:5], v[158:161], v[222:225]
	v_exp_f32_e32 v232, v215
	v_min_f32_e32 v233, s42, v216
	v_mfma_f32_16x16x32_f16 v[222:225], v[6:9], v[162:165], v[222:225]
	v_exp_f32_e32 v234, v217
	v_exp_f32_e32 v233, v233
	v_mfma_f32_16x16x32_f16 v[222:225], v[22:25], v[166:169], v[222:225]
	v_exp_f32_e32 v236, v218
	v_add_f32_e32 v232, 1.0, v232
	v_mfma_f32_16x16x32_f16 v[222:225], v[30:33], v[170:173], v[222:225]
	v_fma_f32 v235, v233, s41, s41
	v_exp_f32_e32 v227, v219
	v_rcp_f32_e32 v232, v232
	v_fma_f32 v235, v231, v235, v235
	v_min_f32_e32 v228, s42, v220
	v_rcp_f32_e32 v235, v235
	s_nop 0
	v_fma_f32 v231, -v233, v235, v235
	v_exp_f32_e32 v229, v221
	v_fma_f32 v201, v201, v232, v231
	v_exp_f32_e32 v231, v201
	v_exp_f32_e32 v228, v228
	v_add_f32_e32 v232, 1.0, v231
	v_fma_f32 v232, v234, v232, v232
	v_add_f32_e32 v227, 1.0, v227
	v_rcp_f32_e32 v232, v232
	v_mfma_f32_16x16x32_f16 v[146:149], v[138:141], v[158:161], v[146:149]
	v_fma_mixhi_f16 v246, -v231, v232, v232
	v_fma_f32 v230, v228, s41, s41
	v_exp_f32_e32 v231, v222
	v_mfma_f32_16x16x32_f16 v[146:149], v[142:145], v[162:165], v[146:149]
	v_exp_f32_e32 v232, v223
	v_rcp_f32_e32 v227, v227
	v_min_f32_e32 v233, s42, v224
	buffer_load_dwordx4 v[138:141], v189, s[16:19], s46 offen
	buffer_load_dwordx4 v[142:145], v208, s[16:19], s46 offen
	v_exp_f32_e32 v234, v225
	v_fma_f32 v230, v236, v230, v230
	v_exp_f32_e32 v233, v233
	s_waitcnt lgkmcnt(0)
	v_mfma_f32_16x16x32_f16 v[210:213], v[70:73], v[150:153], v[98:101]
	v_add_f32_e32 v232, 1.0, v232
	v_rcp_f32_e32 v230, v230
	v_fma_f32 v235, v233, s41, s41
	v_mfma_f32_16x16x32_f16 v[214:217], v[74:77], v[150:153], v[102:105]
	v_rcp_f32_e32 v232, v232
	v_fma_f32 v236, -v228, v230, v230
	v_fma_f32 v235, v231, v235, v235
	v_rcp_f32_e32 v235, v235
	v_fma_f32 v198, v198, v227, v236
	v_fma_f32 v231, -v233, v235, v235
	v_fma_f32 v199, v199, v232, v231
	v_exp_f32_e32 v236, v198
	v_exp_f32_e32 v231, v199
	s_nop 0
	v_add_f32_e32 v232, 1.0, v231
	v_add_f32_e32 v227, 1.0, v236
	v_fma_f32 v232, v234, v232, v232
	v_rcp_f32_e32 v232, v232
	v_fma_f32 v227, v229, v227, v227
	v_fma_mixhi_f16 v247, -v231, v232, v232
	v_rcp_f32_e32 v227, v227
	s_nop 0
	v_fma_mixlo_f16 v247, -v236, v227, v227
	ds_write_b64 v206, v[246:247] offset:8192
	v_mfma_f32_16x16x32_f16 v[210:213], v[66:69], v[154:157], v[210:213]
	v_mfma_f32_16x16x32_f16 v[214:217], v[78:81], v[154:157], v[214:217]
	v_mov_b32_e32 v182, v246
	v_mov_b32_e32 v183, v247
	buffer_load_dwordx2 v[196:197], v209, s[20:23], s45 offen
	s_add_i32 s40, s40, 1
	s_add_i32 s44, s44, 0x1000
	s_waitcnt lgkmcnt(0)
	s_barrier
	ds_read_b128 v[158:161], v252 offset:0
	ds_read_b128 v[162:165], v252 offset:1024
	ds_read_b128 v[166:169], v253 offset:2048
	ds_read_b128 v[170:173], v253 offset:3072
	v_mfma_f32_16x16x32_f16 v[218:221], v[82:85], v[150:153], v[106:109]
	v_mfma_f32_16x16x32_f16 v[222:225], v[90:93], v[150:153], v[110:113]
	v_mfma_f32_16x16x32_f16 v[218:221], v[86:89], v[154:157], v[218:221]
	v_mfma_f32_16x16x32_f16 v[222:225], v[94:97], v[154:157], v[222:225]
	s_waitcnt lgkmcnt(2)
	v_mfma_f32_16x16x32_f16 v[210:213], v[54:57], v[158:161], v[210:213]
	v_mfma_f32_16x16x32_f16 v[210:213], v[58:61], v[162:165], v[210:213]
	s_waitcnt lgkmcnt(0)
	v_mfma_f32_16x16x32_f16 v[210:213], v[62:65], v[166:169], v[210:213]
	v_mfma_f32_16x16x32_f16 v[210:213], v[50:53], v[170:173], v[210:213]
	s_waitcnt vmcnt(9)
	v_cvt_pk_f16_f32 v251, v194, v195
	ds_write_b32 v1, v251 offset:6144
	ds_read_b128 v[150:153], v186 offset:4096
	ds_read_b128 v[154:157], v186 offset:5120
	s_add_i32 s45, s45, 0x100000
	s_add_i32 s46, s46, 0x4000
	s_movk_i32 s47, 0x1000
	s_add_i32 s43, s40, -12
	s_lshl_b32 s43, s43, 12
	s_cmp_lt_u32 s40, 14
	s_cselect_b32 s43, s47, s43
	v_exp_f32_e32 v226, v210
	v_exp_f32_e32 v227, v211
	v_mfma_f32_16x16x32_f16 v[214:217], v[34:37], v[158:161], v[214:217]
	v_min_f32_e32 v228, s42, v212
	v_exp_f32_e32 v229, v213
	v_mfma_f32_16x16x32_f16 v[214:217], v[38:41], v[162:165], v[214:217]
	v_exp_f32_e32 v228, v228
	v_add_f32_e32 v227, 1.0, v227
	v_mfma_f32_16x16x32_f16 v[214:217], v[42:45], v[166:169], v[214:217]
	v_fma_f32 v230, v228, s41, s41
	v_rcp_f32_e32 v227, v227
	v_mfma_f32_16x16x32_f16 v[214:217], v[46:49], v[170:173], v[214:217]
	v_fma_f32 v230, v226, v230, v230
	v_rcp_f32_e32 v230, v230
	v_mfma_f32_16x16x32_f16 v[218:221], v[18:21], v[158:161], v[218:221]
	v_fma_f32 v226, -v228, v230, v230
	v_fma_f32 v200, v200, v227, v226
	v_mfma_f32_16x16x32_f16 v[218:221], v[14:17], v[162:165], v[218:221]
	v_exp_f32_e32 v226, v200
	s_nop 0
	v_add_f32_e32 v227, 1.0, v226
	v_mfma_f32_16x16x32_f16 v[218:221], v[10:13], v[166:169], v[218:221]
	v_fma_f32 v227, v229, v227, v227
	v_rcp_f32_e32 v227, v227
	v_mfma_f32_16x16x32_f16 v[218:221], v[26:29], v[170:173], v[218:221]
	v_fma_mixlo_f16 v246, -v226, v227, v227
	v_exp_f32_e32 v231, v214
	v_mfma_f32_16x16x32_f16 v[222:225], v[2:5], v[158:161], v[222:225]
	v_exp_f32_e32 v232, v215
	v_min_f32_e32 v233, s42, v216
	v_mfma_f32_16x16x32_f16 v[222:225], v[6:9], v[162:165], v[222:225]
	v_exp_f32_e32 v234, v217
	v_exp_f32_e32 v233, v233
	v_mfma_f32_16x16x32_f16 v[222:225], v[22:25], v[166:169], v[222:225]
	v_exp_f32_e32 v236, v218
	v_add_f32_e32 v232, 1.0, v232
	v_mfma_f32_16x16x32_f16 v[222:225], v[30:33], v[170:173], v[222:225]
	v_fma_f32 v235, v233, s41, s41
	v_exp_f32_e32 v227, v219
	v_rcp_f32_e32 v232, v232
	v_fma_f32 v235, v231, v235, v235
	v_min_f32_e32 v228, s42, v220
	v_rcp_f32_e32 v235, v235
	s_nop 0
	v_fma_f32 v231, -v233, v235, v235
	v_exp_f32_e32 v229, v221
	v_fma_f32 v201, v201, v232, v231
	v_exp_f32_e32 v231, v201
	v_exp_f32_e32 v228, v228
	v_add_f32_e32 v232, 1.0, v231
	v_fma_f32 v232, v234, v232, v232
	v_add_f32_e32 v227, 1.0, v227
	v_rcp_f32_e32 v232, v232
	v_mfma_f32_16x16x32_f16 v[146:149], v[130:133], v[158:161], v[146:149]
	v_fma_mixhi_f16 v246, -v231, v232, v232
	v_fma_f32 v230, v228, s41, s41
	v_exp_f32_e32 v231, v222
	v_mfma_f32_16x16x32_f16 v[146:149], v[134:137], v[162:165], v[146:149]
	v_exp_f32_e32 v232, v223
	v_rcp_f32_e32 v227, v227
	v_min_f32_e32 v233, s42, v224
	buffer_load_dwordx4 v[130:133], v189, s[16:19], s46 offen
	buffer_load_dwordx4 v[134:137], v208, s[16:19], s46 offen
	v_exp_f32_e32 v234, v225
	v_fma_f32 v230, v236, v230, v230
	v_exp_f32_e32 v233, v233
	s_waitcnt lgkmcnt(0)
	v_mfma_f32_16x16x32_f16 v[210:213], v[70:73], v[150:153], v[98:101]
	v_add_f32_e32 v232, 1.0, v232
	v_rcp_f32_e32 v230, v230
	v_fma_f32 v235, v233, s41, s41
	v_mfma_f32_16x16x32_f16 v[214:217], v[74:77], v[150:153], v[102:105]
	v_rcp_f32_e32 v232, v232
	v_fma_f32 v236, -v228, v230, v230
	v_fma_f32 v235, v231, v235, v235
	v_rcp_f32_e32 v235, v235
	v_fma_f32 v198, v198, v227, v236
	v_fma_f32 v231, -v233, v235, v235
	v_fma_f32 v199, v199, v232, v231
	v_exp_f32_e32 v236, v198
	v_exp_f32_e32 v231, v199
	s_nop 0
	v_add_f32_e32 v232, 1.0, v231
	v_add_f32_e32 v227, 1.0, v236
	v_fma_f32 v232, v234, v232, v232
	v_rcp_f32_e32 v232, v232
	v_fma_f32 v227, v229, v227, v227
	v_fma_mixhi_f16 v247, -v231, v232, v232
	v_rcp_f32_e32 v227, v227
	s_nop 0
	v_fma_mixlo_f16 v247, -v236, v227, v227
	ds_write_b64 v206, v[246:247] offset:12288
	v_mfma_f32_16x16x32_f16 v[210:213], v[66:69], v[154:157], v[210:213]
	v_mfma_f32_16x16x32_f16 v[214:217], v[78:81], v[154:157], v[214:217]
	v_mov_b32_e32 v184, v246
	v_mov_b32_e32 v185, v247
	buffer_load_dwordx2 v[194:195], v209, s[20:23], s45 offen
	s_add_i32 s40, s40, 1
	s_add_i32 s44, s44, 0x1000
	s_waitcnt lgkmcnt(0)
	s_barrier
	ds_read_b128 v[158:161], v252 offset:4096
	ds_read_b128 v[162:165], v252 offset:5120
	ds_read_b128 v[166:169], v253 offset:6144
	ds_read_b128 v[170:173], v253 offset:7168
	v_mfma_f32_16x16x32_f16 v[218:221], v[82:85], v[150:153], v[106:109]
	v_mfma_f32_16x16x32_f16 v[222:225], v[90:93], v[150:153], v[110:113]
	v_mfma_f32_16x16x32_f16 v[218:221], v[86:89], v[154:157], v[218:221]
	v_mfma_f32_16x16x32_f16 v[222:225], v[94:97], v[154:157], v[222:225]
	s_waitcnt lgkmcnt(2)
	v_mfma_f32_16x16x32_f16 v[210:213], v[54:57], v[158:161], v[210:213]
	v_mfma_f32_16x16x32_f16 v[210:213], v[58:61], v[162:165], v[210:213]
	s_waitcnt lgkmcnt(0)
	v_mfma_f32_16x16x32_f16 v[210:213], v[62:65], v[166:169], v[210:213]
	v_mfma_f32_16x16x32_f16 v[210:213], v[50:53], v[170:173], v[210:213]
	s_waitcnt vmcnt(9)
	v_cvt_pk_f16_f32 v251, v192, v193
	ds_write_b32 v1, v251 offset:0
	ds_read_b128 v[150:153], v186 offset:6144
	ds_read_b128 v[154:157], v186 offset:7168
	s_add_i32 s45, s45, 0x100000
	s_add_i32 s46, s46, 0x4000
	s_movk_i32 s47, 0x0
	s_add_i32 s43, s40, -12
	s_lshl_b32 s43, s43, 12
	s_cmp_lt_u32 s40, 14
	s_cselect_b32 s43, s47, s43
	v_exp_f32_e32 v226, v210
	v_exp_f32_e32 v227, v211
	v_mfma_f32_16x16x32_f16 v[214:217], v[34:37], v[158:161], v[214:217]
	v_min_f32_e32 v228, s42, v212
	v_exp_f32_e32 v229, v213
	v_mfma_f32_16x16x32_f16 v[214:217], v[38:41], v[162:165], v[214:217]
	v_exp_f32_e32 v228, v228
	v_add_f32_e32 v227, 1.0, v227
	v_mfma_f32_16x16x32_f16 v[214:217], v[42:45], v[166:169], v[214:217]
	v_fma_f32 v230, v228, s41, s41
	v_rcp_f32_e32 v227, v227
	v_mfma_f32_16x16x32_f16 v[214:217], v[46:49], v[170:173], v[214:217]
	v_fma_f32 v230, v226, v230, v230
	v_rcp_f32_e32 v230, v230
	v_mfma_f32_16x16x32_f16 v[218:221], v[18:21], v[158:161], v[218:221]
	v_fma_f32 v226, -v228, v230, v230
	v_fma_f32 v200, v200, v227, v226
	v_mfma_f32_16x16x32_f16 v[218:221], v[14:17], v[162:165], v[218:221]
	v_exp_f32_e32 v226, v200
	s_nop 0
	v_add_f32_e32 v227, 1.0, v226
	v_mfma_f32_16x16x32_f16 v[218:221], v[10:13], v[166:169], v[218:221]
	v_fma_f32 v227, v229, v227, v227
	v_rcp_f32_e32 v227, v227
	v_mfma_f32_16x16x32_f16 v[218:221], v[26:29], v[170:173], v[218:221]
	v_fma_mixlo_f16 v246, -v226, v227, v227
	v_exp_f32_e32 v231, v214
	v_mfma_f32_16x16x32_f16 v[222:225], v[2:5], v[158:161], v[222:225]
	v_exp_f32_e32 v232, v215
	v_min_f32_e32 v233, s42, v216
	v_mfma_f32_16x16x32_f16 v[222:225], v[6:9], v[162:165], v[222:225]
	v_exp_f32_e32 v234, v217
	v_exp_f32_e32 v233, v233
	v_mfma_f32_16x16x32_f16 v[222:225], v[22:25], v[166:169], v[222:225]
	v_exp_f32_e32 v236, v218
	v_add_f32_e32 v232, 1.0, v232
	v_mfma_f32_16x16x32_f16 v[222:225], v[30:33], v[170:173], v[222:225]
	v_fma_f32 v235, v233, s41, s41
	v_exp_f32_e32 v227, v219
	v_rcp_f32_e32 v232, v232
	v_fma_f32 v235, v231, v235, v235
	v_min_f32_e32 v228, s42, v220
	v_rcp_f32_e32 v235, v235
	s_nop 0
	v_fma_f32 v231, -v233, v235, v235
	v_exp_f32_e32 v229, v221
	v_fma_f32 v201, v201, v232, v231
	v_exp_f32_e32 v231, v201
	v_exp_f32_e32 v228, v228
	v_add_f32_e32 v232, 1.0, v231
	v_fma_f32 v232, v234, v232, v232
	v_add_f32_e32 v227, 1.0, v227
	v_rcp_f32_e32 v232, v232
	v_mfma_f32_16x16x32_f16 v[146:149], v[122:125], v[158:161], v[146:149]
	v_fma_mixhi_f16 v246, -v231, v232, v232
	v_fma_f32 v230, v228, s41, s41
	v_exp_f32_e32 v231, v222
	v_mfma_f32_16x16x32_f16 v[146:149], v[126:129], v[162:165], v[146:149]
	v_exp_f32_e32 v232, v223
	v_rcp_f32_e32 v227, v227
	v_min_f32_e32 v233, s42, v224
	buffer_load_dwordx4 v[122:125], v189, s[16:19], s46 offen
	buffer_load_dwordx4 v[126:129], v208, s[16:19], s46 offen
	v_exp_f32_e32 v234, v225
	v_fma_f32 v230, v236, v230, v230
	v_exp_f32_e32 v233, v233
	s_waitcnt lgkmcnt(0)
	v_mfma_f32_16x16x32_f16 v[210:213], v[70:73], v[150:153], v[98:101]
	v_add_f32_e32 v232, 1.0, v232
	v_rcp_f32_e32 v230, v230
	v_fma_f32 v235, v233, s41, s41
	v_mfma_f32_16x16x32_f16 v[214:217], v[74:77], v[150:153], v[102:105]
	v_rcp_f32_e32 v232, v232
	v_fma_f32 v236, -v228, v230, v230
	v_fma_f32 v235, v231, v235, v235
	v_rcp_f32_e32 v235, v235
	v_fma_f32 v198, v198, v227, v236
	v_fma_f32 v231, -v233, v235, v235
	v_fma_f32 v199, v199, v232, v231
	v_exp_f32_e32 v236, v198
	v_exp_f32_e32 v231, v199
	s_nop 0
	v_add_f32_e32 v232, 1.0, v231
	v_add_f32_e32 v227, 1.0, v236
	v_fma_f32 v232, v234, v232, v232
	v_rcp_f32_e32 v232, v232
	v_fma_f32 v227, v229, v227, v227
	v_fma_mixhi_f16 v247, -v231, v232, v232
	v_rcp_f32_e32 v227, v227
	s_nop 0
	v_fma_mixlo_f16 v247, -v236, v227, v227
	ds_write_b64 v206, v[246:247] offset:8192
	v_mfma_f32_16x16x32_f16 v[210:213], v[66:69], v[154:157], v[210:213]
	v_mfma_f32_16x16x32_f16 v[214:217], v[78:81], v[154:157], v[214:217]
	v_mov_b32_e32 v237, v246
	v_mov_b32_e32 v238, v247
	buffer_load_dwordx2 v[192:193], v209, s[20:23], s45 offen
	s_add_i32 s40, s40, 1
	s_add_i32 s44, s44, 0x1000
	s_waitcnt lgkmcnt(0)
	s_barrier
	ds_read_b128 v[158:161], v252 offset:0
	ds_read_b128 v[162:165], v252 offset:1024
	ds_read_b128 v[166:169], v253 offset:2048
	ds_read_b128 v[170:173], v253 offset:3072
	v_mfma_f32_16x16x32_f16 v[218:221], v[82:85], v[150:153], v[106:109]
	v_mfma_f32_16x16x32_f16 v[222:225], v[90:93], v[150:153], v[110:113]
	v_mfma_f32_16x16x32_f16 v[218:221], v[86:89], v[154:157], v[218:221]
	v_mfma_f32_16x16x32_f16 v[222:225], v[94:97], v[154:157], v[222:225]
	s_waitcnt lgkmcnt(2)
	v_mfma_f32_16x16x32_f16 v[210:213], v[54:57], v[158:161], v[210:213]
	v_mfma_f32_16x16x32_f16 v[210:213], v[58:61], v[162:165], v[210:213]
	s_waitcnt lgkmcnt(0)
	v_mfma_f32_16x16x32_f16 v[210:213], v[62:65], v[166:169], v[210:213]
	v_mfma_f32_16x16x32_f16 v[210:213], v[50:53], v[170:173], v[210:213]
	s_waitcnt vmcnt(9)
	v_cvt_pk_f16_f32 v251, v190, v191
	ds_write_b32 v1, v251 offset:2048
	ds_read_b128 v[150:153], v186 offset:0
	ds_read_b128 v[154:157], v186 offset:1024
	s_add_i32 s45, s45, 0x100000
	s_add_i32 s46, s46, 0x4000
	s_movk_i32 s47, 0x1000
	s_add_i32 s43, s40, -12
	s_lshl_b32 s43, s43, 12
	s_cmp_lt_u32 s40, 14
	s_cselect_b32 s43, s47, s43
	v_exp_f32_e32 v226, v210
	v_exp_f32_e32 v227, v211
	v_mfma_f32_16x16x32_f16 v[214:217], v[34:37], v[158:161], v[214:217]
	v_min_f32_e32 v228, s42, v212
	v_exp_f32_e32 v229, v213
	v_mfma_f32_16x16x32_f16 v[214:217], v[38:41], v[162:165], v[214:217]
	v_exp_f32_e32 v228, v228
	v_add_f32_e32 v227, 1.0, v227
	v_mfma_f32_16x16x32_f16 v[214:217], v[42:45], v[166:169], v[214:217]
	v_fma_f32 v230, v228, s41, s41
	v_rcp_f32_e32 v227, v227
	v_mfma_f32_16x16x32_f16 v[214:217], v[46:49], v[170:173], v[214:217]
	v_fma_f32 v230, v226, v230, v230
	v_rcp_f32_e32 v230, v230
	v_mfma_f32_16x16x32_f16 v[218:221], v[18:21], v[158:161], v[218:221]
	v_fma_f32 v226, -v228, v230, v230
	v_fma_f32 v200, v200, v227, v226
	v_mfma_f32_16x16x32_f16 v[218:221], v[14:17], v[162:165], v[218:221]
	v_exp_f32_e32 v226, v200
	s_nop 0
	v_add_f32_e32 v227, 1.0, v226
	v_mfma_f32_16x16x32_f16 v[218:221], v[10:13], v[166:169], v[218:221]
	v_fma_f32 v227, v229, v227, v227
	v_rcp_f32_e32 v227, v227
	v_mfma_f32_16x16x32_f16 v[218:221], v[26:29], v[170:173], v[218:221]
	v_fma_mixlo_f16 v246, -v226, v227, v227
	v_exp_f32_e32 v231, v214
	v_mfma_f32_16x16x32_f16 v[222:225], v[2:5], v[158:161], v[222:225]
	v_exp_f32_e32 v232, v215
	v_min_f32_e32 v233, s42, v216
	v_mfma_f32_16x16x32_f16 v[222:225], v[6:9], v[162:165], v[222:225]
	v_exp_f32_e32 v234, v217
	v_exp_f32_e32 v233, v233
	v_mfma_f32_16x16x32_f16 v[222:225], v[22:25], v[166:169], v[222:225]
	v_exp_f32_e32 v236, v218
	v_add_f32_e32 v232, 1.0, v232
	v_mfma_f32_16x16x32_f16 v[222:225], v[30:33], v[170:173], v[222:225]
	v_fma_f32 v235, v233, s41, s41
	v_exp_f32_e32 v227, v219
	v_rcp_f32_e32 v232, v232
	v_fma_f32 v235, v231, v235, v235
	v_min_f32_e32 v228, s42, v220
	v_rcp_f32_e32 v235, v235
	s_nop 0
	v_fma_f32 v231, -v233, v235, v235
	v_exp_f32_e32 v229, v221
	v_fma_f32 v201, v201, v232, v231
	v_exp_f32_e32 v231, v201
	v_exp_f32_e32 v228, v228
	v_add_f32_e32 v232, 1.0, v231
	v_fma_f32 v232, v234, v232, v232
	v_add_f32_e32 v227, 1.0, v227
	v_rcp_f32_e32 v232, v232
	v_mfma_f32_16x16x32_f16 v[146:149], v[114:117], v[158:161], v[146:149]
	v_fma_mixhi_f16 v246, -v231, v232, v232
	v_fma_f32 v230, v228, s41, s41
	v_exp_f32_e32 v231, v222
	v_mfma_f32_16x16x32_f16 v[146:149], v[118:121], v[162:165], v[146:149]
	v_exp_f32_e32 v232, v223
	v_rcp_f32_e32 v227, v227
	v_min_f32_e32 v233, s42, v224
	buffer_load_dwordx4 v[114:117], v189, s[16:19], s46 offen
	buffer_load_dwordx4 v[118:121], v208, s[16:19], s46 offen
	v_exp_f32_e32 v234, v225
	v_fma_f32 v230, v236, v230, v230
	v_exp_f32_e32 v233, v233
	s_waitcnt lgkmcnt(0)
	v_mfma_f32_16x16x32_f16 v[210:213], v[70:73], v[150:153], v[98:101]
	v_add_f32_e32 v232, 1.0, v232
	v_rcp_f32_e32 v230, v230
	v_fma_f32 v235, v233, s41, s41
	v_mfma_f32_16x16x32_f16 v[214:217], v[74:77], v[150:153], v[102:105]
	v_rcp_f32_e32 v232, v232
	v_fma_f32 v236, -v228, v230, v230
	v_fma_f32 v235, v231, v235, v235
	v_rcp_f32_e32 v235, v235
	v_fma_f32 v198, v198, v227, v236
	v_fma_f32 v231, -v233, v235, v235
	v_fma_f32 v199, v199, v232, v231
	v_exp_f32_e32 v236, v198
	v_exp_f32_e32 v231, v199
	s_nop 0
	v_add_f32_e32 v232, 1.0, v231
	v_add_f32_e32 v227, 1.0, v236
	v_fma_f32 v232, v234, v232, v232
	v_rcp_f32_e32 v232, v232
	v_fma_f32 v227, v229, v227, v227
	v_fma_mixhi_f16 v247, -v231, v232, v232
	v_rcp_f32_e32 v227, v227
	s_nop 0
	v_fma_mixlo_f16 v247, -v236, v227, v227
	ds_write_b64 v206, v[246:247] offset:12288
	v_mfma_f32_16x16x32_f16 v[210:213], v[66:69], v[154:157], v[210:213]
	v_mfma_f32_16x16x32_f16 v[214:217], v[78:81], v[154:157], v[214:217]
	v_mov_b32_e32 v239, v246
	v_mov_b32_e32 v240, v247
	buffer_load_dwordx2 v[190:191], v209, s[20:23], s45 offen
	s_add_i32 s40, s40, 1
	s_add_i32 s44, s44, 0x1000
	s_waitcnt lgkmcnt(0)
	s_barrier
	ds_read_b128 v[158:161], v252 offset:4096
	ds_read_b128 v[162:165], v252 offset:5120
	ds_read_b128 v[166:169], v253 offset:6144
	ds_read_b128 v[170:173], v253 offset:7168
	v_mfma_f32_16x16x32_f16 v[218:221], v[82:85], v[150:153], v[106:109]
	v_mfma_f32_16x16x32_f16 v[222:225], v[90:93], v[150:153], v[110:113]
	v_mfma_f32_16x16x32_f16 v[218:221], v[86:89], v[154:157], v[218:221]
	v_mfma_f32_16x16x32_f16 v[222:225], v[94:97], v[154:157], v[222:225]
	s_waitcnt lgkmcnt(2)
	v_mfma_f32_16x16x32_f16 v[210:213], v[54:57], v[158:161], v[210:213]
	v_mfma_f32_16x16x32_f16 v[210:213], v[58:61], v[162:165], v[210:213]
	s_waitcnt lgkmcnt(0)
	v_mfma_f32_16x16x32_f16 v[210:213], v[62:65], v[166:169], v[210:213]
	v_mfma_f32_16x16x32_f16 v[210:213], v[50:53], v[170:173], v[210:213]
	s_waitcnt vmcnt(9)
	v_cvt_pk_f16_f32 v251, v196, v197
	ds_write_b32 v1, v251 offset:4096
	ds_read_b128 v[150:153], v186 offset:2048
	ds_read_b128 v[154:157], v186 offset:3072
	s_add_i32 s45, s45, 0x100000
	s_add_i32 s46, s46, 0x4000
	s_movk_i32 s47, 0x0
	s_add_i32 s43, s40, -12
	s_lshl_b32 s43, s43, 12
	s_cmp_lt_u32 s40, 14
	s_cselect_b32 s43, s47, s43
	v_exp_f32_e32 v226, v210
	v_exp_f32_e32 v227, v211
	v_mfma_f32_16x16x32_f16 v[214:217], v[34:37], v[158:161], v[214:217]
	v_min_f32_e32 v228, s42, v212
	v_exp_f32_e32 v229, v213
	v_mfma_f32_16x16x32_f16 v[214:217], v[38:41], v[162:165], v[214:217]
	v_exp_f32_e32 v228, v228
	v_add_f32_e32 v227, 1.0, v227
	v_mfma_f32_16x16x32_f16 v[214:217], v[42:45], v[166:169], v[214:217]
	v_fma_f32 v230, v228, s41, s41
	v_rcp_f32_e32 v227, v227
	v_mfma_f32_16x16x32_f16 v[214:217], v[46:49], v[170:173], v[214:217]
	v_fma_f32 v230, v226, v230, v230
	v_rcp_f32_e32 v230, v230
	v_mfma_f32_16x16x32_f16 v[218:221], v[18:21], v[158:161], v[218:221]
	v_fma_f32 v226, -v228, v230, v230
	v_fma_f32 v200, v200, v227, v226
	v_mfma_f32_16x16x32_f16 v[218:221], v[14:17], v[162:165], v[218:221]
	v_exp_f32_e32 v226, v200
	s_nop 0
	v_add_f32_e32 v227, 1.0, v226
	v_mfma_f32_16x16x32_f16 v[218:221], v[10:13], v[166:169], v[218:221]
	v_fma_f32 v227, v229, v227, v227
	v_rcp_f32_e32 v227, v227
	v_mfma_f32_16x16x32_f16 v[218:221], v[26:29], v[170:173], v[218:221]
	v_fma_mixlo_f16 v246, -v226, v227, v227
	v_exp_f32_e32 v231, v214
	v_mfma_f32_16x16x32_f16 v[222:225], v[2:5], v[158:161], v[222:225]
	v_exp_f32_e32 v232, v215
	v_min_f32_e32 v233, s42, v216
	v_mfma_f32_16x16x32_f16 v[222:225], v[6:9], v[162:165], v[222:225]
	v_exp_f32_e32 v234, v217
	v_exp_f32_e32 v233, v233
	v_mfma_f32_16x16x32_f16 v[222:225], v[22:25], v[166:169], v[222:225]
	v_exp_f32_e32 v236, v218
	v_add_f32_e32 v232, 1.0, v232
	v_mfma_f32_16x16x32_f16 v[222:225], v[30:33], v[170:173], v[222:225]
	v_fma_f32 v235, v233, s41, s41
	v_exp_f32_e32 v227, v219
	v_rcp_f32_e32 v232, v232
	v_fma_f32 v235, v231, v235, v235
	v_min_f32_e32 v228, s42, v220
	v_rcp_f32_e32 v235, v235
	s_nop 0
	v_fma_f32 v231, -v233, v235, v235
	v_exp_f32_e32 v229, v221
	v_fma_f32 v201, v201, v232, v231
	v_exp_f32_e32 v231, v201
	v_exp_f32_e32 v228, v228
	v_add_f32_e32 v232, 1.0, v231
	v_fma_f32 v232, v234, v232, v232
	v_add_f32_e32 v227, 1.0, v227
	v_rcp_f32_e32 v232, v232
	v_mfma_f32_16x16x32_f16 v[146:149], v[138:141], v[158:161], v[146:149]
	v_fma_mixhi_f16 v246, -v231, v232, v232
	v_fma_f32 v230, v228, s41, s41
	v_exp_f32_e32 v231, v222
	v_mfma_f32_16x16x32_f16 v[146:149], v[142:145], v[162:165], v[146:149]
	v_exp_f32_e32 v232, v223
	v_rcp_f32_e32 v227, v227
	v_min_f32_e32 v233, s42, v224
	buffer_load_dwordx4 v[138:141], v189, s[16:19], s46 offen
	buffer_load_dwordx4 v[142:145], v208, s[16:19], s46 offen
	v_exp_f32_e32 v234, v225
	v_fma_f32 v230, v236, v230, v230
	v_exp_f32_e32 v233, v233
	s_waitcnt lgkmcnt(0)
	v_mfma_f32_16x16x32_f16 v[210:213], v[70:73], v[150:153], v[98:101]
	v_add_f32_e32 v232, 1.0, v232
	v_rcp_f32_e32 v230, v230
	v_fma_f32 v235, v233, s41, s41
	v_mfma_f32_16x16x32_f16 v[214:217], v[74:77], v[150:153], v[102:105]
	v_rcp_f32_e32 v232, v232
	v_fma_f32 v236, -v228, v230, v230
	v_fma_f32 v235, v231, v235, v235
	v_rcp_f32_e32 v235, v235
	v_fma_f32 v198, v198, v227, v236
	v_fma_f32 v231, -v233, v235, v235
	v_fma_f32 v199, v199, v232, v231
	v_exp_f32_e32 v236, v198
	v_exp_f32_e32 v231, v199
	s_nop 0
	v_add_f32_e32 v232, 1.0, v231
	v_add_f32_e32 v227, 1.0, v236
	v_fma_f32 v232, v234, v232, v232
	v_rcp_f32_e32 v232, v232
	v_fma_f32 v227, v229, v227, v227
	v_fma_mixhi_f16 v247, -v231, v232, v232
	v_rcp_f32_e32 v227, v227
	s_nop 0
	v_fma_mixlo_f16 v247, -v236, v227, v227
	ds_write_b64 v206, v[246:247] offset:8192
	v_mfma_f32_16x16x32_f16 v[210:213], v[66:69], v[154:157], v[210:213]
	v_mfma_f32_16x16x32_f16 v[214:217], v[78:81], v[154:157], v[214:217]
	v_mov_b32_e32 v241, v246
	v_mov_b32_e32 v242, v247
	buffer_load_dwordx2 v[196:197], v209, s[20:23], s45 offen
	s_add_i32 s40, s40, 1
	s_add_i32 s44, s44, 0x1000
	s_waitcnt lgkmcnt(0)
	s_barrier
	ds_read_b128 v[158:161], v252 offset:0
	ds_read_b128 v[162:165], v252 offset:1024
	ds_read_b128 v[166:169], v253 offset:2048
	ds_read_b128 v[170:173], v253 offset:3072
	v_mfma_f32_16x16x32_f16 v[218:221], v[82:85], v[150:153], v[106:109]
	v_mfma_f32_16x16x32_f16 v[222:225], v[90:93], v[150:153], v[110:113]
	v_mfma_f32_16x16x32_f16 v[218:221], v[86:89], v[154:157], v[218:221]
	v_mfma_f32_16x16x32_f16 v[222:225], v[94:97], v[154:157], v[222:225]
	s_waitcnt lgkmcnt(2)
	v_mfma_f32_16x16x32_f16 v[210:213], v[54:57], v[158:161], v[210:213]
	v_mfma_f32_16x16x32_f16 v[210:213], v[58:61], v[162:165], v[210:213]
	s_waitcnt lgkmcnt(0)
	v_mfma_f32_16x16x32_f16 v[210:213], v[62:65], v[166:169], v[210:213]
	v_mfma_f32_16x16x32_f16 v[210:213], v[50:53], v[170:173], v[210:213]
	s_waitcnt vmcnt(9)
	v_cvt_pk_f16_f32 v251, v194, v195
	ds_write_b32 v1, v251 offset:6144
	ds_read_b128 v[150:153], v186 offset:4096
	ds_read_b128 v[154:157], v186 offset:5120
	s_add_i32 s45, s45, 0x100000
	s_add_i32 s46, s46, 0x4000
	s_movk_i32 s47, 0x1000
	s_add_i32 s43, s40, -12
	s_lshl_b32 s43, s43, 12
	s_cmp_lt_u32 s40, 14
	s_cselect_b32 s43, s47, s43
	v_exp_f32_e32 v226, v210
	v_exp_f32_e32 v227, v211
	v_mfma_f32_16x16x32_f16 v[214:217], v[34:37], v[158:161], v[214:217]
	v_min_f32_e32 v228, s42, v212
	v_exp_f32_e32 v229, v213
	v_mfma_f32_16x16x32_f16 v[214:217], v[38:41], v[162:165], v[214:217]
	v_exp_f32_e32 v228, v228
	v_add_f32_e32 v227, 1.0, v227
	v_mfma_f32_16x16x32_f16 v[214:217], v[42:45], v[166:169], v[214:217]
	v_fma_f32 v230, v228, s41, s41
	v_rcp_f32_e32 v227, v227
	v_mfma_f32_16x16x32_f16 v[214:217], v[46:49], v[170:173], v[214:217]
	v_fma_f32 v230, v226, v230, v230
	v_rcp_f32_e32 v230, v230
	v_mfma_f32_16x16x32_f16 v[218:221], v[18:21], v[158:161], v[218:221]
	v_fma_f32 v226, -v228, v230, v230
	v_fma_f32 v200, v200, v227, v226
	v_mfma_f32_16x16x32_f16 v[218:221], v[14:17], v[162:165], v[218:221]
	v_exp_f32_e32 v226, v200
	s_nop 0
	v_add_f32_e32 v227, 1.0, v226
	v_mfma_f32_16x16x32_f16 v[218:221], v[10:13], v[166:169], v[218:221]
	v_fma_f32 v227, v229, v227, v227
	v_rcp_f32_e32 v227, v227
	v_mfma_f32_16x16x32_f16 v[218:221], v[26:29], v[170:173], v[218:221]
	v_fma_mixlo_f16 v246, -v226, v227, v227
	v_exp_f32_e32 v231, v214
	v_mfma_f32_16x16x32_f16 v[222:225], v[2:5], v[158:161], v[222:225]
	v_exp_f32_e32 v232, v215
	v_min_f32_e32 v233, s42, v216
	v_mfma_f32_16x16x32_f16 v[222:225], v[6:9], v[162:165], v[222:225]
	v_exp_f32_e32 v234, v217
	v_exp_f32_e32 v233, v233
	v_mfma_f32_16x16x32_f16 v[222:225], v[22:25], v[166:169], v[222:225]
	v_exp_f32_e32 v236, v218
	v_add_f32_e32 v232, 1.0, v232
	v_mfma_f32_16x16x32_f16 v[222:225], v[30:33], v[170:173], v[222:225]
	v_fma_f32 v235, v233, s41, s41
	v_exp_f32_e32 v227, v219
	v_rcp_f32_e32 v232, v232
	v_fma_f32 v235, v231, v235, v235
	v_min_f32_e32 v228, s42, v220
	v_rcp_f32_e32 v235, v235
	s_nop 0
	v_fma_f32 v231, -v233, v235, v235
	v_exp_f32_e32 v229, v221
	v_fma_f32 v201, v201, v232, v231
	v_exp_f32_e32 v231, v201
	v_exp_f32_e32 v228, v228
	v_add_f32_e32 v232, 1.0, v231
	v_fma_f32 v232, v234, v232, v232
	v_add_f32_e32 v227, 1.0, v227
	v_rcp_f32_e32 v232, v232
	v_mfma_f32_16x16x32_f16 v[146:149], v[130:133], v[158:161], v[146:149]
	v_fma_mixhi_f16 v246, -v231, v232, v232
	v_fma_f32 v230, v228, s41, s41
	v_exp_f32_e32 v231, v222
	v_mfma_f32_16x16x32_f16 v[146:149], v[134:137], v[162:165], v[146:149]
	v_exp_f32_e32 v232, v223
	v_rcp_f32_e32 v227, v227
	v_min_f32_e32 v233, s42, v224
	buffer_load_dwordx4 v[130:133], v189, s[16:19], s46 offen
	buffer_load_dwordx4 v[134:137], v208, s[16:19], s46 offen
	v_exp_f32_e32 v234, v225
	v_fma_f32 v230, v236, v230, v230
	v_exp_f32_e32 v233, v233
	s_waitcnt lgkmcnt(0)
	v_mfma_f32_16x16x32_f16 v[210:213], v[70:73], v[150:153], v[98:101]
	v_add_f32_e32 v232, 1.0, v232
	v_rcp_f32_e32 v230, v230
	v_fma_f32 v235, v233, s41, s41
	v_mfma_f32_16x16x32_f16 v[214:217], v[74:77], v[150:153], v[102:105]
	v_rcp_f32_e32 v232, v232
	v_fma_f32 v236, -v228, v230, v230
	v_fma_f32 v235, v231, v235, v235
	v_rcp_f32_e32 v235, v235
	v_fma_f32 v198, v198, v227, v236
	v_fma_f32 v231, -v233, v235, v235
	v_fma_f32 v199, v199, v232, v231
	v_exp_f32_e32 v236, v198
	v_exp_f32_e32 v231, v199
	s_nop 0
	v_add_f32_e32 v232, 1.0, v231
	v_add_f32_e32 v227, 1.0, v236
	v_fma_f32 v232, v234, v232, v232
	v_rcp_f32_e32 v232, v232
	v_fma_f32 v227, v229, v227, v227
	v_fma_mixhi_f16 v247, -v231, v232, v232
	v_rcp_f32_e32 v227, v227
	s_nop 0
	v_fma_mixlo_f16 v247, -v236, v227, v227
	ds_write_b64 v206, v[246:247] offset:12288
	v_mfma_f32_16x16x32_f16 v[210:213], v[66:69], v[154:157], v[210:213]
	v_mfma_f32_16x16x32_f16 v[214:217], v[78:81], v[154:157], v[214:217]
	v_mov_b32_e32 v243, v246
	v_mov_b32_e32 v244, v247
	buffer_load_dwordx2 v[194:195], v209, s[20:23], s45 offen
	s_add_i32 s40, s40, 1
	s_add_i32 s44, s44, 0x1000
	s_waitcnt lgkmcnt(0)
	s_barrier
	ds_read_b128 v[158:161], v252 offset:4096
	ds_read_b128 v[162:165], v252 offset:5120
	ds_read_b128 v[166:169], v253 offset:6144
	ds_read_b128 v[170:173], v253 offset:7168
	v_mfma_f32_16x16x32_f16 v[218:221], v[82:85], v[150:153], v[106:109]
	v_mfma_f32_16x16x32_f16 v[222:225], v[90:93], v[150:153], v[110:113]
	v_mfma_f32_16x16x32_f16 v[218:221], v[86:89], v[154:157], v[218:221]
	v_mfma_f32_16x16x32_f16 v[222:225], v[94:97], v[154:157], v[222:225]
	s_waitcnt lgkmcnt(2)
	v_mfma_f32_16x16x32_f16 v[210:213], v[54:57], v[158:161], v[210:213]
	v_mfma_f32_16x16x32_f16 v[210:213], v[58:61], v[162:165], v[210:213]
	s_waitcnt lgkmcnt(0)
	v_mfma_f32_16x16x32_f16 v[210:213], v[62:65], v[166:169], v[210:213]
	v_mfma_f32_16x16x32_f16 v[210:213], v[50:53], v[170:173], v[210:213]
	s_waitcnt vmcnt(9)
	v_cvt_pk_f16_f32 v251, v192, v193
	ds_write_b32 v1, v251 offset:0
	ds_read_b128 v[150:153], v186 offset:6144
	ds_read_b128 v[154:157], v186 offset:7168
	s_add_i32 s45, s45, 0x100000
	s_add_i32 s46, s46, 0x4000
	s_movk_i32 s47, 0x0
	s_add_i32 s43, s40, -12
	s_lshl_b32 s43, s43, 12
	s_cmp_lt_u32 s40, 14
	s_cselect_b32 s43, s47, s43
	v_exp_f32_e32 v226, v210
	v_exp_f32_e32 v227, v211
	v_mfma_f32_16x16x32_f16 v[214:217], v[34:37], v[158:161], v[214:217]
	v_min_f32_e32 v228, s42, v212
	v_exp_f32_e32 v229, v213
	v_mfma_f32_16x16x32_f16 v[214:217], v[38:41], v[162:165], v[214:217]
	v_exp_f32_e32 v228, v228
	v_add_f32_e32 v227, 1.0, v227
	v_mfma_f32_16x16x32_f16 v[214:217], v[42:45], v[166:169], v[214:217]
	v_fma_f32 v230, v228, s41, s41
	v_rcp_f32_e32 v227, v227
	v_mfma_f32_16x16x32_f16 v[214:217], v[46:49], v[170:173], v[214:217]
	v_fma_f32 v230, v226, v230, v230
	v_rcp_f32_e32 v230, v230
	v_mfma_f32_16x16x32_f16 v[218:221], v[18:21], v[158:161], v[218:221]
	v_fma_f32 v226, -v228, v230, v230
	v_fma_f32 v200, v200, v227, v226
	v_mfma_f32_16x16x32_f16 v[218:221], v[14:17], v[162:165], v[218:221]
	v_exp_f32_e32 v226, v200
	s_nop 0
	v_add_f32_e32 v227, 1.0, v226
	v_mfma_f32_16x16x32_f16 v[218:221], v[10:13], v[166:169], v[218:221]
	v_fma_f32 v227, v229, v227, v227
	v_rcp_f32_e32 v227, v227
	v_mfma_f32_16x16x32_f16 v[218:221], v[26:29], v[170:173], v[218:221]
	v_fma_mixlo_f16 v246, -v226, v227, v227
	v_exp_f32_e32 v231, v214
	v_mfma_f32_16x16x32_f16 v[222:225], v[2:5], v[158:161], v[222:225]
	v_exp_f32_e32 v232, v215
	v_min_f32_e32 v233, s42, v216
	v_mfma_f32_16x16x32_f16 v[222:225], v[6:9], v[162:165], v[222:225]
	v_exp_f32_e32 v234, v217
	v_exp_f32_e32 v233, v233
	v_mfma_f32_16x16x32_f16 v[222:225], v[22:25], v[166:169], v[222:225]
	v_exp_f32_e32 v236, v218
	v_add_f32_e32 v232, 1.0, v232
	v_mfma_f32_16x16x32_f16 v[222:225], v[30:33], v[170:173], v[222:225]
	v_fma_f32 v235, v233, s41, s41
	v_exp_f32_e32 v227, v219
	v_rcp_f32_e32 v232, v232
	v_fma_f32 v235, v231, v235, v235
	v_min_f32_e32 v228, s42, v220
	v_rcp_f32_e32 v235, v235
	s_nop 0
	v_fma_f32 v231, -v233, v235, v235
	v_exp_f32_e32 v229, v221
	v_fma_f32 v201, v201, v232, v231
	v_exp_f32_e32 v231, v201
	v_exp_f32_e32 v228, v228
	v_add_f32_e32 v232, 1.0, v231
	v_fma_f32 v232, v234, v232, v232
	v_add_f32_e32 v227, 1.0, v227
	v_rcp_f32_e32 v232, v232
	v_mfma_f32_16x16x32_f16 v[146:149], v[122:125], v[158:161], v[146:149]
	v_fma_mixhi_f16 v246, -v231, v232, v232
	v_fma_f32 v230, v228, s41, s41
	v_exp_f32_e32 v231, v222
	v_mfma_f32_16x16x32_f16 v[146:149], v[126:129], v[162:165], v[146:149]
	v_exp_f32_e32 v232, v223
	v_rcp_f32_e32 v227, v227
	v_min_f32_e32 v233, s42, v224
	buffer_load_dwordx4 v[122:125], v189, s[16:19], s46 offen
	buffer_load_dwordx4 v[126:129], v208, s[16:19], s46 offen
	v_exp_f32_e32 v234, v225
	v_fma_f32 v230, v236, v230, v230
	v_exp_f32_e32 v233, v233
	s_waitcnt lgkmcnt(0)
	v_mfma_f32_16x16x32_f16 v[210:213], v[70:73], v[150:153], v[98:101]
	v_add_f32_e32 v232, 1.0, v232
	v_rcp_f32_e32 v230, v230
	v_fma_f32 v235, v233, s41, s41
	v_mfma_f32_16x16x32_f16 v[214:217], v[74:77], v[150:153], v[102:105]
	v_rcp_f32_e32 v232, v232
	v_fma_f32 v236, -v228, v230, v230
	v_fma_f32 v235, v231, v235, v235
	v_rcp_f32_e32 v235, v235
	v_fma_f32 v198, v198, v227, v236
	v_fma_f32 v231, -v233, v235, v235
	v_fma_f32 v199, v199, v232, v231
	v_exp_f32_e32 v236, v198
	v_exp_f32_e32 v231, v199
	s_nop 0
	v_add_f32_e32 v232, 1.0, v231
	v_add_f32_e32 v227, 1.0, v236
	v_fma_f32 v232, v234, v232, v232
	v_rcp_f32_e32 v232, v232
	v_fma_f32 v227, v229, v227, v227
	v_fma_mixhi_f16 v247, -v231, v232, v232
	v_rcp_f32_e32 v227, v227
	s_nop 0
	v_fma_mixlo_f16 v247, -v236, v227, v227
	ds_write_b64 v206, v[246:247] offset:8192
	v_mfma_f32_16x16x32_f16 v[210:213], v[66:69], v[154:157], v[210:213]
	v_mfma_f32_16x16x32_f16 v[214:217], v[78:81], v[154:157], v[214:217]
	v_mov_b32_e32 v245, v246
	v_mov_b32_e32 v187, v247
	buffer_load_dwordx2 v[192:193], v209, s[20:23], s45 offen
	s_add_i32 s40, s40, 1
	s_add_i32 s44, s44, 0x1000
	s_waitcnt lgkmcnt(0)
	s_barrier
	ds_read_b128 v[158:161], v252 offset:0
	ds_read_b128 v[162:165], v252 offset:1024
	ds_read_b128 v[166:169], v253 offset:2048
	ds_read_b128 v[170:173], v253 offset:3072
	v_mfma_f32_16x16x32_f16 v[218:221], v[82:85], v[150:153], v[106:109]
	v_mfma_f32_16x16x32_f16 v[222:225], v[90:93], v[150:153], v[110:113]
	v_mfma_f32_16x16x32_f16 v[218:221], v[86:89], v[154:157], v[218:221]
	v_mfma_f32_16x16x32_f16 v[222:225], v[94:97], v[154:157], v[222:225]
	s_waitcnt lgkmcnt(2)
	v_mfma_f32_16x16x32_f16 v[210:213], v[54:57], v[158:161], v[210:213]
	v_mfma_f32_16x16x32_f16 v[210:213], v[58:61], v[162:165], v[210:213]
	s_waitcnt lgkmcnt(0)
	v_mfma_f32_16x16x32_f16 v[210:213], v[62:65], v[166:169], v[210:213]
	v_mfma_f32_16x16x32_f16 v[210:213], v[50:53], v[170:173], v[210:213]
	s_waitcnt vmcnt(9)
	v_cvt_pk_f16_f32 v251, v190, v191
	ds_write_b32 v1, v251 offset:2048
	ds_read_b128 v[150:153], v186 offset:0
	ds_read_b128 v[154:157], v186 offset:1024
	s_add_i32 s45, s45, 0x100000
	s_add_i32 s46, s46, 0x4000
	s_movk_i32 s47, 0x1000
	s_add_i32 s43, s40, -12
	s_lshl_b32 s43, s43, 12
	s_cmp_lt_u32 s40, 14
	s_cselect_b32 s43, s47, s43
	v_exp_f32_e32 v226, v210
	v_exp_f32_e32 v227, v211
	v_mfma_f32_16x16x32_f16 v[214:217], v[34:37], v[158:161], v[214:217]
	v_min_f32_e32 v228, s42, v212
	v_exp_f32_e32 v229, v213
	v_mfma_f32_16x16x32_f16 v[214:217], v[38:41], v[162:165], v[214:217]
	v_exp_f32_e32 v228, v228
	v_add_f32_e32 v227, 1.0, v227
	v_mfma_f32_16x16x32_f16 v[214:217], v[42:45], v[166:169], v[214:217]
	v_fma_f32 v230, v228, s41, s41
	v_rcp_f32_e32 v227, v227
	v_mfma_f32_16x16x32_f16 v[214:217], v[46:49], v[170:173], v[214:217]
	v_fma_f32 v230, v226, v230, v230
	v_rcp_f32_e32 v230, v230
	v_mfma_f32_16x16x32_f16 v[218:221], v[18:21], v[158:161], v[218:221]
	v_fma_f32 v226, -v228, v230, v230
	v_fma_f32 v200, v200, v227, v226
	v_mfma_f32_16x16x32_f16 v[218:221], v[14:17], v[162:165], v[218:221]
	v_exp_f32_e32 v226, v200
	s_nop 0
	v_add_f32_e32 v227, 1.0, v226
	v_mfma_f32_16x16x32_f16 v[218:221], v[10:13], v[166:169], v[218:221]
	v_fma_f32 v227, v229, v227, v227
	v_rcp_f32_e32 v227, v227
	v_mfma_f32_16x16x32_f16 v[218:221], v[26:29], v[170:173], v[218:221]
	v_fma_mixlo_f16 v246, -v226, v227, v227
	v_exp_f32_e32 v231, v214
	v_mfma_f32_16x16x32_f16 v[222:225], v[2:5], v[158:161], v[222:225]
	v_exp_f32_e32 v232, v215
	v_min_f32_e32 v233, s42, v216
	v_mfma_f32_16x16x32_f16 v[222:225], v[6:9], v[162:165], v[222:225]
	v_exp_f32_e32 v234, v217
	v_exp_f32_e32 v233, v233
	v_mfma_f32_16x16x32_f16 v[222:225], v[22:25], v[166:169], v[222:225]
	v_exp_f32_e32 v236, v218
	v_add_f32_e32 v232, 1.0, v232
	v_mfma_f32_16x16x32_f16 v[222:225], v[30:33], v[170:173], v[222:225]
	v_fma_f32 v235, v233, s41, s41
	v_exp_f32_e32 v227, v219
	v_rcp_f32_e32 v232, v232
	v_fma_f32 v235, v231, v235, v235
	v_min_f32_e32 v228, s42, v220
	v_rcp_f32_e32 v235, v235
	s_nop 0
	v_fma_f32 v231, -v233, v235, v235
	v_exp_f32_e32 v229, v221
	v_fma_f32 v201, v201, v232, v231
	v_exp_f32_e32 v231, v201
	v_exp_f32_e32 v228, v228
	v_add_f32_e32 v232, 1.0, v231
	v_fma_f32 v232, v234, v232, v232
	v_add_f32_e32 v227, 1.0, v227
	v_rcp_f32_e32 v232, v232
	v_mfma_f32_16x16x32_f16 v[146:149], v[114:117], v[158:161], v[146:149]
	v_fma_mixhi_f16 v246, -v231, v232, v232
	v_fma_f32 v230, v228, s41, s41
	v_exp_f32_e32 v231, v222
	v_mfma_f32_16x16x32_f16 v[146:149], v[118:121], v[162:165], v[146:149]
	v_exp_f32_e32 v232, v223
	v_rcp_f32_e32 v227, v227
	v_min_f32_e32 v233, s42, v224
	buffer_load_dwordx4 v[114:117], v189, s[16:19], s46 offen
	buffer_load_dwordx4 v[118:121], v208, s[16:19], s46 offen
	v_exp_f32_e32 v234, v225
	v_fma_f32 v230, v236, v230, v230
	v_exp_f32_e32 v233, v233
	s_waitcnt lgkmcnt(0)
	v_mfma_f32_16x16x32_f16 v[210:213], v[70:73], v[150:153], v[98:101]
	v_add_f32_e32 v232, 1.0, v232
	v_rcp_f32_e32 v230, v230
	v_fma_f32 v235, v233, s41, s41
	v_mfma_f32_16x16x32_f16 v[214:217], v[74:77], v[150:153], v[102:105]
	v_rcp_f32_e32 v232, v232
	v_fma_f32 v236, -v228, v230, v230
	v_fma_f32 v235, v231, v235, v235
	v_rcp_f32_e32 v235, v235
	v_fma_f32 v198, v198, v227, v236
	v_fma_f32 v231, -v233, v235, v235
	v_fma_f32 v199, v199, v232, v231
	v_exp_f32_e32 v236, v198
	v_exp_f32_e32 v231, v199
	s_nop 0
	v_add_f32_e32 v232, 1.0, v231
	v_add_f32_e32 v227, 1.0, v236
	v_fma_f32 v232, v234, v232, v232
	v_rcp_f32_e32 v232, v232
	v_fma_f32 v227, v229, v227, v227
	v_fma_mixhi_f16 v247, -v231, v232, v232
	v_rcp_f32_e32 v227, v227
	s_nop 0
	v_fma_mixlo_f16 v247, -v236, v227, v227
	ds_write_b64 v206, v[246:247] offset:12288
	v_mfma_f32_16x16x32_f16 v[210:213], v[66:69], v[154:157], v[210:213]
	v_mfma_f32_16x16x32_f16 v[214:217], v[78:81], v[154:157], v[214:217]
	v_mov_b32_e32 v188, v246
	v_mov_b32_e32 v202, v247
	buffer_load_dwordx2 v[190:191], v209, s[20:23], s45 offen
	s_add_i32 s40, s40, 1
	s_add_i32 s44, s44, 0x1000
	s_waitcnt lgkmcnt(0)
	s_barrier
	ds_read_b128 v[158:161], v252 offset:4096
	ds_read_b128 v[162:165], v252 offset:5120
	ds_read_b128 v[166:169], v253 offset:6144
	ds_read_b128 v[170:173], v253 offset:7168
	v_mfma_f32_16x16x32_f16 v[218:221], v[82:85], v[150:153], v[106:109]
	v_mfma_f32_16x16x32_f16 v[222:225], v[90:93], v[150:153], v[110:113]
	v_mfma_f32_16x16x32_f16 v[218:221], v[86:89], v[154:157], v[218:221]
	v_mfma_f32_16x16x32_f16 v[222:225], v[94:97], v[154:157], v[222:225]
	s_waitcnt lgkmcnt(2)
	v_mfma_f32_16x16x32_f16 v[210:213], v[54:57], v[158:161], v[210:213]
	v_mfma_f32_16x16x32_f16 v[210:213], v[58:61], v[162:165], v[210:213]
	s_waitcnt lgkmcnt(0)
	v_mfma_f32_16x16x32_f16 v[210:213], v[62:65], v[166:169], v[210:213]
	v_mfma_f32_16x16x32_f16 v[210:213], v[50:53], v[170:173], v[210:213]
	s_waitcnt vmcnt(9)
	v_cvt_pk_f16_f32 v251, v196, v197
	ds_write_b32 v1, v251 offset:4096
	ds_read_b128 v[150:153], v186 offset:2048
	ds_read_b128 v[154:157], v186 offset:3072
	s_add_i32 s45, s45, 0x100000
	s_add_i32 s46, s46, 0x4000
	s_movk_i32 s47, 0x0
	s_add_i32 s43, s40, -12
	s_lshl_b32 s43, s43, 12
	s_cmp_lt_u32 s40, 14
	s_cselect_b32 s43, s47, s43
	v_exp_f32_e32 v226, v210
	v_exp_f32_e32 v227, v211
	v_mfma_f32_16x16x32_f16 v[214:217], v[34:37], v[158:161], v[214:217]
	v_min_f32_e32 v228, s42, v212
	v_exp_f32_e32 v229, v213
	v_mfma_f32_16x16x32_f16 v[214:217], v[38:41], v[162:165], v[214:217]
	v_exp_f32_e32 v228, v228
	v_add_f32_e32 v227, 1.0, v227
	v_mfma_f32_16x16x32_f16 v[214:217], v[42:45], v[166:169], v[214:217]
	v_fma_f32 v230, v228, s41, s41
	v_rcp_f32_e32 v227, v227
	v_mfma_f32_16x16x32_f16 v[214:217], v[46:49], v[170:173], v[214:217]
	v_fma_f32 v230, v226, v230, v230
	v_rcp_f32_e32 v230, v230
	v_mfma_f32_16x16x32_f16 v[218:221], v[18:21], v[158:161], v[218:221]
	v_fma_f32 v226, -v228, v230, v230
	v_fma_f32 v200, v200, v227, v226
	v_mfma_f32_16x16x32_f16 v[218:221], v[14:17], v[162:165], v[218:221]
	v_exp_f32_e32 v226, v200
	s_nop 0
	v_add_f32_e32 v227, 1.0, v226
	v_mfma_f32_16x16x32_f16 v[218:221], v[10:13], v[166:169], v[218:221]
	v_fma_f32 v227, v229, v227, v227
	v_rcp_f32_e32 v227, v227
	v_mfma_f32_16x16x32_f16 v[218:221], v[26:29], v[170:173], v[218:221]
	v_fma_mixlo_f16 v246, -v226, v227, v227
	v_exp_f32_e32 v231, v214
	v_mfma_f32_16x16x32_f16 v[222:225], v[2:5], v[158:161], v[222:225]
	v_exp_f32_e32 v232, v215
	v_min_f32_e32 v233, s42, v216
	v_mfma_f32_16x16x32_f16 v[222:225], v[6:9], v[162:165], v[222:225]
	v_exp_f32_e32 v234, v217
	v_exp_f32_e32 v233, v233
	v_mfma_f32_16x16x32_f16 v[222:225], v[22:25], v[166:169], v[222:225]
	v_exp_f32_e32 v236, v218
	v_add_f32_e32 v232, 1.0, v232
	v_mfma_f32_16x16x32_f16 v[222:225], v[30:33], v[170:173], v[222:225]
	v_fma_f32 v235, v233, s41, s41
	v_exp_f32_e32 v227, v219
	v_rcp_f32_e32 v232, v232
	v_fma_f32 v235, v231, v235, v235
	v_min_f32_e32 v228, s42, v220
	v_rcp_f32_e32 v235, v235
	s_nop 0
	v_fma_f32 v231, -v233, v235, v235
	v_exp_f32_e32 v229, v221
	v_fma_f32 v201, v201, v232, v231
	v_exp_f32_e32 v231, v201
	v_exp_f32_e32 v228, v228
	v_add_f32_e32 v232, 1.0, v231
	v_fma_f32 v232, v234, v232, v232
	v_add_f32_e32 v227, 1.0, v227
	v_rcp_f32_e32 v232, v232
	v_mfma_f32_16x16x32_f16 v[146:149], v[138:141], v[158:161], v[146:149]
	v_fma_mixhi_f16 v246, -v231, v232, v232
	v_fma_f32 v230, v228, s41, s41
	v_exp_f32_e32 v231, v222
	v_mfma_f32_16x16x32_f16 v[146:149], v[142:145], v[162:165], v[146:149]
	v_exp_f32_e32 v232, v223
	v_rcp_f32_e32 v227, v227
	v_min_f32_e32 v233, s42, v224
	buffer_load_dwordx4 v[138:141], v189, s[16:19], s46 offen
	buffer_load_dwordx4 v[142:145], v208, s[16:19], s46 offen
	v_exp_f32_e32 v234, v225
	v_fma_f32 v230, v236, v230, v230
	v_exp_f32_e32 v233, v233
	s_waitcnt lgkmcnt(0)
	v_mfma_f32_16x16x32_f16 v[210:213], v[70:73], v[150:153], v[98:101]
	v_add_f32_e32 v232, 1.0, v232
	v_rcp_f32_e32 v230, v230
	v_fma_f32 v235, v233, s41, s41
	v_mfma_f32_16x16x32_f16 v[214:217], v[74:77], v[150:153], v[102:105]
	v_rcp_f32_e32 v232, v232
	v_fma_f32 v236, -v228, v230, v230
	v_fma_f32 v235, v231, v235, v235
	v_rcp_f32_e32 v235, v235
	v_fma_f32 v198, v198, v227, v236
	v_fma_f32 v231, -v233, v235, v235
	v_fma_f32 v199, v199, v232, v231
	v_exp_f32_e32 v236, v198
	v_exp_f32_e32 v231, v199
	s_nop 0
	v_add_f32_e32 v232, 1.0, v231
	v_add_f32_e32 v227, 1.0, v236
	v_fma_f32 v232, v234, v232, v232
	v_rcp_f32_e32 v232, v232
	v_fma_f32 v227, v229, v227, v227
	v_fma_mixhi_f16 v247, -v231, v232, v232
	v_rcp_f32_e32 v227, v227
	s_nop 0
	v_fma_mixlo_f16 v247, -v236, v227, v227
	ds_write_b64 v206, v[246:247] offset:8192
	v_mfma_f32_16x16x32_f16 v[210:213], v[66:69], v[154:157], v[210:213]
	v_mfma_f32_16x16x32_f16 v[214:217], v[78:81], v[154:157], v[214:217]
	v_mov_b32_e32 v203, v246
	v_mov_b32_e32 v204, v247
	buffer_load_dwordx2 v[196:197], v209, s[20:23], s45 offen
	s_add_i32 s40, s40, 1
	s_add_i32 s44, s44, 0x1000
	s_waitcnt lgkmcnt(0)
	s_barrier
	ds_read_b128 v[158:161], v252 offset:0
	ds_read_b128 v[162:165], v252 offset:1024
	ds_read_b128 v[166:169], v253 offset:2048
	ds_read_b128 v[170:173], v253 offset:3072
	v_mfma_f32_16x16x32_f16 v[218:221], v[82:85], v[150:153], v[106:109]
	v_mfma_f32_16x16x32_f16 v[222:225], v[90:93], v[150:153], v[110:113]
	v_mfma_f32_16x16x32_f16 v[218:221], v[86:89], v[154:157], v[218:221]
	v_mfma_f32_16x16x32_f16 v[222:225], v[94:97], v[154:157], v[222:225]
	s_waitcnt lgkmcnt(2)
	v_mfma_f32_16x16x32_f16 v[210:213], v[54:57], v[158:161], v[210:213]
	v_mfma_f32_16x16x32_f16 v[210:213], v[58:61], v[162:165], v[210:213]
	s_waitcnt lgkmcnt(0)
	v_mfma_f32_16x16x32_f16 v[210:213], v[62:65], v[166:169], v[210:213]
	v_mfma_f32_16x16x32_f16 v[210:213], v[50:53], v[170:173], v[210:213]
	s_waitcnt vmcnt(9)
	v_cvt_pk_f16_f32 v251, v194, v195
	ds_write_b32 v1, v251 offset:6144
	ds_read_b128 v[150:153], v186 offset:4096
	ds_read_b128 v[154:157], v186 offset:5120
	s_add_i32 s45, s45, 0x100000
	s_add_i32 s46, s46, 0x4000
	s_movk_i32 s47, 0x1000
	s_add_i32 s43, s40, -12
	s_lshl_b32 s43, s43, 12
	s_cmp_lt_u32 s40, 14
	s_cselect_b32 s43, s47, s43
	v_exp_f32_e32 v226, v210
	v_exp_f32_e32 v227, v211
	v_mfma_f32_16x16x32_f16 v[214:217], v[34:37], v[158:161], v[214:217]
	v_min_f32_e32 v228, s42, v212
	v_exp_f32_e32 v229, v213
	v_mfma_f32_16x16x32_f16 v[214:217], v[38:41], v[162:165], v[214:217]
	v_exp_f32_e32 v228, v228
	v_add_f32_e32 v227, 1.0, v227
	v_mfma_f32_16x16x32_f16 v[214:217], v[42:45], v[166:169], v[214:217]
	v_fma_f32 v230, v228, s41, s41
	v_rcp_f32_e32 v227, v227
	v_mfma_f32_16x16x32_f16 v[214:217], v[46:49], v[170:173], v[214:217]
	v_fma_f32 v230, v226, v230, v230
	v_rcp_f32_e32 v230, v230
	v_mfma_f32_16x16x32_f16 v[218:221], v[18:21], v[158:161], v[218:221]
	v_fma_f32 v226, -v228, v230, v230
	v_fma_f32 v200, v200, v227, v226
	v_mfma_f32_16x16x32_f16 v[218:221], v[14:17], v[162:165], v[218:221]
	v_exp_f32_e32 v226, v200
	s_nop 0
	v_add_f32_e32 v227, 1.0, v226
	v_mfma_f32_16x16x32_f16 v[218:221], v[10:13], v[166:169], v[218:221]
	v_fma_f32 v227, v229, v227, v227
	v_rcp_f32_e32 v227, v227
	v_mfma_f32_16x16x32_f16 v[218:221], v[26:29], v[170:173], v[218:221]
	v_fma_mixlo_f16 v246, -v226, v227, v227
	v_exp_f32_e32 v231, v214
	v_mfma_f32_16x16x32_f16 v[222:225], v[2:5], v[158:161], v[222:225]
	v_exp_f32_e32 v232, v215
	v_min_f32_e32 v233, s42, v216
	v_mfma_f32_16x16x32_f16 v[222:225], v[6:9], v[162:165], v[222:225]
	v_exp_f32_e32 v234, v217
	v_exp_f32_e32 v233, v233
	v_mfma_f32_16x16x32_f16 v[222:225], v[22:25], v[166:169], v[222:225]
	v_exp_f32_e32 v236, v218
	v_add_f32_e32 v232, 1.0, v232
	v_mfma_f32_16x16x32_f16 v[222:225], v[30:33], v[170:173], v[222:225]
	v_fma_f32 v235, v233, s41, s41
	v_exp_f32_e32 v227, v219
	v_rcp_f32_e32 v232, v232
	v_fma_f32 v235, v231, v235, v235
	v_min_f32_e32 v228, s42, v220
	v_rcp_f32_e32 v235, v235
	s_nop 0
	v_fma_f32 v231, -v233, v235, v235
	v_exp_f32_e32 v229, v221
	v_fma_f32 v201, v201, v232, v231
	v_exp_f32_e32 v231, v201
	v_exp_f32_e32 v228, v228
	v_add_f32_e32 v232, 1.0, v231
	v_fma_f32 v232, v234, v232, v232
	v_add_f32_e32 v227, 1.0, v227
	v_rcp_f32_e32 v232, v232
	v_mfma_f32_16x16x32_f16 v[146:149], v[130:133], v[158:161], v[146:149]
	v_fma_mixhi_f16 v246, -v231, v232, v232
	v_fma_f32 v230, v228, s41, s41
	v_exp_f32_e32 v231, v222
	v_mfma_f32_16x16x32_f16 v[146:149], v[134:137], v[162:165], v[146:149]
	v_exp_f32_e32 v232, v223
	v_rcp_f32_e32 v227, v227
	v_min_f32_e32 v233, s42, v224
	buffer_load_dwordx4 v[130:133], v189, s[16:19], s46 offen
	buffer_load_dwordx4 v[134:137], v208, s[16:19], s46 offen
	v_exp_f32_e32 v234, v225
	v_fma_f32 v230, v236, v230, v230
	v_exp_f32_e32 v233, v233
	s_waitcnt lgkmcnt(0)
	v_mfma_f32_16x16x32_f16 v[210:213], v[70:73], v[150:153], v[98:101]
	v_add_f32_e32 v232, 1.0, v232
	v_rcp_f32_e32 v230, v230
	v_fma_f32 v235, v233, s41, s41
	v_mfma_f32_16x16x32_f16 v[214:217], v[74:77], v[150:153], v[102:105]
	v_rcp_f32_e32 v232, v232
	v_fma_f32 v236, -v228, v230, v230
	v_fma_f32 v235, v231, v235, v235
	v_rcp_f32_e32 v235, v235
	v_fma_f32 v198, v198, v227, v236
	v_fma_f32 v231, -v233, v235, v235
	v_fma_f32 v199, v199, v232, v231
	v_exp_f32_e32 v236, v198
	v_exp_f32_e32 v231, v199
	s_nop 0
	v_add_f32_e32 v232, 1.0, v231
	v_add_f32_e32 v227, 1.0, v236
	v_fma_f32 v232, v234, v232, v232
	v_rcp_f32_e32 v232, v232
	v_fma_f32 v227, v229, v227, v227
	v_fma_mixhi_f16 v247, -v231, v232, v232
	v_rcp_f32_e32 v227, v227
	s_nop 0
	v_fma_mixlo_f16 v247, -v236, v227, v227
	ds_write_b64 v206, v[246:247] offset:12288
	v_mfma_f32_16x16x32_f16 v[210:213], v[66:69], v[154:157], v[210:213]
	v_mfma_f32_16x16x32_f16 v[214:217], v[78:81], v[154:157], v[214:217]
	v_mov_b32_e32 v205, v246
	v_mov_b32_e32 v207, v247
	buffer_load_dwordx2 v[194:195], v209, s[20:23], s45 offen
	s_add_i32 s40, s40, 1
	s_add_i32 s44, s44, 0x1000
	s_waitcnt lgkmcnt(0)
	s_barrier
	v_add_u32_e32 v250, 0x1000, v206
	v_add_u32_e32 v248, 0x1000, v252
	v_add_u32_e32 v249, 0x1000, v253
	s_mov_b32 s45, 0xc00000
	s_mov_b32 s46, 0x30000
.Lmy_loopb:
	ds_read_b128 v[158:161], v248 offset:0
	ds_read_b128 v[162:165], v248 offset:1024
	ds_read_b128 v[166:169], v249 offset:2048
	ds_read_b128 v[170:173], v249 offset:3072
	v_mfma_f32_16x16x32_f16 v[218:221], v[82:85], v[150:153], v[106:109]
	v_mfma_f32_16x16x32_f16 v[222:225], v[90:93], v[150:153], v[110:113]
	v_mfma_f32_16x16x32_f16 v[218:221], v[86:89], v[154:157], v[218:221]
	v_mfma_f32_16x16x32_f16 v[222:225], v[94:97], v[154:157], v[222:225]
	s_waitcnt lgkmcnt(2)
	v_mfma_f32_16x16x32_f16 v[210:213], v[54:57], v[158:161], v[210:213]
	v_mfma_f32_16x16x32_f16 v[210:213], v[58:61], v[162:165], v[210:213]
	s_waitcnt lgkmcnt(0)
	v_mfma_f32_16x16x32_f16 v[210:213], v[62:65], v[166:169], v[210:213]
	v_mfma_f32_16x16x32_f16 v[210:213], v[50:53], v[170:173], v[210:213]
	s_waitcnt vmcnt(9)
	v_cvt_pk_f16_f32 v251, v192, v193
	ds_write_b32 v1, v251 offset:0
	ds_read_b128 v[150:153], v186 offset:6144
	ds_read_b128 v[154:157], v186 offset:7168
	s_nop 2
	v_exp_f32_e32 v226, v210
	v_exp_f32_e32 v227, v211
	v_mfma_f32_16x16x32_f16 v[214:217], v[34:37], v[158:161], v[214:217]
	v_min_f32_e32 v228, s42, v212
	v_exp_f32_e32 v229, v213
	v_mfma_f32_16x16x32_f16 v[214:217], v[38:41], v[162:165], v[214:217]
	v_exp_f32_e32 v228, v228
	v_add_f32_e32 v227, 1.0, v227
	v_mfma_f32_16x16x32_f16 v[214:217], v[42:45], v[166:169], v[214:217]
	v_fma_f32 v230, v228, s41, s41
	v_rcp_f32_e32 v227, v227
	v_mfma_f32_16x16x32_f16 v[214:217], v[46:49], v[170:173], v[214:217]
	v_fma_f32 v230, v226, v230, v230
	v_rcp_f32_e32 v230, v230
	v_mfma_f32_16x16x32_f16 v[218:221], v[18:21], v[158:161], v[218:221]
	v_fma_f32 v226, -v228, v230, v230
	v_fma_f32 v200, v200, v227, v226
	v_mfma_f32_16x16x32_f16 v[218:221], v[14:17], v[162:165], v[218:221]
	v_exp_f32_e32 v226, v200
	s_nop 0
	v_add_f32_e32 v227, 1.0, v226
	v_mfma_f32_16x16x32_f16 v[218:221], v[10:13], v[166:169], v[218:221]
	v_fma_f32 v227, v229, v227, v227
	v_rcp_f32_e32 v227, v227
	v_mfma_f32_16x16x32_f16 v[218:221], v[26:29], v[170:173], v[218:221]
	v_fma_mixlo_f16 v246, -v226, v227, v227
	v_exp_f32_e32 v231, v214
	v_mfma_f32_16x16x32_f16 v[222:225], v[2:5], v[158:161], v[222:225]
	v_exp_f32_e32 v232, v215
	v_min_f32_e32 v233, s42, v216
	v_mfma_f32_16x16x32_f16 v[222:225], v[6:9], v[162:165], v[222:225]
	v_exp_f32_e32 v234, v217
	v_exp_f32_e32 v233, v233
	v_mfma_f32_16x16x32_f16 v[222:225], v[22:25], v[166:169], v[222:225]
	v_exp_f32_e32 v236, v218
	v_add_f32_e32 v232, 1.0, v232
	v_mfma_f32_16x16x32_f16 v[222:225], v[30:33], v[170:173], v[222:225]
	v_fma_f32 v235, v233, s41, s41
	v_exp_f32_e32 v227, v219
	v_rcp_f32_e32 v232, v232
	v_fma_f32 v235, v231, v235, v235
	v_min_f32_e32 v228, s42, v220
	v_rcp_f32_e32 v235, v235
	s_nop 0
	v_fma_f32 v231, -v233, v235, v235
	v_exp_f32_e32 v229, v221
	v_fma_f32 v201, v201, v232, v231
	v_exp_f32_e32 v231, v201
	v_exp_f32_e32 v228, v228
	v_add_f32_e32 v232, 1.0, v231
	v_fma_f32 v232, v234, v232, v232
	v_add_f32_e32 v227, 1.0, v227
	v_rcp_f32_e32 v232, v232
	v_mfma_f32_16x16x32_f16 v[146:149], v[122:125], v[158:161], v[146:149]
	v_fma_mixhi_f16 v246, -v231, v232, v232
	v_fma_f32 v230, v228, s41, s41
	v_exp_f32_e32 v231, v222
	v_mfma_f32_16x16x32_f16 v[146:149], v[126:129], v[162:165], v[146:149]
	v_exp_f32_e32 v232, v223
	v_rcp_f32_e32 v227, v227
	v_min_f32_e32 v233, s42, v224
	buffer_load_dwordx4 v[122:125], v189, s[76:79], s46 offen
	buffer_load_dwordx4 v[126:129], v208, s[76:79], s46 offen
	v_exp_f32_e32 v234, v225
	v_fma_f32 v230, v236, v230, v230
	v_exp_f32_e32 v233, v233
	s_waitcnt lgkmcnt(0)
	v_mfma_f32_16x16x32_f16 v[210:213], v[70:73], v[150:153], v[98:101]
	v_add_f32_e32 v232, 1.0, v232
	v_rcp_f32_e32 v230, v230
	v_fma_f32 v235, v233, s41, s41
	v_mfma_f32_16x16x32_f16 v[214:217], v[74:77], v[150:153], v[102:105]
	v_rcp_f32_e32 v232, v232
	v_fma_f32 v236, -v228, v230, v230
	v_fma_f32 v235, v231, v235, v235
	v_rcp_f32_e32 v235, v235
	v_fma_f32 v198, v198, v227, v236
	v_fma_f32 v231, -v233, v235, v235
	v_fma_f32 v199, v199, v232, v231
	v_exp_f32_e32 v236, v198
	v_exp_f32_e32 v231, v199
	s_nop 0
	v_add_f32_e32 v232, 1.0, v231
	v_add_f32_e32 v227, 1.0, v236
	v_fma_f32 v232, v234, v232, v232
	v_rcp_f32_e32 v232, v232
	v_fma_f32 v227, v229, v227, v227
	v_fma_mixhi_f16 v247, -v231, v232, v232
	v_rcp_f32_e32 v227, v227
	s_nop 0
	v_fma_mixlo_f16 v247, -v236, v227, v227
	ds_write_b64 v250, v[246:247] offset:12288
	v_mfma_f32_16x16x32_f16 v[210:213], v[66:69], v[154:157], v[210:213]
	v_mfma_f32_16x16x32_f16 v[214:217], v[78:81], v[154:157], v[214:217]
	buffer_load_dwordx2 v[192:193], v209, s[56:59], s45 offen
	s_waitcnt lgkmcnt(0)
	s_barrier
	ds_read_b128 v[158:161], v248 offset:4096
	ds_read_b128 v[162:165], v248 offset:5120
	ds_read_b128 v[166:169], v249 offset:6144
	ds_read_b128 v[170:173], v249 offset:7168
	v_mfma_f32_16x16x32_f16 v[218:221], v[82:85], v[150:153], v[106:109]
	v_mfma_f32_16x16x32_f16 v[222:225], v[90:93], v[150:153], v[110:113]
	v_mfma_f32_16x16x32_f16 v[218:221], v[86:89], v[154:157], v[218:221]
	v_mfma_f32_16x16x32_f16 v[222:225], v[94:97], v[154:157], v[222:225]
	s_waitcnt lgkmcnt(2)
	v_mfma_f32_16x16x32_f16 v[210:213], v[54:57], v[158:161], v[210:213]
	v_mfma_f32_16x16x32_f16 v[210:213], v[58:61], v[162:165], v[210:213]
	s_waitcnt lgkmcnt(0)
	v_mfma_f32_16x16x32_f16 v[210:213], v[62:65], v[166:169], v[210:213]
	v_mfma_f32_16x16x32_f16 v[210:213], v[50:53], v[170:173], v[210:213]
	s_waitcnt vmcnt(9)
	v_cvt_pk_f16_f32 v251, v190, v191
	ds_write_b32 v1, v251 offset:2048
	ds_read_b128 v[150:153], v186 offset:0
	ds_read_b128 v[154:157], v186 offset:1024
	s_nop 2
	v_exp_f32_e32 v226, v210
	v_exp_f32_e32 v227, v211
	v_mfma_f32_16x16x32_f16 v[214:217], v[34:37], v[158:161], v[214:217]
	v_min_f32_e32 v228, s42, v212
	v_exp_f32_e32 v229, v213
	v_mfma_f32_16x16x32_f16 v[214:217], v[38:41], v[162:165], v[214:217]
	v_exp_f32_e32 v228, v228
	v_add_f32_e32 v227, 1.0, v227
	v_mfma_f32_16x16x32_f16 v[214:217], v[42:45], v[166:169], v[214:217]
	v_fma_f32 v230, v228, s41, s41
	v_rcp_f32_e32 v227, v227
	v_mfma_f32_16x16x32_f16 v[214:217], v[46:49], v[170:173], v[214:217]
	v_fma_f32 v230, v226, v230, v230
	v_rcp_f32_e32 v230, v230
	v_mfma_f32_16x16x32_f16 v[218:221], v[18:21], v[158:161], v[218:221]
	v_fma_f32 v226, -v228, v230, v230
	v_fma_f32 v200, v200, v227, v226
	v_mfma_f32_16x16x32_f16 v[218:221], v[14:17], v[162:165], v[218:221]
	v_exp_f32_e32 v226, v200
	s_nop 0
	v_add_f32_e32 v227, 1.0, v226
	v_mfma_f32_16x16x32_f16 v[218:221], v[10:13], v[166:169], v[218:221]
	v_fma_f32 v227, v229, v227, v227
	v_rcp_f32_e32 v227, v227
	v_mfma_f32_16x16x32_f16 v[218:221], v[26:29], v[170:173], v[218:221]
	v_fma_mixlo_f16 v246, -v226, v227, v227
	v_exp_f32_e32 v231, v214
	v_mfma_f32_16x16x32_f16 v[222:225], v[2:5], v[158:161], v[222:225]
	v_exp_f32_e32 v232, v215
	v_min_f32_e32 v233, s42, v216
	v_mfma_f32_16x16x32_f16 v[222:225], v[6:9], v[162:165], v[222:225]
	v_exp_f32_e32 v234, v217
	v_exp_f32_e32 v233, v233
	v_mfma_f32_16x16x32_f16 v[222:225], v[22:25], v[166:169], v[222:225]
	v_exp_f32_e32 v236, v218
	v_add_f32_e32 v232, 1.0, v232
	v_mfma_f32_16x16x32_f16 v[222:225], v[30:33], v[170:173], v[222:225]
	v_fma_f32 v235, v233, s41, s41
	v_exp_f32_e32 v227, v219
	v_rcp_f32_e32 v232, v232
	v_fma_f32 v235, v231, v235, v235
	v_min_f32_e32 v228, s42, v220
	v_rcp_f32_e32 v235, v235
	s_nop 0
	v_fma_f32 v231, -v233, v235, v235
	v_exp_f32_e32 v229, v221
	v_fma_f32 v201, v201, v232, v231
	v_exp_f32_e32 v231, v201
	v_exp_f32_e32 v228, v228
	v_add_f32_e32 v232, 1.0, v231
	v_fma_f32 v232, v234, v232, v232
	v_add_f32_e32 v227, 1.0, v227
	v_rcp_f32_e32 v232, v232
	v_mfma_f32_16x16x32_f16 v[146:149], v[114:117], v[158:161], v[146:149]
	v_fma_mixhi_f16 v246, -v231, v232, v232
	v_fma_f32 v230, v228, s41, s41
	v_exp_f32_e32 v231, v222
	v_mfma_f32_16x16x32_f16 v[146:149], v[118:121], v[162:165], v[146:149]
	v_exp_f32_e32 v232, v223
	v_rcp_f32_e32 v227, v227
	v_min_f32_e32 v233, s42, v224
	buffer_load_dwordx4 v[114:117], v189, s[80:83], s46 offen
	buffer_load_dwordx4 v[118:121], v208, s[80:83], s46 offen
	v_exp_f32_e32 v234, v225
	v_fma_f32 v230, v236, v230, v230
	v_exp_f32_e32 v233, v233
	s_waitcnt lgkmcnt(0)
	v_mfma_f32_16x16x32_f16 v[210:213], v[70:73], v[150:153], v[98:101]
	v_add_f32_e32 v232, 1.0, v232
	v_rcp_f32_e32 v230, v230
	v_fma_f32 v235, v233, s41, s41
	v_mfma_f32_16x16x32_f16 v[214:217], v[74:77], v[150:153], v[102:105]
	v_rcp_f32_e32 v232, v232
	v_fma_f32 v236, -v228, v230, v230
	v_fma_f32 v235, v231, v235, v235
	v_rcp_f32_e32 v235, v235
	v_fma_f32 v198, v198, v227, v236
	v_fma_f32 v231, -v233, v235, v235
	v_fma_f32 v199, v199, v232, v231
	v_exp_f32_e32 v236, v198
	v_exp_f32_e32 v231, v199
	s_nop 0
	v_add_f32_e32 v232, 1.0, v231
	v_add_f32_e32 v227, 1.0, v236
	v_fma_f32 v232, v234, v232, v232
	v_rcp_f32_e32 v232, v232
	v_fma_f32 v227, v229, v227, v227
	v_fma_mixhi_f16 v247, -v231, v232, v232
	v_rcp_f32_e32 v227, v227
	s_nop 0
	v_fma_mixlo_f16 v247, -v236, v227, v227
	ds_write_b64 v250, v[246:247] offset:16384
	v_mfma_f32_16x16x32_f16 v[210:213], v[66:69], v[154:157], v[210:213]
	v_mfma_f32_16x16x32_f16 v[214:217], v[78:81], v[154:157], v[214:217]
	buffer_load_dwordx2 v[190:191], v209, s[60:63], s45 offen
	s_add_i32 s45, s45, 0x400000
	s_add_i32 s46, s46, 0x10000
	s_waitcnt lgkmcnt(0)
	s_barrier
	ds_read_b128 v[158:161], v248 offset:8192
	ds_read_b128 v[162:165], v248 offset:9216
	ds_read_b128 v[166:169], v249 offset:10240
	ds_read_b128 v[170:173], v249 offset:11264
	v_mfma_f32_16x16x32_f16 v[218:221], v[82:85], v[150:153], v[106:109]
	v_mfma_f32_16x16x32_f16 v[222:225], v[90:93], v[150:153], v[110:113]
	v_mfma_f32_16x16x32_f16 v[218:221], v[86:89], v[154:157], v[218:221]
	v_mfma_f32_16x16x32_f16 v[222:225], v[94:97], v[154:157], v[222:225]
	s_waitcnt lgkmcnt(2)
	v_mfma_f32_16x16x32_f16 v[210:213], v[54:57], v[158:161], v[210:213]
	v_mfma_f32_16x16x32_f16 v[210:213], v[58:61], v[162:165], v[210:213]
	s_waitcnt lgkmcnt(0)
	v_mfma_f32_16x16x32_f16 v[210:213], v[62:65], v[166:169], v[210:213]
	v_mfma_f32_16x16x32_f16 v[210:213], v[50:53], v[170:173], v[210:213]
	s_waitcnt vmcnt(9)
	v_cvt_pk_f16_f32 v251, v196, v197
	ds_write_b32 v1, v251 offset:4096
	ds_read_b128 v[150:153], v186 offset:2048
	ds_read_b128 v[154:157], v186 offset:3072
	s_nop 2
	v_exp_f32_e32 v226, v210
	v_exp_f32_e32 v227, v211
	v_mfma_f32_16x16x32_f16 v[214:217], v[34:37], v[158:161], v[214:217]
	v_min_f32_e32 v228, s42, v212
	v_exp_f32_e32 v229, v213
	v_mfma_f32_16x16x32_f16 v[214:217], v[38:41], v[162:165], v[214:217]
	v_exp_f32_e32 v228, v228
	v_add_f32_e32 v227, 1.0, v227
	v_mfma_f32_16x16x32_f16 v[214:217], v[42:45], v[166:169], v[214:217]
	v_fma_f32 v230, v228, s41, s41
	v_rcp_f32_e32 v227, v227
	v_mfma_f32_16x16x32_f16 v[214:217], v[46:49], v[170:173], v[214:217]
	v_fma_f32 v230, v226, v230, v230
	v_rcp_f32_e32 v230, v230
	v_mfma_f32_16x16x32_f16 v[218:221], v[18:21], v[158:161], v[218:221]
	v_fma_f32 v226, -v228, v230, v230
	v_fma_f32 v200, v200, v227, v226
	v_mfma_f32_16x16x32_f16 v[218:221], v[14:17], v[162:165], v[218:221]
	v_exp_f32_e32 v226, v200
	s_nop 0
	v_add_f32_e32 v227, 1.0, v226
	v_mfma_f32_16x16x32_f16 v[218:221], v[10:13], v[166:169], v[218:221]
	v_fma_f32 v227, v229, v227, v227
	v_rcp_f32_e32 v227, v227
	v_mfma_f32_16x16x32_f16 v[218:221], v[26:29], v[170:173], v[218:221]
	v_fma_mixlo_f16 v246, -v226, v227, v227
	v_exp_f32_e32 v231, v214
	v_mfma_f32_16x16x32_f16 v[222:225], v[2:5], v[158:161], v[222:225]
	v_exp_f32_e32 v232, v215
	v_min_f32_e32 v233, s42, v216
	v_mfma_f32_16x16x32_f16 v[222:225], v[6:9], v[162:165], v[222:225]
	v_exp_f32_e32 v234, v217
	v_exp_f32_e32 v233, v233
	v_mfma_f32_16x16x32_f16 v[222:225], v[22:25], v[166:169], v[222:225]
	v_exp_f32_e32 v236, v218
	v_add_f32_e32 v232, 1.0, v232
	v_mfma_f32_16x16x32_f16 v[222:225], v[30:33], v[170:173], v[222:225]
	v_fma_f32 v235, v233, s41, s41
	v_exp_f32_e32 v227, v219
	v_rcp_f32_e32 v232, v232
	v_fma_f32 v235, v231, v235, v235
	v_min_f32_e32 v228, s42, v220
	v_rcp_f32_e32 v235, v235
	s_nop 0
	v_fma_f32 v231, -v233, v235, v235
	v_exp_f32_e32 v229, v221
	v_fma_f32 v201, v201, v232, v231
	v_exp_f32_e32 v231, v201
	v_exp_f32_e32 v228, v228
	v_add_f32_e32 v232, 1.0, v231
	v_fma_f32 v232, v234, v232, v232
	v_add_f32_e32 v227, 1.0, v227
	v_rcp_f32_e32 v232, v232
	v_mfma_f32_16x16x32_f16 v[146:149], v[138:141], v[158:161], v[146:149]
	v_fma_mixhi_f16 v246, -v231, v232, v232
	v_fma_f32 v230, v228, s41, s41
	v_exp_f32_e32 v231, v222
	v_mfma_f32_16x16x32_f16 v[146:149], v[142:145], v[162:165], v[146:149]
	v_exp_f32_e32 v232, v223
	v_rcp_f32_e32 v227, v227
	v_min_f32_e32 v233, s42, v224
	buffer_load_dwordx4 v[138:141], v189, s[68:71], s46 offen
	buffer_load_dwordx4 v[142:145], v208, s[68:71], s46 offen
	v_exp_f32_e32 v234, v225
	v_fma_f32 v230, v236, v230, v230
	v_exp_f32_e32 v233, v233
	s_waitcnt lgkmcnt(0)
	v_mfma_f32_16x16x32_f16 v[210:213], v[70:73], v[150:153], v[98:101]
	v_add_f32_e32 v232, 1.0, v232
	v_rcp_f32_e32 v230, v230
	v_fma_f32 v235, v233, s41, s41
	v_mfma_f32_16x16x32_f16 v[214:217], v[74:77], v[150:153], v[102:105]
	v_rcp_f32_e32 v232, v232
	v_fma_f32 v236, -v228, v230, v230
	v_fma_f32 v235, v231, v235, v235
	v_rcp_f32_e32 v235, v235
	v_fma_f32 v198, v198, v227, v236
	v_fma_f32 v231, -v233, v235, v235
	v_fma_f32 v199, v199, v232, v231
	v_exp_f32_e32 v236, v198
	v_exp_f32_e32 v231, v199
	s_nop 0
	v_add_f32_e32 v232, 1.0, v231
	v_add_f32_e32 v227, 1.0, v236
	v_fma_f32 v232, v234, v232, v232
	v_rcp_f32_e32 v232, v232
	v_fma_f32 v227, v229, v227, v227
	v_fma_mixhi_f16 v247, -v231, v232, v232
	v_rcp_f32_e32 v227, v227
	s_nop 0
	v_fma_mixlo_f16 v247, -v236, v227, v227
	ds_write_b64 v250, v[246:247] offset:20480
	v_mfma_f32_16x16x32_f16 v[210:213], v[66:69], v[154:157], v[210:213]
	v_mfma_f32_16x16x32_f16 v[214:217], v[78:81], v[154:157], v[214:217]
	buffer_load_dwordx2 v[196:197], v209, s[48:51], s45 offen
	s_waitcnt lgkmcnt(0)
	s_barrier
	ds_read_b128 v[158:161], v248 offset:12288
	ds_read_b128 v[162:165], v248 offset:13312
	ds_read_b128 v[166:169], v249 offset:14336
	ds_read_b128 v[170:173], v249 offset:15360
	v_mfma_f32_16x16x32_f16 v[218:221], v[82:85], v[150:153], v[106:109]
	v_mfma_f32_16x16x32_f16 v[222:225], v[90:93], v[150:153], v[110:113]
	v_mfma_f32_16x16x32_f16 v[218:221], v[86:89], v[154:157], v[218:221]
	v_mfma_f32_16x16x32_f16 v[222:225], v[94:97], v[154:157], v[222:225]
	s_waitcnt lgkmcnt(2)
	v_mfma_f32_16x16x32_f16 v[210:213], v[54:57], v[158:161], v[210:213]
	v_mfma_f32_16x16x32_f16 v[210:213], v[58:61], v[162:165], v[210:213]
	s_waitcnt lgkmcnt(0)
	v_mfma_f32_16x16x32_f16 v[210:213], v[62:65], v[166:169], v[210:213]
	v_mfma_f32_16x16x32_f16 v[210:213], v[50:53], v[170:173], v[210:213]
	s_waitcnt vmcnt(9)
	v_cvt_pk_f16_f32 v251, v194, v195
	ds_write_b32 v1, v251 offset:6144
	ds_read_b128 v[150:153], v186 offset:4096
	ds_read_b128 v[154:157], v186 offset:5120
	s_nop 2
	v_exp_f32_e32 v226, v210
	v_exp_f32_e32 v227, v211
	v_mfma_f32_16x16x32_f16 v[214:217], v[34:37], v[158:161], v[214:217]
	v_min_f32_e32 v228, s42, v212
	v_exp_f32_e32 v229, v213
	v_mfma_f32_16x16x32_f16 v[214:217], v[38:41], v[162:165], v[214:217]
	v_exp_f32_e32 v228, v228
	v_add_f32_e32 v227, 1.0, v227
	v_mfma_f32_16x16x32_f16 v[214:217], v[42:45], v[166:169], v[214:217]
	v_fma_f32 v230, v228, s41, s41
	v_rcp_f32_e32 v227, v227
	v_mfma_f32_16x16x32_f16 v[214:217], v[46:49], v[170:173], v[214:217]
	v_fma_f32 v230, v226, v230, v230
	v_rcp_f32_e32 v230, v230
	v_mfma_f32_16x16x32_f16 v[218:221], v[18:21], v[158:161], v[218:221]
	v_fma_f32 v226, -v228, v230, v230
	v_fma_f32 v200, v200, v227, v226
	v_mfma_f32_16x16x32_f16 v[218:221], v[14:17], v[162:165], v[218:221]
	v_exp_f32_e32 v226, v200
	s_nop 0
	v_add_f32_e32 v227, 1.0, v226
	v_mfma_f32_16x16x32_f16 v[218:221], v[10:13], v[166:169], v[218:221]
	v_fma_f32 v227, v229, v227, v227
	v_rcp_f32_e32 v227, v227
	v_mfma_f32_16x16x32_f16 v[218:221], v[26:29], v[170:173], v[218:221]
	v_fma_mixlo_f16 v246, -v226, v227, v227
	v_exp_f32_e32 v231, v214
	v_mfma_f32_16x16x32_f16 v[222:225], v[2:5], v[158:161], v[222:225]
	v_exp_f32_e32 v232, v215
	v_min_f32_e32 v233, s42, v216
	v_mfma_f32_16x16x32_f16 v[222:225], v[6:9], v[162:165], v[222:225]
	v_exp_f32_e32 v234, v217
	v_exp_f32_e32 v233, v233
	v_mfma_f32_16x16x32_f16 v[222:225], v[22:25], v[166:169], v[222:225]
	v_exp_f32_e32 v236, v218
	v_add_f32_e32 v232, 1.0, v232
	v_mfma_f32_16x16x32_f16 v[222:225], v[30:33], v[170:173], v[222:225]
	v_fma_f32 v235, v233, s41, s41
	v_exp_f32_e32 v227, v219
	v_rcp_f32_e32 v232, v232
	v_fma_f32 v235, v231, v235, v235
	v_min_f32_e32 v228, s42, v220
	v_rcp_f32_e32 v235, v235
	s_nop 0
	v_fma_f32 v231, -v233, v235, v235
	v_exp_f32_e32 v229, v221
	v_fma_f32 v201, v201, v232, v231
	v_exp_f32_e32 v231, v201
	v_exp_f32_e32 v228, v228
	v_add_f32_e32 v232, 1.0, v231
	v_fma_f32 v232, v234, v232, v232
	v_add_f32_e32 v227, 1.0, v227
	v_rcp_f32_e32 v232, v232
	v_mfma_f32_16x16x32_f16 v[146:149], v[130:133], v[158:161], v[146:149]
	v_fma_mixhi_f16 v246, -v231, v232, v232
	v_fma_f32 v230, v228, s41, s41
	v_exp_f32_e32 v231, v222
	v_mfma_f32_16x16x32_f16 v[146:149], v[134:137], v[162:165], v[146:149]
	v_exp_f32_e32 v232, v223
	v_rcp_f32_e32 v227, v227
	v_min_f32_e32 v233, s42, v224
	buffer_load_dwordx4 v[130:133], v189, s[72:75], s46 offen
	buffer_load_dwordx4 v[134:137], v208, s[72:75], s46 offen
	v_exp_f32_e32 v234, v225
	v_fma_f32 v230, v236, v230, v230
	v_exp_f32_e32 v233, v233
	s_waitcnt lgkmcnt(0)
	v_mfma_f32_16x16x32_f16 v[210:213], v[70:73], v[150:153], v[98:101]
	v_add_f32_e32 v232, 1.0, v232
	v_rcp_f32_e32 v230, v230
	v_fma_f32 v235, v233, s41, s41
	v_mfma_f32_16x16x32_f16 v[214:217], v[74:77], v[150:153], v[102:105]
	v_rcp_f32_e32 v232, v232
	v_fma_f32 v236, -v228, v230, v230
	v_fma_f32 v235, v231, v235, v235
	v_rcp_f32_e32 v235, v235
	v_fma_f32 v198, v198, v227, v236
	v_fma_f32 v231, -v233, v235, v235
	v_fma_f32 v199, v199, v232, v231
	v_exp_f32_e32 v236, v198
	v_exp_f32_e32 v231, v199
	s_nop 0
	v_add_f32_e32 v232, 1.0, v231
	v_add_f32_e32 v227, 1.0, v236
	v_fma_f32 v232, v234, v232, v232
	v_rcp_f32_e32 v232, v232
	v_fma_f32 v227, v229, v227, v227
	v_fma_mixhi_f16 v247, -v231, v232, v232
	v_rcp_f32_e32 v227, v227
	s_nop 0
	v_fma_mixlo_f16 v247, -v236, v227, v227
	ds_write_b64 v250, v[246:247] offset:24576
	v_mfma_f32_16x16x32_f16 v[210:213], v[66:69], v[154:157], v[210:213]
	v_mfma_f32_16x16x32_f16 v[214:217], v[78:81], v[154:157], v[214:217]
	buffer_load_dwordx2 v[194:195], v209, s[52:55], s45 offen
	v_add_u32_e32 v250, 0x4000, v250
	v_add_u32_e32 v248, 0x4000, v248
	v_add_u32_e32 v249, 0x4000, v249
	s_waitcnt lgkmcnt(0)
	s_barrier
	s_cmp_lt_u32 s46, 0xa0000
	s_cbranch_scc1 .Lmy_loopb
	ds_read_b128 v[158:161], v248 offset:0
	ds_read_b128 v[162:165], v248 offset:1024
	ds_read_b128 v[166:169], v249 offset:2048
	ds_read_b128 v[170:173], v249 offset:3072
	v_mfma_f32_16x16x32_f16 v[218:221], v[82:85], v[150:153], v[106:109]
	v_mfma_f32_16x16x32_f16 v[222:225], v[90:93], v[150:153], v[110:113]
	v_mfma_f32_16x16x32_f16 v[218:221], v[86:89], v[154:157], v[218:221]
	v_mfma_f32_16x16x32_f16 v[222:225], v[94:97], v[154:157], v[222:225]
	s_waitcnt lgkmcnt(2)
	v_mfma_f32_16x16x32_f16 v[210:213], v[54:57], v[158:161], v[210:213]
	v_mfma_f32_16x16x32_f16 v[210:213], v[58:61], v[162:165], v[210:213]
	s_waitcnt lgkmcnt(0)
	v_mfma_f32_16x16x32_f16 v[210:213], v[62:65], v[166:169], v[210:213]
	v_mfma_f32_16x16x32_f16 v[210:213], v[50:53], v[170:173], v[210:213]
	s_waitcnt vmcnt(9)
	v_cvt_pk_f16_f32 v251, v192, v193
	ds_write_b32 v1, v251 offset:0
	ds_read_b128 v[150:153], v186 offset:6144
	ds_read_b128 v[154:157], v186 offset:7168
	s_nop 2
	v_exp_f32_e32 v226, v210
	v_exp_f32_e32 v227, v211
	v_mfma_f32_16x16x32_f16 v[214:217], v[34:37], v[158:161], v[214:217]
	v_min_f32_e32 v228, s42, v212
	v_exp_f32_e32 v229, v213
	v_mfma_f32_16x16x32_f16 v[214:217], v[38:41], v[162:165], v[214:217]
	v_exp_f32_e32 v228, v228
	v_add_f32_e32 v227, 1.0, v227
	v_mfma_f32_16x16x32_f16 v[214:217], v[42:45], v[166:169], v[214:217]
	v_fma_f32 v230, v228, s41, s41
	v_rcp_f32_e32 v227, v227
	v_mfma_f32_16x16x32_f16 v[214:217], v[46:49], v[170:173], v[214:217]
	v_fma_f32 v230, v226, v230, v230
	v_rcp_f32_e32 v230, v230
	v_mfma_f32_16x16x32_f16 v[218:221], v[18:21], v[158:161], v[218:221]
	v_fma_f32 v226, -v228, v230, v230
	v_fma_f32 v200, v200, v227, v226
	v_mfma_f32_16x16x32_f16 v[218:221], v[14:17], v[162:165], v[218:221]
	v_min_f32_e32 v226, s42, v200
	v_exp_f32_e32 v226, v226
	v_mfma_f32_16x16x32_f16 v[218:221], v[10:13], v[166:169], v[218:221]
	v_add_f32_e32 v227, 1.0, v226
	v_fma_f32 v227, v229, v227, v227
	v_mfma_f32_16x16x32_f16 v[218:221], v[26:29], v[170:173], v[218:221]
	v_rcp_f32_e32 v227, v227
	v_exp_f32_e32 v231, v214
	v_mfma_f32_16x16x32_f16 v[222:225], v[2:5], v[158:161], v[222:225]
	v_exp_f32_e32 v232, v215
	v_fma_mixlo_f16 v246, -v226, v227, v227
	v_mfma_f32_16x16x32_f16 v[222:225], v[6:9], v[162:165], v[222:225]
	v_min_f32_e32 v233, s42, v216
	v_exp_f32_e32 v234, v217
	v_mfma_f32_16x16x32_f16 v[222:225], v[22:25], v[166:169], v[222:225]
	v_exp_f32_e32 v236, v218
	v_exp_f32_e32 v233, v233
	v_mfma_f32_16x16x32_f16 v[222:225], v[30:33], v[170:173], v[222:225]
	v_add_f32_e32 v232, 1.0, v232
	v_exp_f32_e32 v227, v219
	v_fma_f32 v235, v233, s41, s41
	v_rcp_f32_e32 v232, v232
	v_min_f32_e32 v228, s42, v220
	v_fma_f32 v235, v231, v235, v235
	v_rcp_f32_e32 v235, v235
	v_exp_f32_e32 v229, v221
	v_fma_f32 v231, -v233, v235, v235
	v_fma_f32 v201, v201, v232, v231
	v_exp_f32_e32 v228, v228
	v_min_f32_e32 v231, s42, v201
	v_exp_f32_e32 v231, v231
	v_add_f32_e32 v227, 1.0, v227
	v_add_f32_e32 v232, 1.0, v231
	v_mfma_f32_16x16x32_f16 v[146:149], v[122:125], v[158:161], v[146:149]
	v_fma_f32 v232, v234, v232, v232
	v_fma_f32 v230, v228, s41, s41
	v_rcp_f32_e32 v232, v232
	v_mfma_f32_16x16x32_f16 v[146:149], v[126:129], v[162:165], v[146:149]
	v_fma_mixhi_f16 v246, -v231, v232, v232
	v_rcp_f32_e32 v227, v227
	v_exp_f32_e32 v231, v222
	buffer_load_dwordx4 v[122:125], v189, s[76:79], s46 offen
	buffer_load_dwordx4 v[126:129], v208, s[76:79], s46 offen
	v_exp_f32_e32 v232, v223
	v_fma_f32 v230, v236, v230, v230
	v_min_f32_e32 v233, s42, v224
	s_waitcnt lgkmcnt(0)
	v_mfma_f32_16x16x32_f16 v[210:213], v[70:73], v[150:153], v[98:101]
	v_exp_f32_e32 v234, v225
	v_rcp_f32_e32 v230, v230
	v_exp_f32_e32 v233, v233
	v_mfma_f32_16x16x32_f16 v[214:217], v[74:77], v[150:153], v[102:105]
	v_add_f32_e32 v232, 1.0, v232
	v_fma_f32 v236, -v228, v230, v230
	v_fma_f32 v235, v233, s41, s41
	v_rcp_f32_e32 v232, v232
	v_fma_f32 v198, v198, v227, v236
	v_fma_f32 v235, v231, v235, v235
	v_rcp_f32_e32 v235, v235
	v_min_f32_e32 v236, s42, v198
	v_fma_f32 v231, -v233, v235, v235
	v_fma_f32 v199, v199, v232, v231
	v_exp_f32_e32 v236, v236
	v_min_f32_e32 v231, s42, v199
	v_exp_f32_e32 v231, v231
	v_add_f32_e32 v227, 1.0, v236
	v_add_f32_e32 v232, 1.0, v231
	v_fma_f32 v227, v229, v227, v227
	v_fma_f32 v232, v234, v232, v232
	v_rcp_f32_e32 v227, v227
	v_rcp_f32_e32 v232, v232
	v_fma_mixlo_f16 v247, -v236, v227, v227
	v_fma_mixhi_f16 v247, -v231, v232, v232
	ds_write_b64 v250, v[246:247] offset:12288
	v_mfma_f32_16x16x32_f16 v[210:213], v[66:69], v[154:157], v[210:213]
	v_mfma_f32_16x16x32_f16 v[214:217], v[78:81], v[154:157], v[214:217]
	buffer_load_dwordx2 v[192:193], v209, s[56:59], s45 offen
	s_waitcnt lgkmcnt(0)
	s_barrier
	ds_read_b128 v[158:161], v248 offset:4096
	ds_read_b128 v[162:165], v248 offset:5120
	ds_read_b128 v[166:169], v249 offset:6144
	ds_read_b128 v[170:173], v249 offset:7168
	v_mfma_f32_16x16x32_f16 v[218:221], v[82:85], v[150:153], v[106:109]
	v_mfma_f32_16x16x32_f16 v[222:225], v[90:93], v[150:153], v[110:113]
	v_mfma_f32_16x16x32_f16 v[218:221], v[86:89], v[154:157], v[218:221]
	v_mfma_f32_16x16x32_f16 v[222:225], v[94:97], v[154:157], v[222:225]
	s_waitcnt lgkmcnt(2)
	v_mfma_f32_16x16x32_f16 v[210:213], v[54:57], v[158:161], v[210:213]
	v_mfma_f32_16x16x32_f16 v[210:213], v[58:61], v[162:165], v[210:213]
	s_waitcnt lgkmcnt(0)
	v_mfma_f32_16x16x32_f16 v[210:213], v[62:65], v[166:169], v[210:213]
	v_mfma_f32_16x16x32_f16 v[210:213], v[50:53], v[170:173], v[210:213]
	s_waitcnt vmcnt(9)
	v_cvt_pk_f16_f32 v251, v190, v191
	ds_write_b32 v1, v251 offset:2048
	ds_read_b128 v[150:153], v186 offset:0
	ds_read_b128 v[154:157], v186 offset:1024
	s_nop 2
	v_exp_f32_e32 v226, v210
	v_exp_f32_e32 v227, v211
	v_mfma_f32_16x16x32_f16 v[214:217], v[34:37], v[158:161], v[214:217]
	v_min_f32_e32 v228, s42, v212
	v_exp_f32_e32 v229, v213
	v_mfma_f32_16x16x32_f16 v[214:217], v[38:41], v[162:165], v[214:217]
	v_exp_f32_e32 v228, v228
	v_add_f32_e32 v227, 1.0, v227
	v_mfma_f32_16x16x32_f16 v[214:217], v[42:45], v[166:169], v[214:217]
	v_fma_f32 v230, v228, s41, s41
	v_rcp_f32_e32 v227, v227
	v_mfma_f32_16x16x32_f16 v[214:217], v[46:49], v[170:173], v[214:217]
	v_fma_f32 v230, v226, v230, v230
	v_rcp_f32_e32 v230, v230
	v_mfma_f32_16x16x32_f16 v[218:221], v[18:21], v[158:161], v[218:221]
	v_fma_f32 v226, -v228, v230, v230
	v_fma_f32 v200, v200, v227, v226
	v_mfma_f32_16x16x32_f16 v[218:221], v[14:17], v[162:165], v[218:221]
	v_min_f32_e32 v226, s42, v200
	v_exp_f32_e32 v226, v226
	v_mfma_f32_16x16x32_f16 v[218:221], v[10:13], v[166:169], v[218:221]
	v_add_f32_e32 v227, 1.0, v226
	v_fma_f32 v227, v229, v227, v227
	v_mfma_f32_16x16x32_f16 v[218:221], v[26:29], v[170:173], v[218:221]
	v_rcp_f32_e32 v227, v227
	v_exp_f32_e32 v231, v214
	v_mfma_f32_16x16x32_f16 v[222:225], v[2:5], v[158:161], v[222:225]
	v_exp_f32_e32 v232, v215
	v_fma_mixlo_f16 v246, -v226, v227, v227
	v_mfma_f32_16x16x32_f16 v[222:225], v[6:9], v[162:165], v[222:225]
	v_min_f32_e32 v233, s42, v216
	v_exp_f32_e32 v234, v217
	v_mfma_f32_16x16x32_f16 v[222:225], v[22:25], v[166:169], v[222:225]
	v_exp_f32_e32 v236, v218
	v_exp_f32_e32 v233, v233
	v_mfma_f32_16x16x32_f16 v[222:225], v[30:33], v[170:173], v[222:225]
	v_add_f32_e32 v232, 1.0, v232
	v_exp_f32_e32 v227, v219
	v_fma_f32 v235, v233, s41, s41
	v_rcp_f32_e32 v232, v232
	v_min_f32_e32 v228, s42, v220
	v_fma_f32 v235, v231, v235, v235
	v_rcp_f32_e32 v235, v235
	v_exp_f32_e32 v229, v221
	v_fma_f32 v231, -v233, v235, v235
	v_fma_f32 v201, v201, v232, v231
	v_exp_f32_e32 v228, v228
	v_min_f32_e32 v231, s42, v201
	v_exp_f32_e32 v231, v231
	v_add_f32_e32 v227, 1.0, v227
	v_add_f32_e32 v232, 1.0, v231
	v_mfma_f32_16x16x32_f16 v[146:149], v[114:117], v[158:161], v[146:149]
	v_fma_f32 v232, v234, v232, v232
	v_fma_f32 v230, v228, s41, s41
	v_rcp_f32_e32 v232, v232
	v_mfma_f32_16x16x32_f16 v[146:149], v[118:121], v[162:165], v[146:149]
	v_fma_mixhi_f16 v246, -v231, v232, v232
	v_rcp_f32_e32 v227, v227
	v_exp_f32_e32 v231, v222
	buffer_load_dwordx4 v[114:117], v189, s[80:83], s46 offen
	buffer_load_dwordx4 v[118:121], v208, s[80:83], s46 offen
	v_exp_f32_e32 v232, v223
	v_fma_f32 v230, v236, v230, v230
	v_min_f32_e32 v233, s42, v224
	s_waitcnt lgkmcnt(0)
	v_mfma_f32_16x16x32_f16 v[210:213], v[70:73], v[150:153], v[98:101]
	v_exp_f32_e32 v234, v225
	v_rcp_f32_e32 v230, v230
	v_exp_f32_e32 v233, v233
	v_mfma_f32_16x16x32_f16 v[214:217], v[74:77], v[150:153], v[102:105]
	v_add_f32_e32 v232, 1.0, v232
	v_fma_f32 v236, -v228, v230, v230
	v_fma_f32 v235, v233, s41, s41
	v_rcp_f32_e32 v232, v232
	v_fma_f32 v198, v198, v227, v236
	v_fma_f32 v235, v231, v235, v235
	v_rcp_f32_e32 v235, v235
	v_min_f32_e32 v236, s42, v198
	v_fma_f32 v231, -v233, v235, v235
	v_fma_f32 v199, v199, v232, v231
	v_exp_f32_e32 v236, v236
	v_min_f32_e32 v231, s42, v199
	v_exp_f32_e32 v231, v231
	v_add_f32_e32 v227, 1.0, v236
	v_add_f32_e32 v232, 1.0, v231
	v_fma_f32 v227, v229, v227, v227
	v_fma_f32 v232, v234, v232, v232
	v_rcp_f32_e32 v227, v227
	v_rcp_f32_e32 v232, v232
	v_fma_mixlo_f16 v247, -v236, v227, v227
	v_fma_mixhi_f16 v247, -v231, v232, v232
	ds_write_b64 v250, v[246:247] offset:16384
	v_mfma_f32_16x16x32_f16 v[210:213], v[66:69], v[154:157], v[210:213]
	v_mfma_f32_16x16x32_f16 v[214:217], v[78:81], v[154:157], v[214:217]
	buffer_load_dwordx2 v[190:191], v209, s[60:63], s45 offen
	s_add_i32 s45, s45, 0x400000
	s_add_i32 s46, s46, 0x10000
	s_waitcnt lgkmcnt(0)
	s_barrier
	ds_read_b128 v[158:161], v248 offset:8192
	ds_read_b128 v[162:165], v248 offset:9216
	ds_read_b128 v[166:169], v249 offset:10240
	ds_read_b128 v[170:173], v249 offset:11264
	v_mfma_f32_16x16x32_f16 v[218:221], v[82:85], v[150:153], v[106:109]
	v_mfma_f32_16x16x32_f16 v[222:225], v[90:93], v[150:153], v[110:113]
	v_mfma_f32_16x16x32_f16 v[218:221], v[86:89], v[154:157], v[218:221]
	v_mfma_f32_16x16x32_f16 v[222:225], v[94:97], v[154:157], v[222:225]
	s_waitcnt lgkmcnt(2)
	v_mfma_f32_16x16x32_f16 v[210:213], v[54:57], v[158:161], v[210:213]
	v_mfma_f32_16x16x32_f16 v[210:213], v[58:61], v[162:165], v[210:213]
	s_waitcnt lgkmcnt(0)
	v_mfma_f32_16x16x32_f16 v[210:213], v[62:65], v[166:169], v[210:213]
	v_mfma_f32_16x16x32_f16 v[210:213], v[50:53], v[170:173], v[210:213]
	s_waitcnt vmcnt(9)
	v_cvt_pk_f16_f32 v251, v196, v197
	ds_write_b32 v1, v251 offset:4096
	ds_read_b128 v[150:153], v186 offset:2048
	ds_read_b128 v[154:157], v186 offset:3072
	s_nop 2
	v_exp_f32_e32 v226, v210
	v_exp_f32_e32 v227, v211
	v_mfma_f32_16x16x32_f16 v[214:217], v[34:37], v[158:161], v[214:217]
	v_min_f32_e32 v228, s42, v212
	v_exp_f32_e32 v229, v213
	v_mfma_f32_16x16x32_f16 v[214:217], v[38:41], v[162:165], v[214:217]
	v_exp_f32_e32 v228, v228
	v_add_f32_e32 v227, 1.0, v227
	v_mfma_f32_16x16x32_f16 v[214:217], v[42:45], v[166:169], v[214:217]
	v_fma_f32 v230, v228, s41, s41
	v_rcp_f32_e32 v227, v227
	v_mfma_f32_16x16x32_f16 v[214:217], v[46:49], v[170:173], v[214:217]
	v_fma_f32 v230, v226, v230, v230
	v_rcp_f32_e32 v230, v230
	v_mfma_f32_16x16x32_f16 v[218:221], v[18:21], v[158:161], v[218:221]
	v_fma_f32 v226, -v228, v230, v230
	v_fma_f32 v200, v200, v227, v226
	v_mfma_f32_16x16x32_f16 v[218:221], v[14:17], v[162:165], v[218:221]
	v_min_f32_e32 v226, s42, v200
	v_exp_f32_e32 v226, v226
	v_mfma_f32_16x16x32_f16 v[218:221], v[10:13], v[166:169], v[218:221]
	v_add_f32_e32 v227, 1.0, v226
	v_fma_f32 v227, v229, v227, v227
	v_mfma_f32_16x16x32_f16 v[218:221], v[26:29], v[170:173], v[218:221]
	v_rcp_f32_e32 v227, v227
	v_exp_f32_e32 v231, v214
	v_mfma_f32_16x16x32_f16 v[222:225], v[2:5], v[158:161], v[222:225]
	v_exp_f32_e32 v232, v215
	v_fma_mixlo_f16 v246, -v226, v227, v227
	v_mfma_f32_16x16x32_f16 v[222:225], v[6:9], v[162:165], v[222:225]
	v_min_f32_e32 v233, s42, v216
	v_exp_f32_e32 v234, v217
	v_mfma_f32_16x16x32_f16 v[222:225], v[22:25], v[166:169], v[222:225]
	v_exp_f32_e32 v236, v218
	v_exp_f32_e32 v233, v233
	v_mfma_f32_16x16x32_f16 v[222:225], v[30:33], v[170:173], v[222:225]
	v_add_f32_e32 v232, 1.0, v232
	v_exp_f32_e32 v227, v219
	v_fma_f32 v235, v233, s41, s41
	v_rcp_f32_e32 v232, v232
	v_min_f32_e32 v228, s42, v220
	v_fma_f32 v235, v231, v235, v235
	v_rcp_f32_e32 v235, v235
	v_exp_f32_e32 v229, v221
	v_fma_f32 v231, -v233, v235, v235
	v_fma_f32 v201, v201, v232, v231
	v_exp_f32_e32 v228, v228
	v_min_f32_e32 v231, s42, v201
	v_exp_f32_e32 v231, v231
	v_add_f32_e32 v227, 1.0, v227
	v_add_f32_e32 v232, 1.0, v231
	v_mfma_f32_16x16x32_f16 v[146:149], v[138:141], v[158:161], v[146:149]
	v_fma_f32 v232, v234, v232, v232
	v_fma_f32 v230, v228, s41, s41
	v_rcp_f32_e32 v232, v232
	v_mfma_f32_16x16x32_f16 v[146:149], v[142:145], v[162:165], v[146:149]
	v_fma_mixhi_f16 v246, -v231, v232, v232
	v_rcp_f32_e32 v227, v227
	v_exp_f32_e32 v231, v222
	buffer_load_dwordx4 v[138:141], v189, s[68:71], s46 offen
	buffer_load_dwordx4 v[142:145], v208, s[68:71], s46 offen
	v_exp_f32_e32 v232, v223
	v_fma_f32 v230, v236, v230, v230
	v_min_f32_e32 v233, s42, v224
	s_waitcnt lgkmcnt(0)
	v_mfma_f32_16x16x32_f16 v[210:213], v[70:73], v[150:153], v[98:101]
	v_exp_f32_e32 v234, v225
	v_rcp_f32_e32 v230, v230
	v_exp_f32_e32 v233, v233
	v_mfma_f32_16x16x32_f16 v[214:217], v[74:77], v[150:153], v[102:105]
	v_add_f32_e32 v232, 1.0, v232
	v_fma_f32 v236, -v228, v230, v230
	v_fma_f32 v235, v233, s41, s41
	v_rcp_f32_e32 v232, v232
	v_fma_f32 v198, v198, v227, v236
	v_fma_f32 v235, v231, v235, v235
	v_rcp_f32_e32 v235, v235
	v_min_f32_e32 v236, s42, v198
	v_fma_f32 v231, -v233, v235, v235
	v_fma_f32 v199, v199, v232, v231
	v_exp_f32_e32 v236, v236
	v_min_f32_e32 v231, s42, v199
	v_exp_f32_e32 v231, v231
	v_add_f32_e32 v227, 1.0, v236
	v_add_f32_e32 v232, 1.0, v231
	v_fma_f32 v227, v229, v227, v227
	v_fma_f32 v232, v234, v232, v232
	v_rcp_f32_e32 v227, v227
	v_rcp_f32_e32 v232, v232
	v_fma_mixlo_f16 v247, -v236, v227, v227
	v_fma_mixhi_f16 v247, -v231, v232, v232
	ds_write_b64 v250, v[246:247] offset:20480
	v_mfma_f32_16x16x32_f16 v[210:213], v[66:69], v[154:157], v[210:213]
	v_mfma_f32_16x16x32_f16 v[214:217], v[78:81], v[154:157], v[214:217]
	buffer_load_dwordx2 v[196:197], v209, s[48:51], s45 offen
	s_waitcnt lgkmcnt(0)
	s_barrier
	ds_read_b128 v[158:161], v248 offset:12288
	ds_read_b128 v[162:165], v248 offset:13312
	ds_read_b128 v[166:169], v249 offset:14336
	ds_read_b128 v[170:173], v249 offset:15360
	v_mfma_f32_16x16x32_f16 v[218:221], v[82:85], v[150:153], v[106:109]
	v_mfma_f32_16x16x32_f16 v[222:225], v[90:93], v[150:153], v[110:113]
	v_mfma_f32_16x16x32_f16 v[218:221], v[86:89], v[154:157], v[218:221]
	v_mfma_f32_16x16x32_f16 v[222:225], v[94:97], v[154:157], v[222:225]
	s_waitcnt lgkmcnt(2)
	v_mfma_f32_16x16x32_f16 v[210:213], v[54:57], v[158:161], v[210:213]
	v_mfma_f32_16x16x32_f16 v[210:213], v[58:61], v[162:165], v[210:213]
	s_waitcnt lgkmcnt(0)
	v_mfma_f32_16x16x32_f16 v[210:213], v[62:65], v[166:169], v[210:213]
	v_mfma_f32_16x16x32_f16 v[210:213], v[50:53], v[170:173], v[210:213]
	s_waitcnt vmcnt(9)
	v_cvt_pk_f16_f32 v251, v194, v195
	ds_write_b32 v1, v251 offset:6144
	ds_read_b128 v[150:153], v186 offset:4096
	ds_read_b128 v[154:157], v186 offset:5120
	s_nop 2
	v_exp_f32_e32 v226, v210
	v_exp_f32_e32 v227, v211
	v_mfma_f32_16x16x32_f16 v[214:217], v[34:37], v[158:161], v[214:217]
	v_min_f32_e32 v228, s42, v212
	v_exp_f32_e32 v229, v213
	v_mfma_f32_16x16x32_f16 v[214:217], v[38:41], v[162:165], v[214:217]
	v_exp_f32_e32 v228, v228
	v_add_f32_e32 v227, 1.0, v227
	v_mfma_f32_16x16x32_f16 v[214:217], v[42:45], v[166:169], v[214:217]
	v_fma_f32 v230, v228, s41, s41
	v_rcp_f32_e32 v227, v227
	v_mfma_f32_16x16x32_f16 v[214:217], v[46:49], v[170:173], v[214:217]
	v_fma_f32 v230, v226, v230, v230
	v_rcp_f32_e32 v230, v230
	v_mfma_f32_16x16x32_f16 v[218:221], v[18:21], v[158:161], v[218:221]
	v_fma_f32 v226, -v228, v230, v230
	v_fma_f32 v200, v200, v227, v226
	v_mfma_f32_16x16x32_f16 v[218:221], v[14:17], v[162:165], v[218:221]
	v_min_f32_e32 v226, s42, v200
	v_exp_f32_e32 v226, v226
	v_mfma_f32_16x16x32_f16 v[218:221], v[10:13], v[166:169], v[218:221]
	v_add_f32_e32 v227, 1.0, v226
	v_fma_f32 v227, v229, v227, v227
	v_mfma_f32_16x16x32_f16 v[218:221], v[26:29], v[170:173], v[218:221]
	v_rcp_f32_e32 v227, v227
	v_exp_f32_e32 v231, v214
	v_mfma_f32_16x16x32_f16 v[222:225], v[2:5], v[158:161], v[222:225]
	v_exp_f32_e32 v232, v215
	v_fma_mixlo_f16 v246, -v226, v227, v227
	v_mfma_f32_16x16x32_f16 v[222:225], v[6:9], v[162:165], v[222:225]
	v_min_f32_e32 v233, s42, v216
	v_exp_f32_e32 v234, v217
	v_mfma_f32_16x16x32_f16 v[222:225], v[22:25], v[166:169], v[222:225]
	v_exp_f32_e32 v236, v218
	v_exp_f32_e32 v233, v233
	v_mfma_f32_16x16x32_f16 v[222:225], v[30:33], v[170:173], v[222:225]
	v_add_f32_e32 v232, 1.0, v232
	v_exp_f32_e32 v227, v219
	v_fma_f32 v235, v233, s41, s41
	v_rcp_f32_e32 v232, v232
	v_min_f32_e32 v228, s42, v220
	v_fma_f32 v235, v231, v235, v235
	v_rcp_f32_e32 v235, v235
	v_exp_f32_e32 v229, v221
	v_fma_f32 v231, -v233, v235, v235
	v_fma_f32 v201, v201, v232, v231
	v_exp_f32_e32 v228, v228
	v_min_f32_e32 v231, s42, v201
	v_exp_f32_e32 v231, v231
	v_add_f32_e32 v227, 1.0, v227
	v_add_f32_e32 v232, 1.0, v231
	v_mfma_f32_16x16x32_f16 v[146:149], v[130:133], v[158:161], v[146:149]
	v_fma_f32 v232, v234, v232, v232
	v_fma_f32 v230, v228, s41, s41
	v_rcp_f32_e32 v232, v232
	v_mfma_f32_16x16x32_f16 v[146:149], v[134:137], v[162:165], v[146:149]
	v_fma_mixhi_f16 v246, -v231, v232, v232
	v_rcp_f32_e32 v227, v227
	v_exp_f32_e32 v231, v222
	buffer_load_dwordx4 v[130:133], v189, s[72:75], s46 offen
	buffer_load_dwordx4 v[134:137], v208, s[72:75], s46 offen
	v_exp_f32_e32 v232, v223
	v_fma_f32 v230, v236, v230, v230
	v_min_f32_e32 v233, s42, v224
	s_waitcnt lgkmcnt(0)
	v_mfma_f32_16x16x32_f16 v[210:213], v[70:73], v[150:153], v[98:101]
	v_exp_f32_e32 v234, v225
	v_rcp_f32_e32 v230, v230
	v_exp_f32_e32 v233, v233
	v_mfma_f32_16x16x32_f16 v[214:217], v[74:77], v[150:153], v[102:105]
	v_add_f32_e32 v232, 1.0, v232
	v_fma_f32 v236, -v228, v230, v230
	v_fma_f32 v235, v233, s41, s41
	v_rcp_f32_e32 v232, v232
	v_fma_f32 v198, v198, v227, v236
	v_fma_f32 v235, v231, v235, v235
	v_rcp_f32_e32 v235, v235
	v_min_f32_e32 v236, s42, v198
	v_fma_f32 v231, -v233, v235, v235
	v_fma_f32 v199, v199, v232, v231
	v_exp_f32_e32 v236, v236
	v_min_f32_e32 v231, s42, v199
	v_exp_f32_e32 v231, v231
	v_add_f32_e32 v227, 1.0, v236
	v_add_f32_e32 v232, 1.0, v231
	v_fma_f32 v227, v229, v227, v227
	v_fma_f32 v232, v234, v232, v232
	v_rcp_f32_e32 v227, v227
	v_rcp_f32_e32 v232, v232
	v_fma_mixlo_f16 v247, -v236, v227, v227
	v_fma_mixhi_f16 v247, -v231, v232, v232
	ds_write_b64 v250, v[246:247] offset:24576
	v_mfma_f32_16x16x32_f16 v[210:213], v[66:69], v[154:157], v[210:213]
	v_mfma_f32_16x16x32_f16 v[214:217], v[78:81], v[154:157], v[214:217]
	buffer_load_dwordx2 v[194:195], v209, s[52:55], s45 offen
	v_add_u32_e32 v250, 0x4000, v250
	v_add_u32_e32 v248, 0x4000, v248
	v_add_u32_e32 v249, 0x4000, v249
	s_waitcnt lgkmcnt(0)
	s_barrier
	ds_read_b128 v[158:161], v248 offset:0
	ds_read_b128 v[162:165], v248 offset:1024
	ds_read_b128 v[166:169], v249 offset:2048
	ds_read_b128 v[170:173], v249 offset:3072
	v_mfma_f32_16x16x32_f16 v[218:221], v[82:85], v[150:153], v[106:109]
	v_mfma_f32_16x16x32_f16 v[222:225], v[90:93], v[150:153], v[110:113]
	v_mfma_f32_16x16x32_f16 v[218:221], v[86:89], v[154:157], v[218:221]
	v_mfma_f32_16x16x32_f16 v[222:225], v[94:97], v[154:157], v[222:225]
	s_waitcnt lgkmcnt(2)
	v_mfma_f32_16x16x32_f16 v[210:213], v[54:57], v[158:161], v[210:213]
	v_mfma_f32_16x16x32_f16 v[210:213], v[58:61], v[162:165], v[210:213]
	s_waitcnt lgkmcnt(0)
	v_mfma_f32_16x16x32_f16 v[210:213], v[62:65], v[166:169], v[210:213]
	v_mfma_f32_16x16x32_f16 v[210:213], v[50:53], v[170:173], v[210:213]
	s_waitcnt vmcnt(9)
	v_cvt_pk_f16_f32 v251, v192, v193
	ds_write_b32 v1, v251 offset:0
	ds_read_b128 v[150:153], v186 offset:6144
	ds_read_b128 v[154:157], v186 offset:7168
	s_nop 2
	v_exp_f32_e32 v226, v210
	v_exp_f32_e32 v227, v211
	v_mfma_f32_16x16x32_f16 v[214:217], v[34:37], v[158:161], v[214:217]
	v_min_f32_e32 v228, s42, v212
	v_exp_f32_e32 v229, v213
	v_mfma_f32_16x16x32_f16 v[214:217], v[38:41], v[162:165], v[214:217]
	v_exp_f32_e32 v228, v228
	v_add_f32_e32 v227, 1.0, v227
	v_mfma_f32_16x16x32_f16 v[214:217], v[42:45], v[166:169], v[214:217]
	v_fma_f32 v230, v228, s41, s41
	v_rcp_f32_e32 v227, v227
	v_mfma_f32_16x16x32_f16 v[214:217], v[46:49], v[170:173], v[214:217]
	v_fma_f32 v230, v226, v230, v230
	v_rcp_f32_e32 v230, v230
	v_mfma_f32_16x16x32_f16 v[218:221], v[18:21], v[158:161], v[218:221]
	v_fma_f32 v226, -v228, v230, v230
	v_fma_f32 v200, v200, v227, v226
	v_mfma_f32_16x16x32_f16 v[218:221], v[14:17], v[162:165], v[218:221]
	v_min_f32_e32 v226, s42, v200
	v_exp_f32_e32 v226, v226
	v_mfma_f32_16x16x32_f16 v[218:221], v[10:13], v[166:169], v[218:221]
	v_add_f32_e32 v227, 1.0, v226
	v_fma_f32 v227, v229, v227, v227
	v_mfma_f32_16x16x32_f16 v[218:221], v[26:29], v[170:173], v[218:221]
	v_rcp_f32_e32 v227, v227
	v_exp_f32_e32 v231, v214
	v_mfma_f32_16x16x32_f16 v[222:225], v[2:5], v[158:161], v[222:225]
	v_exp_f32_e32 v232, v215
	v_fma_mixlo_f16 v246, -v226, v227, v227
	v_mfma_f32_16x16x32_f16 v[222:225], v[6:9], v[162:165], v[222:225]
	v_min_f32_e32 v233, s42, v216
	v_exp_f32_e32 v234, v217
	v_mfma_f32_16x16x32_f16 v[222:225], v[22:25], v[166:169], v[222:225]
	v_exp_f32_e32 v236, v218
	v_exp_f32_e32 v233, v233
	v_mfma_f32_16x16x32_f16 v[222:225], v[30:33], v[170:173], v[222:225]
	v_add_f32_e32 v232, 1.0, v232
	v_exp_f32_e32 v227, v219
	v_fma_f32 v235, v233, s41, s41
	v_rcp_f32_e32 v232, v232
	v_min_f32_e32 v228, s42, v220
	v_fma_f32 v235, v231, v235, v235
	v_rcp_f32_e32 v235, v235
	v_exp_f32_e32 v229, v221
	v_fma_f32 v231, -v233, v235, v235
	v_fma_f32 v201, v201, v232, v231
	v_exp_f32_e32 v228, v228
	v_min_f32_e32 v231, s42, v201
	v_exp_f32_e32 v231, v231
	v_add_f32_e32 v227, 1.0, v227
	v_add_f32_e32 v232, 1.0, v231
	v_mfma_f32_16x16x32_f16 v[146:149], v[122:125], v[158:161], v[146:149]
	v_fma_f32 v232, v234, v232, v232
	v_fma_f32 v230, v228, s41, s41
	v_rcp_f32_e32 v232, v232
	v_mfma_f32_16x16x32_f16 v[146:149], v[126:129], v[162:165], v[146:149]
	v_fma_mixhi_f16 v246, -v231, v232, v232
	v_rcp_f32_e32 v227, v227
	v_exp_f32_e32 v231, v222
	buffer_load_dwordx4 v[122:125], v189, s[76:79], s46 offen
	buffer_load_dwordx4 v[126:129], v208, s[76:79], s46 offen
	v_exp_f32_e32 v232, v223
	v_fma_f32 v230, v236, v230, v230
	v_min_f32_e32 v233, s42, v224
	s_waitcnt lgkmcnt(0)
	v_mfma_f32_16x16x32_f16 v[210:213], v[70:73], v[150:153], v[98:101]
	v_exp_f32_e32 v234, v225
	v_rcp_f32_e32 v230, v230
	v_exp_f32_e32 v233, v233
	v_mfma_f32_16x16x32_f16 v[214:217], v[74:77], v[150:153], v[102:105]
	v_add_f32_e32 v232, 1.0, v232
	v_fma_f32 v236, -v228, v230, v230
	v_fma_f32 v235, v233, s41, s41
	v_rcp_f32_e32 v232, v232
	v_fma_f32 v198, v198, v227, v236
	v_fma_f32 v235, v231, v235, v235
	v_rcp_f32_e32 v235, v235
	v_min_f32_e32 v236, s42, v198
	v_fma_f32 v231, -v233, v235, v235
	v_fma_f32 v199, v199, v232, v231
	v_exp_f32_e32 v236, v236
	v_min_f32_e32 v231, s42, v199
	v_exp_f32_e32 v231, v231
	v_add_f32_e32 v227, 1.0, v236
	v_add_f32_e32 v232, 1.0, v231
	v_fma_f32 v227, v229, v227, v227
	v_fma_f32 v232, v234, v232, v232
	v_rcp_f32_e32 v227, v227
	v_rcp_f32_e32 v232, v232
	v_fma_mixlo_f16 v247, -v236, v227, v227
	v_fma_mixhi_f16 v247, -v231, v232, v232
	ds_write_b64 v250, v[246:247] offset:12288
	v_mfma_f32_16x16x32_f16 v[210:213], v[66:69], v[154:157], v[210:213]
	v_mfma_f32_16x16x32_f16 v[214:217], v[78:81], v[154:157], v[214:217]
	buffer_load_dwordx2 v[192:193], v209, s[56:59], s45 offen
	s_waitcnt lgkmcnt(0)
	s_barrier
	ds_read_b128 v[158:161], v248 offset:4096
	ds_read_b128 v[162:165], v248 offset:5120
	ds_read_b128 v[166:169], v249 offset:6144
	ds_read_b128 v[170:173], v249 offset:7168
	v_mfma_f32_16x16x32_f16 v[218:221], v[82:85], v[150:153], v[106:109]
	v_mfma_f32_16x16x32_f16 v[222:225], v[90:93], v[150:153], v[110:113]
	v_mfma_f32_16x16x32_f16 v[218:221], v[86:89], v[154:157], v[218:221]
	v_mfma_f32_16x16x32_f16 v[222:225], v[94:97], v[154:157], v[222:225]
	s_waitcnt lgkmcnt(2)
	v_mfma_f32_16x16x32_f16 v[210:213], v[54:57], v[158:161], v[210:213]
	v_mfma_f32_16x16x32_f16 v[210:213], v[58:61], v[162:165], v[210:213]
	s_waitcnt lgkmcnt(0)
	v_mfma_f32_16x16x32_f16 v[210:213], v[62:65], v[166:169], v[210:213]
	v_mfma_f32_16x16x32_f16 v[210:213], v[50:53], v[170:173], v[210:213]
	s_waitcnt vmcnt(9)
	v_cvt_pk_f16_f32 v251, v190, v191
	ds_write_b32 v1, v251 offset:2048
	ds_read_b128 v[150:153], v186 offset:0
	ds_read_b128 v[154:157], v186 offset:1024
	s_nop 2
	v_exp_f32_e32 v226, v210
	v_exp_f32_e32 v227, v211
	v_mfma_f32_16x16x32_f16 v[214:217], v[34:37], v[158:161], v[214:217]
	v_min_f32_e32 v228, s42, v212
	v_exp_f32_e32 v229, v213
	v_mfma_f32_16x16x32_f16 v[214:217], v[38:41], v[162:165], v[214:217]
	v_exp_f32_e32 v228, v228
	v_add_f32_e32 v227, 1.0, v227
	v_mfma_f32_16x16x32_f16 v[214:217], v[42:45], v[166:169], v[214:217]
	v_fma_f32 v230, v228, s41, s41
	v_rcp_f32_e32 v227, v227
	v_mfma_f32_16x16x32_f16 v[214:217], v[46:49], v[170:173], v[214:217]
	v_fma_f32 v230, v226, v230, v230
	v_rcp_f32_e32 v230, v230
	v_mfma_f32_16x16x32_f16 v[218:221], v[18:21], v[158:161], v[218:221]
	v_fma_f32 v226, -v228, v230, v230
	v_fma_f32 v200, v200, v227, v226
	v_mfma_f32_16x16x32_f16 v[218:221], v[14:17], v[162:165], v[218:221]
	v_min_f32_e32 v226, s42, v200
	v_exp_f32_e32 v226, v226
	v_mfma_f32_16x16x32_f16 v[218:221], v[10:13], v[166:169], v[218:221]
	v_add_f32_e32 v227, 1.0, v226
	v_fma_f32 v227, v229, v227, v227
	v_mfma_f32_16x16x32_f16 v[218:221], v[26:29], v[170:173], v[218:221]
	v_rcp_f32_e32 v227, v227
	v_exp_f32_e32 v231, v214
	v_mfma_f32_16x16x32_f16 v[222:225], v[2:5], v[158:161], v[222:225]
	v_exp_f32_e32 v232, v215
	v_fma_mixlo_f16 v246, -v226, v227, v227
	v_mfma_f32_16x16x32_f16 v[222:225], v[6:9], v[162:165], v[222:225]
	v_min_f32_e32 v233, s42, v216
	v_exp_f32_e32 v234, v217
	v_mfma_f32_16x16x32_f16 v[222:225], v[22:25], v[166:169], v[222:225]
	v_exp_f32_e32 v236, v218
	v_exp_f32_e32 v233, v233
	v_mfma_f32_16x16x32_f16 v[222:225], v[30:33], v[170:173], v[222:225]
	v_add_f32_e32 v232, 1.0, v232
	v_exp_f32_e32 v227, v219
	v_fma_f32 v235, v233, s41, s41
	v_rcp_f32_e32 v232, v232
	v_min_f32_e32 v228, s42, v220
	v_fma_f32 v235, v231, v235, v235
	v_rcp_f32_e32 v235, v235
	v_exp_f32_e32 v229, v221
	v_fma_f32 v231, -v233, v235, v235
	v_fma_f32 v201, v201, v232, v231
	v_exp_f32_e32 v228, v228
	v_min_f32_e32 v231, s42, v201
	v_exp_f32_e32 v231, v231
	v_add_f32_e32 v227, 1.0, v227
	v_add_f32_e32 v232, 1.0, v231
	v_mfma_f32_16x16x32_f16 v[146:149], v[114:117], v[158:161], v[146:149]
	v_fma_f32 v232, v234, v232, v232
	v_fma_f32 v230, v228, s41, s41
	v_rcp_f32_e32 v232, v232
	v_mfma_f32_16x16x32_f16 v[146:149], v[118:121], v[162:165], v[146:149]
	v_fma_mixhi_f16 v246, -v231, v232, v232
	v_rcp_f32_e32 v227, v227
	v_exp_f32_e32 v231, v222
	buffer_load_dwordx4 v[114:117], v189, s[80:83], s46 offen
	buffer_load_dwordx4 v[118:121], v208, s[80:83], s46 offen
	v_exp_f32_e32 v232, v223
	v_fma_f32 v230, v236, v230, v230
	v_min_f32_e32 v233, s42, v224
	s_waitcnt lgkmcnt(0)
	v_mfma_f32_16x16x32_f16 v[210:213], v[70:73], v[150:153], v[98:101]
	v_exp_f32_e32 v234, v225
	v_rcp_f32_e32 v230, v230
	v_exp_f32_e32 v233, v233
	v_mfma_f32_16x16x32_f16 v[214:217], v[74:77], v[150:153], v[102:105]
	v_add_f32_e32 v232, 1.0, v232
	v_fma_f32 v236, -v228, v230, v230
	v_fma_f32 v235, v233, s41, s41
	v_rcp_f32_e32 v232, v232
	v_fma_f32 v198, v198, v227, v236
	v_fma_f32 v235, v231, v235, v235
	v_rcp_f32_e32 v235, v235
	v_min_f32_e32 v236, s42, v198
	v_fma_f32 v231, -v233, v235, v235
	v_fma_f32 v199, v199, v232, v231
	v_exp_f32_e32 v236, v236
	v_min_f32_e32 v231, s42, v199
	v_exp_f32_e32 v231, v231
	v_add_f32_e32 v227, 1.0, v236
	v_add_f32_e32 v232, 1.0, v231
	v_fma_f32 v227, v229, v227, v227
	v_fma_f32 v232, v234, v232, v232
	v_rcp_f32_e32 v227, v227
	v_rcp_f32_e32 v232, v232
	v_fma_mixlo_f16 v247, -v236, v227, v227
	v_fma_mixhi_f16 v247, -v231, v232, v232
	ds_write_b64 v250, v[246:247] offset:16384
	v_mfma_f32_16x16x32_f16 v[210:213], v[66:69], v[154:157], v[210:213]
	v_mfma_f32_16x16x32_f16 v[214:217], v[78:81], v[154:157], v[214:217]
	buffer_load_dwordx2 v[190:191], v209, s[60:63], s45 offen
	s_add_i32 s45, s45, 0x400000
	s_add_i32 s46, s46, 0x10000
	s_waitcnt lgkmcnt(0)
	s_barrier
	ds_read_b128 v[158:161], v248 offset:8192
	ds_read_b128 v[162:165], v248 offset:9216
	ds_read_b128 v[166:169], v249 offset:10240
	ds_read_b128 v[170:173], v249 offset:11264
	v_mfma_f32_16x16x32_f16 v[218:221], v[82:85], v[150:153], v[106:109]
	v_mfma_f32_16x16x32_f16 v[222:225], v[90:93], v[150:153], v[110:113]
	v_mfma_f32_16x16x32_f16 v[218:221], v[86:89], v[154:157], v[218:221]
	v_mfma_f32_16x16x32_f16 v[222:225], v[94:97], v[154:157], v[222:225]
	s_waitcnt lgkmcnt(2)
	v_mfma_f32_16x16x32_f16 v[210:213], v[54:57], v[158:161], v[210:213]
	v_mfma_f32_16x16x32_f16 v[210:213], v[58:61], v[162:165], v[210:213]
	s_waitcnt lgkmcnt(0)
	v_mfma_f32_16x16x32_f16 v[210:213], v[62:65], v[166:169], v[210:213]
	v_mfma_f32_16x16x32_f16 v[210:213], v[50:53], v[170:173], v[210:213]
	s_waitcnt vmcnt(9)
	v_cvt_pk_f16_f32 v251, v196, v197
	ds_write_b32 v1, v251 offset:4096
	ds_read_b128 v[150:153], v186 offset:2048
	ds_read_b128 v[154:157], v186 offset:3072
	s_nop 2
	v_exp_f32_e32 v226, v210
	v_exp_f32_e32 v227, v211
	v_mfma_f32_16x16x32_f16 v[214:217], v[34:37], v[158:161], v[214:217]
	v_min_f32_e32 v228, s42, v212
	v_exp_f32_e32 v229, v213
	v_mfma_f32_16x16x32_f16 v[214:217], v[38:41], v[162:165], v[214:217]
	v_exp_f32_e32 v228, v228
	v_add_f32_e32 v227, 1.0, v227
	v_mfma_f32_16x16x32_f16 v[214:217], v[42:45], v[166:169], v[214:217]
	v_fma_f32 v230, v228, s41, s41
	v_rcp_f32_e32 v227, v227
	v_mfma_f32_16x16x32_f16 v[214:217], v[46:49], v[170:173], v[214:217]
	v_fma_f32 v230, v226, v230, v230
	v_rcp_f32_e32 v230, v230
	v_mfma_f32_16x16x32_f16 v[218:221], v[18:21], v[158:161], v[218:221]
	v_fma_f32 v226, -v228, v230, v230
	v_fma_f32 v200, v200, v227, v226
	v_mfma_f32_16x16x32_f16 v[218:221], v[14:17], v[162:165], v[218:221]
	v_min_f32_e32 v226, s42, v200
	v_exp_f32_e32 v226, v226
	v_mfma_f32_16x16x32_f16 v[218:221], v[10:13], v[166:169], v[218:221]
	v_add_f32_e32 v227, 1.0, v226
	v_fma_f32 v227, v229, v227, v227
	v_mfma_f32_16x16x32_f16 v[218:221], v[26:29], v[170:173], v[218:221]
	v_rcp_f32_e32 v227, v227
	v_exp_f32_e32 v231, v214
	v_mfma_f32_16x16x32_f16 v[222:225], v[2:5], v[158:161], v[222:225]
	v_exp_f32_e32 v232, v215
	v_fma_mixlo_f16 v246, -v226, v227, v227
	v_mfma_f32_16x16x32_f16 v[222:225], v[6:9], v[162:165], v[222:225]
	v_min_f32_e32 v233, s42, v216
	v_exp_f32_e32 v234, v217
	v_mfma_f32_16x16x32_f16 v[222:225], v[22:25], v[166:169], v[222:225]
	v_exp_f32_e32 v236, v218
	v_exp_f32_e32 v233, v233
	v_mfma_f32_16x16x32_f16 v[222:225], v[30:33], v[170:173], v[222:225]
	v_add_f32_e32 v232, 1.0, v232
	v_exp_f32_e32 v227, v219
	v_fma_f32 v235, v233, s41, s41
	v_rcp_f32_e32 v232, v232
	v_min_f32_e32 v228, s42, v220
	v_fma_f32 v235, v231, v235, v235
	v_rcp_f32_e32 v235, v235
	v_exp_f32_e32 v229, v221
	v_fma_f32 v231, -v233, v235, v235
	v_fma_f32 v201, v201, v232, v231
	v_exp_f32_e32 v228, v228
	v_min_f32_e32 v231, s42, v201
	v_exp_f32_e32 v231, v231
	v_add_f32_e32 v227, 1.0, v227
	v_add_f32_e32 v232, 1.0, v231
	v_mfma_f32_16x16x32_f16 v[146:149], v[138:141], v[158:161], v[146:149]
	v_fma_f32 v232, v234, v232, v232
	v_fma_f32 v230, v228, s41, s41
	v_rcp_f32_e32 v232, v232
	v_mfma_f32_16x16x32_f16 v[146:149], v[142:145], v[162:165], v[146:149]
	v_fma_mixhi_f16 v246, -v231, v232, v232
	v_rcp_f32_e32 v227, v227
	v_exp_f32_e32 v231, v222
	buffer_load_dwordx4 v[138:141], v189, s[68:71], s46 offen
	buffer_load_dwordx4 v[142:145], v208, s[68:71], s46 offen
	v_exp_f32_e32 v232, v223
	v_fma_f32 v230, v236, v230, v230
	v_min_f32_e32 v233, s42, v224
	s_waitcnt lgkmcnt(0)
	v_mfma_f32_16x16x32_f16 v[210:213], v[70:73], v[150:153], v[98:101]
	v_exp_f32_e32 v234, v225
	v_rcp_f32_e32 v230, v230
	v_exp_f32_e32 v233, v233
	v_mfma_f32_16x16x32_f16 v[214:217], v[74:77], v[150:153], v[102:105]
	v_add_f32_e32 v232, 1.0, v232
	v_fma_f32 v236, -v228, v230, v230
	v_fma_f32 v235, v233, s41, s41
	v_rcp_f32_e32 v232, v232
	v_fma_f32 v198, v198, v227, v236
	v_fma_f32 v235, v231, v235, v235
	v_rcp_f32_e32 v235, v235
	v_min_f32_e32 v236, s42, v198
	v_fma_f32 v231, -v233, v235, v235
	v_fma_f32 v199, v199, v232, v231
	v_exp_f32_e32 v236, v236
	v_min_f32_e32 v231, s42, v199
	v_exp_f32_e32 v231, v231
	v_add_f32_e32 v227, 1.0, v236
	v_add_f32_e32 v232, 1.0, v231
	v_fma_f32 v227, v229, v227, v227
	v_fma_f32 v232, v234, v232, v232
	v_rcp_f32_e32 v227, v227
	v_rcp_f32_e32 v232, v232
	v_fma_mixlo_f16 v247, -v236, v227, v227
	v_fma_mixhi_f16 v247, -v231, v232, v232
	ds_write_b64 v250, v[246:247] offset:20480
	v_mfma_f32_16x16x32_f16 v[210:213], v[66:69], v[154:157], v[210:213]
	v_mfma_f32_16x16x32_f16 v[214:217], v[78:81], v[154:157], v[214:217]
	buffer_load_dwordx2 v[196:197], v209, s[48:51], s45 offen
	s_waitcnt lgkmcnt(0)
	s_barrier
	ds_read_b128 v[158:161], v248 offset:12288
	ds_read_b128 v[162:165], v248 offset:13312
	ds_read_b128 v[166:169], v249 offset:14336
	ds_read_b128 v[170:173], v249 offset:15360
	v_mfma_f32_16x16x32_f16 v[218:221], v[82:85], v[150:153], v[106:109]
	v_mfma_f32_16x16x32_f16 v[222:225], v[90:93], v[150:153], v[110:113]
	v_mfma_f32_16x16x32_f16 v[218:221], v[86:89], v[154:157], v[218:221]
	v_mfma_f32_16x16x32_f16 v[222:225], v[94:97], v[154:157], v[222:225]
	s_waitcnt lgkmcnt(2)
	v_mfma_f32_16x16x32_f16 v[210:213], v[54:57], v[158:161], v[210:213]
	v_mfma_f32_16x16x32_f16 v[210:213], v[58:61], v[162:165], v[210:213]
	s_waitcnt lgkmcnt(0)
	v_mfma_f32_16x16x32_f16 v[210:213], v[62:65], v[166:169], v[210:213]
	v_mfma_f32_16x16x32_f16 v[210:213], v[50:53], v[170:173], v[210:213]
	s_waitcnt vmcnt(9)
	v_cvt_pk_f16_f32 v251, v194, v195
	ds_write_b32 v1, v251 offset:6144
	ds_read_b128 v[150:153], v186 offset:4096
	ds_read_b128 v[154:157], v186 offset:5120
	s_nop 2
	v_exp_f32_e32 v226, v210
	v_exp_f32_e32 v227, v211
	v_mfma_f32_16x16x32_f16 v[214:217], v[34:37], v[158:161], v[214:217]
	v_min_f32_e32 v228, s42, v212
	v_exp_f32_e32 v229, v213
	v_mfma_f32_16x16x32_f16 v[214:217], v[38:41], v[162:165], v[214:217]
	v_exp_f32_e32 v228, v228
	v_add_f32_e32 v227, 1.0, v227
	v_mfma_f32_16x16x32_f16 v[214:217], v[42:45], v[166:169], v[214:217]
	v_fma_f32 v230, v228, s41, s41
	v_rcp_f32_e32 v227, v227
	v_mfma_f32_16x16x32_f16 v[214:217], v[46:49], v[170:173], v[214:217]
	v_fma_f32 v230, v226, v230, v230
	v_rcp_f32_e32 v230, v230
	v_mfma_f32_16x16x32_f16 v[218:221], v[18:21], v[158:161], v[218:221]
	v_fma_f32 v226, -v228, v230, v230
	v_fma_f32 v200, v200, v227, v226
	v_mfma_f32_16x16x32_f16 v[218:221], v[14:17], v[162:165], v[218:221]
	v_min_f32_e32 v226, s42, v200
	v_exp_f32_e32 v226, v226
	v_mfma_f32_16x16x32_f16 v[218:221], v[10:13], v[166:169], v[218:221]
	v_add_f32_e32 v227, 1.0, v226
	v_fma_f32 v227, v229, v227, v227
	v_mfma_f32_16x16x32_f16 v[218:221], v[26:29], v[170:173], v[218:221]
	v_rcp_f32_e32 v227, v227
	v_exp_f32_e32 v231, v214
	v_mfma_f32_16x16x32_f16 v[222:225], v[2:5], v[158:161], v[222:225]
	v_exp_f32_e32 v232, v215
	v_fma_mixlo_f16 v246, -v226, v227, v227
	v_mfma_f32_16x16x32_f16 v[222:225], v[6:9], v[162:165], v[222:225]
	v_min_f32_e32 v233, s42, v216
	v_exp_f32_e32 v234, v217
	v_mfma_f32_16x16x32_f16 v[222:225], v[22:25], v[166:169], v[222:225]
	v_exp_f32_e32 v236, v218
	v_exp_f32_e32 v233, v233
	v_mfma_f32_16x16x32_f16 v[222:225], v[30:33], v[170:173], v[222:225]
	v_add_f32_e32 v232, 1.0, v232
	v_exp_f32_e32 v227, v219
	v_fma_f32 v235, v233, s41, s41
	v_rcp_f32_e32 v232, v232
	v_min_f32_e32 v228, s42, v220
	v_fma_f32 v235, v231, v235, v235
	v_rcp_f32_e32 v235, v235
	v_exp_f32_e32 v229, v221
	v_fma_f32 v231, -v233, v235, v235
	v_fma_f32 v201, v201, v232, v231
	v_exp_f32_e32 v228, v228
	v_min_f32_e32 v231, s42, v201
	v_exp_f32_e32 v231, v231
	v_add_f32_e32 v227, 1.0, v227
	v_add_f32_e32 v232, 1.0, v231
	v_mfma_f32_16x16x32_f16 v[146:149], v[130:133], v[158:161], v[146:149]
	v_fma_f32 v232, v234, v232, v232
	v_fma_f32 v230, v228, s41, s41
	v_rcp_f32_e32 v232, v232
	v_mfma_f32_16x16x32_f16 v[146:149], v[134:137], v[162:165], v[146:149]
	v_fma_mixhi_f16 v246, -v231, v232, v232
	v_rcp_f32_e32 v227, v227
	v_exp_f32_e32 v231, v222
	buffer_load_dwordx4 v[130:133], v189, s[72:75], s46 offen
	buffer_load_dwordx4 v[134:137], v208, s[72:75], s46 offen
	v_exp_f32_e32 v232, v223
	v_fma_f32 v230, v236, v230, v230
	v_min_f32_e32 v233, s42, v224
	s_waitcnt lgkmcnt(0)
	v_mfma_f32_16x16x32_f16 v[210:213], v[70:73], v[150:153], v[98:101]
	v_exp_f32_e32 v234, v225
	v_rcp_f32_e32 v230, v230
	v_exp_f32_e32 v233, v233
	v_mfma_f32_16x16x32_f16 v[214:217], v[74:77], v[150:153], v[102:105]
	v_add_f32_e32 v232, 1.0, v232
	v_fma_f32 v236, -v228, v230, v230
	v_fma_f32 v235, v233, s41, s41
	v_rcp_f32_e32 v232, v232
	v_fma_f32 v198, v198, v227, v236
	v_fma_f32 v235, v231, v235, v235
	v_rcp_f32_e32 v235, v235
	v_min_f32_e32 v236, s42, v198
	v_fma_f32 v231, -v233, v235, v235
	v_fma_f32 v199, v199, v232, v231
	v_exp_f32_e32 v236, v236
	v_min_f32_e32 v231, s42, v199
	v_exp_f32_e32 v231, v231
	v_add_f32_e32 v227, 1.0, v236
	v_add_f32_e32 v232, 1.0, v231
	v_fma_f32 v227, v229, v227, v227
	v_fma_f32 v232, v234, v232, v232
	v_rcp_f32_e32 v227, v227
	v_rcp_f32_e32 v232, v232
	v_fma_mixlo_f16 v247, -v236, v227, v227
	v_fma_mixhi_f16 v247, -v231, v232, v232
	ds_write_b64 v250, v[246:247] offset:24576
	v_mfma_f32_16x16x32_f16 v[210:213], v[66:69], v[154:157], v[210:213]
	v_mfma_f32_16x16x32_f16 v[214:217], v[78:81], v[154:157], v[214:217]
	buffer_load_dwordx2 v[194:195], v209, s[52:55], s45 offen
	v_add_u32_e32 v250, 0x4000, v250
	v_add_u32_e32 v248, 0x4000, v248
	v_add_u32_e32 v249, 0x4000, v249
	s_waitcnt lgkmcnt(0)
	s_barrier
	s_nop 7
	ds_read_b128 v[158:161], v248 offset:0
	ds_read_b128 v[162:165], v248 offset:1024
	s_lshr_b32 s48, s35, 5
	v_and_b32_e32 v211, 15, v0
	v_bfe_u32 v212, v0, 4, 2
	v_and_b32_e32 v213, 31, v0
	v_bfe_u32 v214, v0, 5, 1
	v_add_u32_e32 v214, s48, v214
	s_lshl_b32 s49, s35, 4
	s_addk_i32 s49, 0x2000
	v_lshl_add_u32 v215, v212, 8, s49
	v_lshl_add_u32 v215, v211, 2, v215
	v_lshlrev_b32_e32 v216, 6, v213
	v_lshl_add_u32 v216, v214, 2, v216
	v_mul_u32_u24_e32 v217, 0x110, v214
	v_lshl_add_u32 v217, v213, 2, v217
	v_mul_u32_u24_e32 v218, 0x110, v211
	v_add_u32_e32 v219, 0x4000, v206
	v_add_u32_e32 v220, 0x14000, v206
	v_add_u32_e32 v221, 0x24000, v206
	v_add_u32_e32 v222, s34, v211
	v_lshlrev_b32_e32 v222, 9, v222
	v_add_u32_e32 v222, s35, v222
	v_lshl_add_u32 v222, v212, 4, v222
	s_waitcnt vmcnt(10) lgkmcnt(0)
	v_mfma_f32_16x16x32_f16 v[146:149], v[122:125], v[158:161], v[146:149]
	v_mfma_f32_16x16x32_f16 v[146:149], v[126:129], v[162:165], v[146:149]
	ds_read_b64 v[30:31], v219 offset:0
	ds_read_b64 v[32:33], v219 offset:4096
	ds_read_b64 v[34:35], v219 offset:8192
	ds_read_b64 v[36:37], v219 offset:12288
	ds_read_b64 v[38:39], v219 offset:16384
	ds_read_b64 v[40:41], v219 offset:20480
	ds_read_b64 v[42:43], v219 offset:24576
	ds_read_b64 v[44:45], v219 offset:28672
	s_waitcnt lgkmcnt(4)
	ds_read_b64 v[46:47], v219 offset:32768
	ds_read_b64 v[48:49], v219 offset:36864
	ds_read_b64 v[50:51], v219 offset:40960
	ds_read_b64 v[52:53], v219 offset:45056
	ds_read_b64 v[54:55], v219 offset:49152
	ds_read_b64 v[56:57], v219 offset:53248
	ds_read_b64 v[58:59], v219 offset:57344
	ds_read_b64 v[60:61], v219 offset:61440
	s_waitcnt lgkmcnt(4)
	ds_read_b64 v[62:63], v220 offset:0
	ds_read_b64 v[64:65], v220 offset:4096
	ds_read_b64 v[66:67], v220 offset:8192
	ds_read_b64 v[68:69], v220 offset:12288
	ds_read_b64 v[70:71], v220 offset:16384
	ds_read_b64 v[72:73], v220 offset:20480
	ds_read_b64 v[74:75], v220 offset:24576
	ds_read_b64 v[76:77], v220 offset:28672
	s_waitcnt lgkmcnt(4)
	ds_read_b64 v[78:79], v220 offset:32768
	ds_read_b64 v[80:81], v220 offset:36864
	ds_read_b64 v[82:83], v220 offset:40960
	ds_read_b64 v[84:85], v220 offset:45056
	ds_read_b64 v[86:87], v220 offset:49152
	ds_read_b64 v[88:89], v220 offset:53248
	ds_read_b64 v[90:91], v220 offset:57344
	ds_read_b64 v[92:93], v220 offset:61440
	s_waitcnt lgkmcnt(4)
	ds_read_b64 v[94:95], v221 offset:0
	ds_read_b64 v[96:97], v221 offset:4096
	ds_read_b64 v[98:99], v221 offset:8192
	ds_read_b64 v[100:101], v221 offset:12288
	ds_write2_b32 v215, v146, v147 offset1:16
	ds_write2_b32 v215, v148, v149 offset0:32 offset1:48
	s_waitcnt lgkmcnt(0)
	s_barrier
	ds_read2st64_b32 v[230:231], v216 offset0:32 offset1:48
	ds_read2st64_b32 v[232:233], v216 offset0:40 offset1:56
	v_cmp_gt_u32_e32 vcc, 18, v213
	s_waitcnt vmcnt(0) lgkmcnt(0)
	v_add_f32_e32 v223, v230, v231
	v_add_f32_e32 v224, v232, v233
	v_add_f32_e32 v223, v223, v254
	v_add_f32_e32 v224, v224, v255
	v_max_f32_e32 v223, 0, v223
	v_max_f32_e32 v224, 0, v224
	v_mov_b32_e32 v226, 0xf149f2ca
	v_cndmask_b32_e32 v224, v226, v224, vcc
	v_max_f32_e32 v225, v223, v224
	s_nop 1
	v_max_f32_dpp v226, v225, v225 quad_perm:[1,0,3,2] row_mask:0xf bank_mask:0xf
	s_nop 1
	v_max_f32_dpp v225, v226, v226 quad_perm:[2,3,0,1] row_mask:0xf bank_mask:0xf
	s_nop 1
	v_max_f32_dpp v226, v225, v225 row_half_mirror row_mask:0xf bank_mask:0xf
	s_nop 1
	v_max_f32_dpp v225, v226, v226 row_mirror row_mask:0xf bank_mask:0xf
	ds_swizzle_b32 v226, v225 offset:swizzle(SWAP,16)
	s_waitcnt lgkmcnt(0)
	v_max_f32_e32 v225, v225, v226
	v_sub_f32_e32 v223, v223, v225
	v_sub_f32_e32 v224, v224, v225
	v_mul_f32_e32 v223, 0x3fb8aa3b, v223
	v_mul_f32_e32 v224, 0x3fb8aa3b, v224
	v_exp_f32_e32 v227, v223
	v_exp_f32_e32 v228, v224
	s_nop 0
	v_add_f32_e32 v229, v227, v228
	s_nop 1
	v_add_f32_dpp v226, v229, v229 quad_perm:[1,0,3,2] row_mask:0xf bank_mask:0xf
	s_nop 1
	v_add_f32_dpp v229, v226, v226 quad_perm:[2,3,0,1] row_mask:0xf bank_mask:0xf
	s_nop 1
	v_add_f32_dpp v226, v229, v229 row_half_mirror row_mask:0xf bank_mask:0xf
	s_nop 1
	v_add_f32_dpp v229, v226, v226 row_mirror row_mask:0xf bank_mask:0xf
	ds_swizzle_b32 v226, v229 offset:swizzle(SWAP,16)
	s_waitcnt lgkmcnt(0)
	v_add_f32_e32 v229, v229, v226
	v_rcp_f32_e32 v234, v229
	s_nop 0
	v_mul_f32_e32 v227, v227, v234
	v_mul_f32_e32 v228, v228, v234
	ds_write_b32 v217, v227
	ds_write_b32 v217, v228 offset:128
	s_waitcnt lgkmcnt(0)
	s_barrier
	ds_read_b128 v[102:105], v218 offset:0
	ds_read_b128 v[106:109], v218 offset:16
	ds_read_b128 v[110:113], v218 offset:32
	ds_read_b128 v[114:117], v218 offset:48
	ds_read_b128 v[118:121], v218 offset:64
	ds_read_b128 v[122:125], v218 offset:80
	ds_read_b128 v[126:129], v218 offset:96
	ds_read_b128 v[130:133], v218 offset:112
	ds_read_b128 v[134:137], v218 offset:128
	ds_read_b128 v[138:141], v218 offset:144
	ds_read_b128 v[142:145], v218 offset:160
	ds_read_b128 v[146:149], v218 offset:176
	ds_read_b128 v[150:153], v218 offset:192
	v_mov_b32_e32 v154, 0
	v_mov_b32_e32 v155, 0
	v_mov_b32_e32 v156, 0
	v_mov_b32_e32 v157, 0
	s_waitcnt vmcnt(0) lgkmcnt(0)
	v_fma_mix_f32 v154, v174, v102, v154 op_sel_hi:[1,0,0]
	v_fma_mix_f32 v155, v174, v102, v155 op_sel:[1,0,0] op_sel_hi:[1,0,0]
	v_fma_mix_f32 v156, v175, v102, v156 op_sel_hi:[1,0,0]
	v_fma_mix_f32 v157, v175, v102, v157 op_sel:[1,0,0] op_sel_hi:[1,0,0]
	v_fma_mix_f32 v154, v176, v103, v154 op_sel_hi:[1,0,0]
	v_fma_mix_f32 v155, v176, v103, v155 op_sel:[1,0,0] op_sel_hi:[1,0,0]
	v_fma_mix_f32 v156, v177, v103, v156 op_sel_hi:[1,0,0]
	v_fma_mix_f32 v157, v177, v103, v157 op_sel:[1,0,0] op_sel_hi:[1,0,0]
	v_fma_mix_f32 v154, v178, v104, v154 op_sel_hi:[1,0,0]
	v_fma_mix_f32 v155, v178, v104, v155 op_sel:[1,0,0] op_sel_hi:[1,0,0]
	v_fma_mix_f32 v156, v179, v104, v156 op_sel_hi:[1,0,0]
	v_fma_mix_f32 v157, v179, v104, v157 op_sel:[1,0,0] op_sel_hi:[1,0,0]
	v_fma_mix_f32 v154, v180, v105, v154 op_sel_hi:[1,0,0]
	v_fma_mix_f32 v155, v180, v105, v155 op_sel:[1,0,0] op_sel_hi:[1,0,0]
	v_fma_mix_f32 v156, v181, v105, v156 op_sel_hi:[1,0,0]
	v_fma_mix_f32 v157, v181, v105, v157 op_sel:[1,0,0] op_sel_hi:[1,0,0]
	v_fma_mix_f32 v154, v182, v106, v154 op_sel_hi:[1,0,0]
	v_fma_mix_f32 v155, v182, v106, v155 op_sel:[1,0,0] op_sel_hi:[1,0,0]
	v_fma_mix_f32 v156, v183, v106, v156 op_sel_hi:[1,0,0]
	v_fma_mix_f32 v157, v183, v106, v157 op_sel:[1,0,0] op_sel_hi:[1,0,0]
	v_fma_mix_f32 v154, v184, v107, v154 op_sel_hi:[1,0,0]
	v_fma_mix_f32 v155, v184, v107, v155 op_sel:[1,0,0] op_sel_hi:[1,0,0]
	v_fma_mix_f32 v156, v185, v107, v156 op_sel_hi:[1,0,0]
	v_fma_mix_f32 v157, v185, v107, v157 op_sel:[1,0,0] op_sel_hi:[1,0,0]
	v_fma_mix_f32 v154, v237, v108, v154 op_sel_hi:[1,0,0]
	v_fma_mix_f32 v155, v237, v108, v155 op_sel:[1,0,0] op_sel_hi:[1,0,0]
	v_fma_mix_f32 v156, v238, v108, v156 op_sel_hi:[1,0,0]
	v_fma_mix_f32 v157, v238, v108, v157 op_sel:[1,0,0] op_sel_hi:[1,0,0]
	v_fma_mix_f32 v154, v239, v109, v154 op_sel_hi:[1,0,0]
	v_fma_mix_f32 v155, v239, v109, v155 op_sel:[1,0,0] op_sel_hi:[1,0,0]
	v_fma_mix_f32 v156, v240, v109, v156 op_sel_hi:[1,0,0]
	v_fma_mix_f32 v157, v240, v109, v157 op_sel:[1,0,0] op_sel_hi:[1,0,0]
	v_fma_mix_f32 v154, v241, v110, v154 op_sel_hi:[1,0,0]
	v_fma_mix_f32 v155, v241, v110, v155 op_sel:[1,0,0] op_sel_hi:[1,0,0]
	v_fma_mix_f32 v156, v242, v110, v156 op_sel_hi:[1,0,0]
	v_fma_mix_f32 v157, v242, v110, v157 op_sel:[1,0,0] op_sel_hi:[1,0,0]
	v_fma_mix_f32 v154, v243, v111, v154 op_sel_hi:[1,0,0]
	v_fma_mix_f32 v155, v243, v111, v155 op_sel:[1,0,0] op_sel_hi:[1,0,0]
	v_fma_mix_f32 v156, v244, v111, v156 op_sel_hi:[1,0,0]
	v_fma_mix_f32 v157, v244, v111, v157 op_sel:[1,0,0] op_sel_hi:[1,0,0]
	v_fma_mix_f32 v154, v245, v112, v154 op_sel_hi:[1,0,0]
	v_fma_mix_f32 v155, v245, v112, v155 op_sel:[1,0,0] op_sel_hi:[1,0,0]
	v_fma_mix_f32 v156, v187, v112, v156 op_sel_hi:[1,0,0]
	v_fma_mix_f32 v157, v187, v112, v157 op_sel:[1,0,0] op_sel_hi:[1,0,0]
	v_fma_mix_f32 v154, v188, v113, v154 op_sel_hi:[1,0,0]
	v_fma_mix_f32 v155, v188, v113, v155 op_sel:[1,0,0] op_sel_hi:[1,0,0]
	v_fma_mix_f32 v156, v202, v113, v156 op_sel_hi:[1,0,0]
	v_fma_mix_f32 v157, v202, v113, v157 op_sel:[1,0,0] op_sel_hi:[1,0,0]
	v_fma_mix_f32 v154, v203, v114, v154 op_sel_hi:[1,0,0]
	v_fma_mix_f32 v155, v203, v114, v155 op_sel:[1,0,0] op_sel_hi:[1,0,0]
	v_fma_mix_f32 v156, v204, v114, v156 op_sel_hi:[1,0,0]
	v_fma_mix_f32 v157, v204, v114, v157 op_sel:[1,0,0] op_sel_hi:[1,0,0]
	v_fma_mix_f32 v154, v205, v115, v154 op_sel_hi:[1,0,0]
	v_fma_mix_f32 v155, v205, v115, v155 op_sel:[1,0,0] op_sel_hi:[1,0,0]
	v_fma_mix_f32 v156, v207, v115, v156 op_sel_hi:[1,0,0]
	v_fma_mix_f32 v157, v207, v115, v157 op_sel:[1,0,0] op_sel_hi:[1,0,0]
	v_fma_mix_f32 v154, v30, v116, v154 op_sel_hi:[1,0,0]
	v_fma_mix_f32 v155, v30, v116, v155 op_sel:[1,0,0] op_sel_hi:[1,0,0]
	v_fma_mix_f32 v156, v31, v116, v156 op_sel_hi:[1,0,0]
	v_fma_mix_f32 v157, v31, v116, v157 op_sel:[1,0,0] op_sel_hi:[1,0,0]
	v_fma_mix_f32 v154, v32, v117, v154 op_sel_hi:[1,0,0]
	v_fma_mix_f32 v155, v32, v117, v155 op_sel:[1,0,0] op_sel_hi:[1,0,0]
	v_fma_mix_f32 v156, v33, v117, v156 op_sel_hi:[1,0,0]
	v_fma_mix_f32 v157, v33, v117, v157 op_sel:[1,0,0] op_sel_hi:[1,0,0]
	v_fma_mix_f32 v154, v34, v118, v154 op_sel_hi:[1,0,0]
	v_fma_mix_f32 v155, v34, v118, v155 op_sel:[1,0,0] op_sel_hi:[1,0,0]
	v_fma_mix_f32 v156, v35, v118, v156 op_sel_hi:[1,0,0]
	v_fma_mix_f32 v157, v35, v118, v157 op_sel:[1,0,0] op_sel_hi:[1,0,0]
	v_fma_mix_f32 v154, v36, v119, v154 op_sel_hi:[1,0,0]
	v_fma_mix_f32 v155, v36, v119, v155 op_sel:[1,0,0] op_sel_hi:[1,0,0]
	v_fma_mix_f32 v156, v37, v119, v156 op_sel_hi:[1,0,0]
	v_fma_mix_f32 v157, v37, v119, v157 op_sel:[1,0,0] op_sel_hi:[1,0,0]
	v_fma_mix_f32 v154, v38, v120, v154 op_sel_hi:[1,0,0]
	v_fma_mix_f32 v155, v38, v120, v155 op_sel:[1,0,0] op_sel_hi:[1,0,0]
	v_fma_mix_f32 v156, v39, v120, v156 op_sel_hi:[1,0,0]
	v_fma_mix_f32 v157, v39, v120, v157 op_sel:[1,0,0] op_sel_hi:[1,0,0]
	v_fma_mix_f32 v154, v40, v121, v154 op_sel_hi:[1,0,0]
	v_fma_mix_f32 v155, v40, v121, v155 op_sel:[1,0,0] op_sel_hi:[1,0,0]
	v_fma_mix_f32 v156, v41, v121, v156 op_sel_hi:[1,0,0]
	v_fma_mix_f32 v157, v41, v121, v157 op_sel:[1,0,0] op_sel_hi:[1,0,0]
	v_fma_mix_f32 v154, v42, v122, v154 op_sel_hi:[1,0,0]
	v_fma_mix_f32 v155, v42, v122, v155 op_sel:[1,0,0] op_sel_hi:[1,0,0]
	v_fma_mix_f32 v156, v43, v122, v156 op_sel_hi:[1,0,0]
	v_fma_mix_f32 v157, v43, v122, v157 op_sel:[1,0,0] op_sel_hi:[1,0,0]
	v_fma_mix_f32 v154, v44, v123, v154 op_sel_hi:[1,0,0]
	v_fma_mix_f32 v155, v44, v123, v155 op_sel:[1,0,0] op_sel_hi:[1,0,0]
	v_fma_mix_f32 v156, v45, v123, v156 op_sel_hi:[1,0,0]
	v_fma_mix_f32 v157, v45, v123, v157 op_sel:[1,0,0] op_sel_hi:[1,0,0]
	v_fma_mix_f32 v154, v46, v124, v154 op_sel_hi:[1,0,0]
	v_fma_mix_f32 v155, v46, v124, v155 op_sel:[1,0,0] op_sel_hi:[1,0,0]
	v_fma_mix_f32 v156, v47, v124, v156 op_sel_hi:[1,0,0]
	v_fma_mix_f32 v157, v47, v124, v157 op_sel:[1,0,0] op_sel_hi:[1,0,0]
	v_fma_mix_f32 v154, v48, v125, v154 op_sel_hi:[1,0,0]
	v_fma_mix_f32 v155, v48, v125, v155 op_sel:[1,0,0] op_sel_hi:[1,0,0]
	v_fma_mix_f32 v156, v49, v125, v156 op_sel_hi:[1,0,0]
	v_fma_mix_f32 v157, v49, v125, v157 op_sel:[1,0,0] op_sel_hi:[1,0,0]
	v_fma_mix_f32 v154, v50, v126, v154 op_sel_hi:[1,0,0]
	v_fma_mix_f32 v155, v50, v126, v155 op_sel:[1,0,0] op_sel_hi:[1,0,0]
	v_fma_mix_f32 v156, v51, v126, v156 op_sel_hi:[1,0,0]
	v_fma_mix_f32 v157, v51, v126, v157 op_sel:[1,0,0] op_sel_hi:[1,0,0]
	v_fma_mix_f32 v154, v52, v127, v154 op_sel_hi:[1,0,0]
	v_fma_mix_f32 v155, v52, v127, v155 op_sel:[1,0,0] op_sel_hi:[1,0,0]
	v_fma_mix_f32 v156, v53, v127, v156 op_sel_hi:[1,0,0]
	v_fma_mix_f32 v157, v53, v127, v157 op_sel:[1,0,0] op_sel_hi:[1,0,0]
	v_fma_mix_f32 v154, v54, v128, v154 op_sel_hi:[1,0,0]
	v_fma_mix_f32 v155, v54, v128, v155 op_sel:[1,0,0] op_sel_hi:[1,0,0]
	v_fma_mix_f32 v156, v55, v128, v156 op_sel_hi:[1,0,0]
	v_fma_mix_f32 v157, v55, v128, v157 op_sel:[1,0,0] op_sel_hi:[1,0,0]
	v_fma_mix_f32 v154, v56, v129, v154 op_sel_hi:[1,0,0]
	v_fma_mix_f32 v155, v56, v129, v155 op_sel:[1,0,0] op_sel_hi:[1,0,0]
	v_fma_mix_f32 v156, v57, v129, v156 op_sel_hi:[1,0,0]
	v_fma_mix_f32 v157, v57, v129, v157 op_sel:[1,0,0] op_sel_hi:[1,0,0]
	v_fma_mix_f32 v154, v58, v130, v154 op_sel_hi:[1,0,0]
	v_fma_mix_f32 v155, v58, v130, v155 op_sel:[1,0,0] op_sel_hi:[1,0,0]
	v_fma_mix_f32 v156, v59, v130, v156 op_sel_hi:[1,0,0]
	v_fma_mix_f32 v157, v59, v130, v157 op_sel:[1,0,0] op_sel_hi:[1,0,0]
	v_fma_mix_f32 v154, v60, v131, v154 op_sel_hi:[1,0,0]
	v_fma_mix_f32 v155, v60, v131, v155 op_sel:[1,0,0] op_sel_hi:[1,0,0]
	v_fma_mix_f32 v156, v61, v131, v156 op_sel_hi:[1,0,0]
	v_fma_mix_f32 v157, v61, v131, v157 op_sel:[1,0,0] op_sel_hi:[1,0,0]
	v_fma_mix_f32 v154, v62, v132, v154 op_sel_hi:[1,0,0]
	v_fma_mix_f32 v155, v62, v132, v155 op_sel:[1,0,0] op_sel_hi:[1,0,0]
	v_fma_mix_f32 v156, v63, v132, v156 op_sel_hi:[1,0,0]
	v_fma_mix_f32 v157, v63, v132, v157 op_sel:[1,0,0] op_sel_hi:[1,0,0]
	v_fma_mix_f32 v154, v64, v133, v154 op_sel_hi:[1,0,0]
	v_fma_mix_f32 v155, v64, v133, v155 op_sel:[1,0,0] op_sel_hi:[1,0,0]
	v_fma_mix_f32 v156, v65, v133, v156 op_sel_hi:[1,0,0]
	v_fma_mix_f32 v157, v65, v133, v157 op_sel:[1,0,0] op_sel_hi:[1,0,0]
	v_fma_mix_f32 v154, v66, v134, v154 op_sel_hi:[1,0,0]
	v_fma_mix_f32 v155, v66, v134, v155 op_sel:[1,0,0] op_sel_hi:[1,0,0]
	v_fma_mix_f32 v156, v67, v134, v156 op_sel_hi:[1,0,0]
	v_fma_mix_f32 v157, v67, v134, v157 op_sel:[1,0,0] op_sel_hi:[1,0,0]
	v_fma_mix_f32 v154, v68, v135, v154 op_sel_hi:[1,0,0]
	v_fma_mix_f32 v155, v68, v135, v155 op_sel:[1,0,0] op_sel_hi:[1,0,0]
	v_fma_mix_f32 v156, v69, v135, v156 op_sel_hi:[1,0,0]
	v_fma_mix_f32 v157, v69, v135, v157 op_sel:[1,0,0] op_sel_hi:[1,0,0]
	v_fma_mix_f32 v154, v70, v136, v154 op_sel_hi:[1,0,0]
	v_fma_mix_f32 v155, v70, v136, v155 op_sel:[1,0,0] op_sel_hi:[1,0,0]
	v_fma_mix_f32 v156, v71, v136, v156 op_sel_hi:[1,0,0]
	v_fma_mix_f32 v157, v71, v136, v157 op_sel:[1,0,0] op_sel_hi:[1,0,0]
	v_fma_mix_f32 v154, v72, v137, v154 op_sel_hi:[1,0,0]
	v_fma_mix_f32 v155, v72, v137, v155 op_sel:[1,0,0] op_sel_hi:[1,0,0]
	v_fma_mix_f32 v156, v73, v137, v156 op_sel_hi:[1,0,0]
	v_fma_mix_f32 v157, v73, v137, v157 op_sel:[1,0,0] op_sel_hi:[1,0,0]
	v_fma_mix_f32 v154, v74, v138, v154 op_sel_hi:[1,0,0]
	v_fma_mix_f32 v155, v74, v138, v155 op_sel:[1,0,0] op_sel_hi:[1,0,0]
	v_fma_mix_f32 v156, v75, v138, v156 op_sel_hi:[1,0,0]
	v_fma_mix_f32 v157, v75, v138, v157 op_sel:[1,0,0] op_sel_hi:[1,0,0]
	v_fma_mix_f32 v154, v76, v139, v154 op_sel_hi:[1,0,0]
	v_fma_mix_f32 v155, v76, v139, v155 op_sel:[1,0,0] op_sel_hi:[1,0,0]
	v_fma_mix_f32 v156, v77, v139, v156 op_sel_hi:[1,0,0]
	v_fma_mix_f32 v157, v77, v139, v157 op_sel:[1,0,0] op_sel_hi:[1,0,0]
	v_fma_mix_f32 v154, v78, v140, v154 op_sel_hi:[1,0,0]
	v_fma_mix_f32 v155, v78, v140, v155 op_sel:[1,0,0] op_sel_hi:[1,0,0]
	v_fma_mix_f32 v156, v79, v140, v156 op_sel_hi:[1,0,0]
	v_fma_mix_f32 v157, v79, v140, v157 op_sel:[1,0,0] op_sel_hi:[1,0,0]
	v_fma_mix_f32 v154, v80, v141, v154 op_sel_hi:[1,0,0]
	v_fma_mix_f32 v155, v80, v141, v155 op_sel:[1,0,0] op_sel_hi:[1,0,0]
	v_fma_mix_f32 v156, v81, v141, v156 op_sel_hi:[1,0,0]
	v_fma_mix_f32 v157, v81, v141, v157 op_sel:[1,0,0] op_sel_hi:[1,0,0]
	v_fma_mix_f32 v154, v82, v142, v154 op_sel_hi:[1,0,0]
	v_fma_mix_f32 v155, v82, v142, v155 op_sel:[1,0,0] op_sel_hi:[1,0,0]
	v_fma_mix_f32 v156, v83, v142, v156 op_sel_hi:[1,0,0]
	v_fma_mix_f32 v157, v83, v142, v157 op_sel:[1,0,0] op_sel_hi:[1,0,0]
	v_fma_mix_f32 v154, v84, v143, v154 op_sel_hi:[1,0,0]
	v_fma_mix_f32 v155, v84, v143, v155 op_sel:[1,0,0] op_sel_hi:[1,0,0]
	v_fma_mix_f32 v156, v85, v143, v156 op_sel_hi:[1,0,0]
	v_fma_mix_f32 v157, v85, v143, v157 op_sel:[1,0,0] op_sel_hi:[1,0,0]
	v_fma_mix_f32 v154, v86, v144, v154 op_sel_hi:[1,0,0]
	v_fma_mix_f32 v155, v86, v144, v155 op_sel:[1,0,0] op_sel_hi:[1,0,0]
	v_fma_mix_f32 v156, v87, v144, v156 op_sel_hi:[1,0,0]
	v_fma_mix_f32 v157, v87, v144, v157 op_sel:[1,0,0] op_sel_hi:[1,0,0]
	v_fma_mix_f32 v154, v88, v145, v154 op_sel_hi:[1,0,0]
	v_fma_mix_f32 v155, v88, v145, v155 op_sel:[1,0,0] op_sel_hi:[1,0,0]
	v_fma_mix_f32 v156, v89, v145, v156 op_sel_hi:[1,0,0]
	v_fma_mix_f32 v157, v89, v145, v157 op_sel:[1,0,0] op_sel_hi:[1,0,0]
	v_fma_mix_f32 v154, v90, v146, v154 op_sel_hi:[1,0,0]
	v_fma_mix_f32 v155, v90, v146, v155 op_sel:[1,0,0] op_sel_hi:[1,0,0]
	v_fma_mix_f32 v156, v91, v146, v156 op_sel_hi:[1,0,0]
	v_fma_mix_f32 v157, v91, v146, v157 op_sel:[1,0,0] op_sel_hi:[1,0,0]
	v_fma_mix_f32 v154, v92, v147, v154 op_sel_hi:[1,0,0]
	v_fma_mix_f32 v155, v92, v147, v155 op_sel:[1,0,0] op_sel_hi:[1,0,0]
	v_fma_mix_f32 v156, v93, v147, v156 op_sel_hi:[1,0,0]
	v_fma_mix_f32 v157, v93, v147, v157 op_sel:[1,0,0] op_sel_hi:[1,0,0]
	v_fma_mix_f32 v154, v94, v148, v154 op_sel_hi:[1,0,0]
	v_fma_mix_f32 v155, v94, v148, v155 op_sel:[1,0,0] op_sel_hi:[1,0,0]
	v_fma_mix_f32 v156, v95, v148, v156 op_sel_hi:[1,0,0]
	v_fma_mix_f32 v157, v95, v148, v157 op_sel:[1,0,0] op_sel_hi:[1,0,0]
	v_fma_mix_f32 v154, v96, v149, v154 op_sel_hi:[1,0,0]
	v_fma_mix_f32 v155, v96, v149, v155 op_sel:[1,0,0] op_sel_hi:[1,0,0]
	v_fma_mix_f32 v156, v97, v149, v156 op_sel_hi:[1,0,0]
	v_fma_mix_f32 v157, v97, v149, v157 op_sel:[1,0,0] op_sel_hi:[1,0,0]
	v_fma_mix_f32 v154, v98, v150, v154 op_sel_hi:[1,0,0]
	v_fma_mix_f32 v155, v98, v150, v155 op_sel:[1,0,0] op_sel_hi:[1,0,0]
	v_fma_mix_f32 v156, v99, v150, v156 op_sel_hi:[1,0,0]
	v_fma_mix_f32 v157, v99, v150, v157 op_sel:[1,0,0] op_sel_hi:[1,0,0]
	v_fma_mix_f32 v154, v100, v151, v154 op_sel_hi:[1,0,0]
	v_fma_mix_f32 v155, v100, v151, v155 op_sel:[1,0,0] op_sel_hi:[1,0,0]
	v_fma_mix_f32 v156, v101, v151, v156 op_sel_hi:[1,0,0]
	v_fma_mix_f32 v157, v101, v151, v157 op_sel:[1,0,0] op_sel_hi:[1,0,0]
	global_store_dwordx4 v222, v[154:157], s[8:9]
	s_endpgm
